# v60 + one static s_setprio 1 for waves 4-7 at kernel entry, all 168 per-segment s_setprio flips in the GEMM K-loops removed
# baseline (speedup 1.0000x reference)
_Z8mega_fwd5FArgs:
	v_readfirstlane_b32 s98, v0
	s_nop 0
	s_bitcmp1_b32 s98, 8
	s_cbranch_scc0 .Lprio_skip
	s_setprio 1
.Lprio_skip:
	v_lshl_add_u32 v1, v0, 2, 0
	v_add_u32_e32 v1, 0x20000, v1
	v_mov_b32_e32 v2, 0
	s_mov_b32 s96, s2
	s_mov_b64 s[76:77], s[0:1]
	ds_write2st64_b32 v1, v2, v2 offset1:8
	ds_write2st64_b32 v1, v2, v2 offset0:16 offset1:24
	v_or_b32_e32 v1, 0x800, v0
	s_mov_b64 s[2:3], -1
	s_and_saveexec_b64 s[4:5], s[2:3]
	v_lshl_add_u32 v3, v1, 2, 0
	v_add_u32_e32 v3, 0x20000, v3
	ds_write_b32 v3, v2
	s_or_b64 exec, exec, s[4:5]
	s_and_saveexec_b64 s[4:5], s[2:3]
	s_add_i32 s0, 0, 0x20000
	v_lshl_add_u32 v1, v1, 2, s0
	v_mov_b32_e32 v2, 0
	ds_write_b32 v1, v2 offset:2048
	s_or_b64 exec, exec, s[4:5]
	v_or_b32_e32 v1, 0xc00, v0
	v_cmp_gt_u32_e64 s[2:3], 7, 6
	v_cmp_gt_u32_e64 s[0:1], 7, 5
	s_and_saveexec_b64 s[4:5], s[0:1]
	v_lshl_add_u32 v2, v1, 2, 0
	v_add_u32_e32 v2, 0x20000, v2
	v_mov_b32_e32 v3, 0
	ds_write_b32 v2, v3
	s_or_b64 exec, exec, s[4:5]
	s_and_saveexec_b64 s[4:5], s[2:3]
	s_add_i32 s0, 0, 0x20000
	v_lshl_add_u32 v1, v1, 2, s0
	v_mov_b32_e32 v2, 0
	ds_write_b32 v1, v2 offset:2048
	s_or_b64 exec, exec, s[4:5]
	s_load_dwordx2 s[38:39], s[76:77], 0xb0
	s_waitcnt lgkmcnt(0)
	s_barrier
	s_getreg_b32 s0, hwreg(HW_REG_XCC_ID, 0, 4)
	v_cmp_eq_u32_e64 s[68:69], 0, v0
	v_mov_b64_e32 v[106:107], s[38:39]
	s_and_saveexec_b64 s[2:3], s[68:69]
	s_cbranch_execz .LBB6_12
	s_mov_b64 s[6:7], exec
	v_mbcnt_lo_u32_b32 v1, s6, 0
	v_mbcnt_hi_u32_b32 v1, s7, v1
	v_cmp_eq_u32_e32 vcc, 0, v1
	v_mov_b64_e32 v[106:107], s[38:39]
	s_and_saveexec_b64 s[4:5], vcc
	s_cbranch_execz .LBB6_11
	s_lshl_b32 s0, s0, 8
	s_and_b32 s0, s0, 0xf00
	s_add_u32 s0, s38, s0
	s_addc_u32 s1, s39, 0
	s_bcnt1_i32_b64 s6, s[6:7]
	v_mov_b32_e32 v1, 0x4000
	v_mov_b32_e32 v2, s6
	global_atomic_add v1, v2, s[0:1] offset:1024
	s_load_dwordx2 s[0:1], s[76:77], 0xb0
	s_waitcnt lgkmcnt(0)
	v_mov_b64_e32 v[106:107], s[0:1]

.LBB6_497:
	s_add_u32 s13, s8, 0xfff80080
	s_addc_u32 s33, s9, -1
	s_add_i32 s45, 0, 0x10000
	s_cmp_eq_u32 s12, 28
	s_cselect_b32 vcc_hi, s93, s33
	s_cselect_b32 vcc_lo, s92, s13
	s_waitcnt lgkmcnt(0)
	v_add_u32_e32 v2, s45, v175
	s_cselect_b32 s81, s91, s7
	s_cselect_b32 s80, s90, s0
	s_add_i32 s13, 0, 0x14000
	ds_read_b128 v[132:135], v2
	ds_read_b128 v[136:139], v2 offset:1024
	ds_read_b128 v[140:143], v2 offset:2048
	ds_read_b128 v[144:147], v2 offset:3072
	v_add_u32_e32 v2, s13, v175
	ds_read_b128 v[148:151], v2
	ds_read_b128 v[152:155], v2 offset:1024
	ds_read_b128 v[156:159], v2 offset:2048
	ds_read_b128 v[160:163], v2 offset:3072
	v_lshl_add_u64 v[210:211], s[8:9], 0, v[190:191]
	s_add_i32 m0, s63, 0xc000
	ds_read_b128 v[192:195], v200
	ds_read_b128 v[196:199], v200 offset:1024
	ds_read_b128 v[202:205], v200 offset:2048
	ds_read_b128 v[206:209], v200 offset:3072
	ds_read_b128 v[228:231], v200 offset:4096
	ds_read_b128 v[232:235], v200 offset:5120
	ds_read_b128 v[236:239], v200 offset:6144
	ds_read_b128 v[240:243], v200 offset:7168
	global_load_lds_dwordx4 v[210:211], off
	v_lshl_add_u64 v[210:211], s[8:9], 0, v[188:189]
	s_add_i32 m0, s63, 0xe000
	s_nop 0
	global_load_lds_dwordx4 v[210:211], off
	s_waitcnt vmcnt(8)
	s_waitcnt lgkmcnt(0)
	s_barrier
	s_waitcnt lgkmcnt(0)
	v_mfma_f32_16x16x32_bf16 v[128:131], v[132:135], v[192:195], v[128:131]
	v_mfma_f32_16x16x32_bf16 v[124:127], v[140:143], v[192:195], v[124:127]
	v_mfma_f32_16x16x32_bf16 v[120:123], v[132:135], v[202:205], v[120:123]
	v_mfma_f32_16x16x32_bf16 v[116:119], v[140:143], v[202:205], v[116:119]
	v_mfma_f32_16x16x32_bf16 v[104:107], v[132:135], v[228:231], v[104:107]
	v_mfma_f32_16x16x32_bf16 v[100:103], v[140:143], v[228:231], v[100:103]
	v_mfma_f32_16x16x32_bf16 v[88:91], v[132:135], v[236:239], v[88:91]
	v_mfma_f32_16x16x32_bf16 v[84:87], v[140:143], v[236:239], v[84:87]
	v_mfma_f32_16x16x32_bf16 v[128:131], v[136:139], v[196:199], v[128:131]
	v_mfma_f32_16x16x32_bf16 v[124:127], v[144:147], v[196:199], v[124:127]
	v_mfma_f32_16x16x32_bf16 v[120:123], v[136:139], v[206:209], v[120:123]
	v_mfma_f32_16x16x32_bf16 v[116:119], v[144:147], v[206:209], v[116:119]
	v_mfma_f32_16x16x32_bf16 v[104:107], v[136:139], v[232:235], v[104:107]
	v_mfma_f32_16x16x32_bf16 v[100:103], v[144:147], v[232:235], v[100:103]
	v_mfma_f32_16x16x32_bf16 v[88:91], v[136:139], v[240:243], v[88:91]
	v_mfma_f32_16x16x32_bf16 v[84:87], v[144:147], v[240:243], v[84:87]
	v_mfma_f32_16x16x32_bf16 v[112:115], v[148:151], v[192:195], v[112:115]
	v_mfma_f32_16x16x32_bf16 v[108:111], v[156:159], v[192:195], v[108:111]
	v_mfma_f32_16x16x32_bf16 v[96:99], v[148:151], v[202:205], v[96:99]
	v_mfma_f32_16x16x32_bf16 v[92:95], v[156:159], v[202:205], v[92:95]
	v_mfma_f32_16x16x32_bf16 v[80:83], v[148:151], v[228:231], v[80:83]
	v_mfma_f32_16x16x32_bf16 v[76:79], v[156:159], v[228:231], v[76:79]
	v_mfma_f32_16x16x32_bf16 v[72:75], v[148:151], v[236:239], v[72:75]
	v_mfma_f32_16x16x32_bf16 v[68:71], v[156:159], v[236:239], v[68:71]
	v_mfma_f32_16x16x32_bf16 v[112:115], v[152:155], v[196:199], v[112:115]
	v_mfma_f32_16x16x32_bf16 v[108:111], v[160:163], v[196:199], v[108:111]
	v_mfma_f32_16x16x32_bf16 v[96:99], v[152:155], v[206:209], v[96:99]
	v_mfma_f32_16x16x32_bf16 v[92:95], v[160:163], v[206:209], v[92:95]
	v_mfma_f32_16x16x32_bf16 v[80:83], v[152:155], v[232:235], v[80:83]
	v_mfma_f32_16x16x32_bf16 v[76:79], v[160:163], v[232:235], v[76:79]
	v_mfma_f32_16x16x32_bf16 v[72:75], v[152:155], v[240:243], v[72:75]
	v_mfma_f32_16x16x32_bf16 v[68:71], v[160:163], v[240:243], v[68:71]
	s_barrier
	s_add_i32 s33, s45, s62
	v_lshl_add_u64 v[210:211], s[80:81], 0, v[166:167]
	s_mov_b32 m0, s33
	ds_read_b128 v[192:195], v200 offset:16384
	ds_read_b128 v[196:199], v200 offset:17408
	ds_read_b128 v[202:205], v200 offset:18432
	ds_read_b128 v[206:209], v200 offset:19456
	ds_read_b128 v[228:231], v200 offset:20480
	ds_read_b128 v[232:235], v200 offset:21504
	ds_read_b128 v[236:239], v200 offset:22528
	ds_read_b128 v[240:243], v200 offset:23552
	global_load_lds_dwordx4 v[210:211], off
	s_add_i32 m0, s33, 0x2000
	s_add_u32 s70, s80, 0x80000
	v_lshl_add_u64 v[216:217], s[80:81], 0, v[170:171]
	s_addc_u32 s71, s81, 0
	s_add_i32 s13, s13, s62
	global_load_lds_dwordx4 v[216:217], off
	v_lshl_add_u64 v[218:219], s[70:71], 0, v[166:167]
	s_mov_b32 m0, s13
	v_lshl_add_u64 v[220:221], vcc, 0, v[168:169]
	global_load_lds_dwordx4 v[218:219], off
	v_lshl_add_u64 v[218:219], s[70:71], 0, v[170:171]
	s_add_i32 m0, s13, 0x2000
	s_nop 0
	global_load_lds_dwordx4 v[218:219], off
	v_lshl_add_u64 v[218:219], vcc, 0, v[164:165]
	s_mov_b32 m0, s63
	s_nop 0
	global_load_lds_dwordx4 v[218:219], off
	s_mov_b32 m0, s68
	s_nop 0
	global_load_lds_dwordx4 v[220:221], off
	s_waitcnt vmcnt(8)
	s_waitcnt lgkmcnt(0)
	s_barrier
	s_waitcnt lgkmcnt(0)
	v_mfma_f32_16x16x32_bf16 v[64:67], v[132:135], v[192:195], v[64:67]
	v_mfma_f32_16x16x32_bf16 v[60:63], v[140:143], v[192:195], v[60:63]
	v_mfma_f32_16x16x32_bf16 v[56:59], v[132:135], v[202:205], v[56:59]
	v_mfma_f32_16x16x32_bf16 v[52:55], v[140:143], v[202:205], v[52:55]
	v_mfma_f32_16x16x32_bf16 v[40:43], v[132:135], v[228:231], v[40:43]
	v_mfma_f32_16x16x32_bf16 v[36:39], v[140:143], v[228:231], v[36:39]
	v_mfma_f32_16x16x32_bf16 v[24:27], v[132:135], v[236:239], v[24:27]
	v_mfma_f32_16x16x32_bf16 v[20:23], v[140:143], v[236:239], v[20:23]
	v_mfma_f32_16x16x32_bf16 v[64:67], v[136:139], v[196:199], v[64:67]
	v_mfma_f32_16x16x32_bf16 v[60:63], v[144:147], v[196:199], v[60:63]
	v_mfma_f32_16x16x32_bf16 v[56:59], v[136:139], v[206:209], v[56:59]
	v_mfma_f32_16x16x32_bf16 v[52:55], v[144:147], v[206:209], v[52:55]
	v_mfma_f32_16x16x32_bf16 v[40:43], v[136:139], v[232:235], v[40:43]
	v_mfma_f32_16x16x32_bf16 v[36:39], v[144:147], v[232:235], v[36:39]
	v_mfma_f32_16x16x32_bf16 v[24:27], v[136:139], v[240:243], v[24:27]
	v_mfma_f32_16x16x32_bf16 v[20:23], v[144:147], v[240:243], v[20:23]
	v_mfma_f32_16x16x32_bf16 v[48:51], v[148:151], v[192:195], v[48:51]
	v_mfma_f32_16x16x32_bf16 v[44:47], v[156:159], v[192:195], v[44:47]
	v_mfma_f32_16x16x32_bf16 v[32:35], v[148:151], v[202:205], v[32:35]
	v_mfma_f32_16x16x32_bf16 v[28:31], v[156:159], v[202:205], v[28:31]
	v_mfma_f32_16x16x32_bf16 v[16:19], v[148:151], v[228:231], v[16:19]
	v_mfma_f32_16x16x32_bf16 v[12:15], v[156:159], v[228:231], v[12:15]
	v_mfma_f32_16x16x32_bf16 v[8:11], v[148:151], v[236:239], v[8:11]
	v_mfma_f32_16x16x32_bf16 v[4:7], v[156:159], v[236:239], v[4:7]
	v_mfma_f32_16x16x32_bf16 v[48:51], v[152:155], v[196:199], v[48:51]
	v_mfma_f32_16x16x32_bf16 v[44:47], v[160:163], v[196:199], v[44:47]
	v_mfma_f32_16x16x32_bf16 v[32:35], v[152:155], v[206:209], v[32:35]
	v_mfma_f32_16x16x32_bf16 v[28:31], v[160:163], v[206:209], v[28:31]
	v_mfma_f32_16x16x32_bf16 v[16:19], v[152:155], v[232:235], v[16:19]
	v_mfma_f32_16x16x32_bf16 v[12:15], v[160:163], v[232:235], v[12:15]
	v_mfma_f32_16x16x32_bf16 v[8:11], v[152:155], v[240:243], v[8:11]
	v_mfma_f32_16x16x32_bf16 v[4:7], v[160:163], v[240:243], v[4:7]
	s_barrier
	s_add_i32 s13, 0, 0x18000
	v_add_u32_e32 v2, s13, v175
	s_add_i32 s33, 0, 0x1c000
	ds_read_b128 v[132:135], v2
	ds_read_b128 v[136:139], v2 offset:1024
	ds_read_b128 v[140:143], v2 offset:2048
	ds_read_b128 v[144:147], v2 offset:3072
	v_add_u32_e32 v2, s33, v175
	ds_read_b128 v[148:151], v2
	ds_read_b128 v[152:155], v2 offset:1024
	ds_read_b128 v[156:159], v2 offset:2048
	ds_read_b128 v[160:163], v2 offset:3072
	s_add_u32 s70, vcc_lo, 0x80000
	s_addc_u32 s71, vcc_hi, 0
	s_mov_b32 m0, s26
	v_lshl_add_u64 v[222:223], s[70:71], 0, v[164:165]
	ds_read_b128 v[192:195], v200 offset:32768
	ds_read_b128 v[196:199], v200 offset:33792
	ds_read_b128 v[202:205], v200 offset:34816
	ds_read_b128 v[206:209], v200 offset:35840
	ds_read_b128 v[228:231], v200 offset:36864
	ds_read_b128 v[232:235], v200 offset:37888
	ds_read_b128 v[236:239], v200 offset:38912
	ds_read_b128 v[240:243], v200 offset:39936
	global_load_lds_dwordx4 v[222:223], off
	v_lshl_add_u64 v[222:223], s[70:71], 0, v[168:169]
	s_mov_b32 m0, s27
	s_nop 0
	global_load_lds_dwordx4 v[222:223], off
	s_waitcnt vmcnt(8)
	s_waitcnt lgkmcnt(0)
	s_barrier
	s_waitcnt lgkmcnt(0)
	v_mfma_f32_16x16x32_bf16 v[128:131], v[132:135], v[192:195], v[128:131]
	v_mfma_f32_16x16x32_bf16 v[124:127], v[140:143], v[192:195], v[124:127]
	v_mfma_f32_16x16x32_bf16 v[120:123], v[132:135], v[202:205], v[120:123]
	v_mfma_f32_16x16x32_bf16 v[116:119], v[140:143], v[202:205], v[116:119]
	v_mfma_f32_16x16x32_bf16 v[104:107], v[132:135], v[228:231], v[104:107]
	v_mfma_f32_16x16x32_bf16 v[100:103], v[140:143], v[228:231], v[100:103]
	v_mfma_f32_16x16x32_bf16 v[88:91], v[132:135], v[236:239], v[88:91]
	v_mfma_f32_16x16x32_bf16 v[84:87], v[140:143], v[236:239], v[84:87]
	v_mfma_f32_16x16x32_bf16 v[128:131], v[136:139], v[196:199], v[128:131]
	v_mfma_f32_16x16x32_bf16 v[124:127], v[144:147], v[196:199], v[124:127]
	v_mfma_f32_16x16x32_bf16 v[120:123], v[136:139], v[206:209], v[120:123]
	v_mfma_f32_16x16x32_bf16 v[116:119], v[144:147], v[206:209], v[116:119]
	v_mfma_f32_16x16x32_bf16 v[104:107], v[136:139], v[232:235], v[104:107]
	v_mfma_f32_16x16x32_bf16 v[100:103], v[144:147], v[232:235], v[100:103]
	v_mfma_f32_16x16x32_bf16 v[88:91], v[136:139], v[240:243], v[88:91]
	v_mfma_f32_16x16x32_bf16 v[84:87], v[144:147], v[240:243], v[84:87]
	v_mfma_f32_16x16x32_bf16 v[112:115], v[148:151], v[192:195], v[112:115]
	v_mfma_f32_16x16x32_bf16 v[108:111], v[156:159], v[192:195], v[108:111]
	v_mfma_f32_16x16x32_bf16 v[96:99], v[148:151], v[202:205], v[96:99]
	v_mfma_f32_16x16x32_bf16 v[92:95], v[156:159], v[202:205], v[92:95]
	v_mfma_f32_16x16x32_bf16 v[80:83], v[148:151], v[228:231], v[80:83]
	v_mfma_f32_16x16x32_bf16 v[76:79], v[156:159], v[228:231], v[76:79]
	v_mfma_f32_16x16x32_bf16 v[72:75], v[148:151], v[236:239], v[72:75]
	v_mfma_f32_16x16x32_bf16 v[68:71], v[156:159], v[236:239], v[68:71]
	v_mfma_f32_16x16x32_bf16 v[112:115], v[152:155], v[196:199], v[112:115]
	v_mfma_f32_16x16x32_bf16 v[108:111], v[160:163], v[196:199], v[108:111]
	v_mfma_f32_16x16x32_bf16 v[96:99], v[152:155], v[206:209], v[96:99]
	v_mfma_f32_16x16x32_bf16 v[92:95], v[160:163], v[206:209], v[92:95]
	v_mfma_f32_16x16x32_bf16 v[80:83], v[152:155], v[232:235], v[80:83]
	v_mfma_f32_16x16x32_bf16 v[76:79], v[160:163], v[232:235], v[76:79]
	v_mfma_f32_16x16x32_bf16 v[72:75], v[152:155], v[240:243], v[72:75]
	v_mfma_f32_16x16x32_bf16 v[68:71], v[160:163], v[240:243], v[68:71]
	s_barrier
	s_add_i32 s13, s13, s62
	v_lshl_add_u64 v[210:211], v[210:211], 0, s[86:87]
	s_mov_b32 m0, s13
	ds_read_b128 v[192:195], v200 offset:49152
	ds_read_b128 v[196:199], v200 offset:50176
	ds_read_b128 v[202:205], v200 offset:51200
	ds_read_b128 v[206:209], v200 offset:52224
	ds_read_b128 v[228:231], v200 offset:53248
	ds_read_b128 v[232:235], v200 offset:54272
	ds_read_b128 v[236:239], v200 offset:55296
	ds_read_b128 v[240:243], v200 offset:56320
	global_load_lds_dwordx4 v[210:211], off
	s_add_i32 m0, s13, 0x2000
	s_add_u32 s70, s80, 0x80080
	v_lshl_add_u64 v[210:211], v[216:217], 0, s[86:87]
	s_addc_u32 s71, s81, 0
	s_add_i32 s13, s33, s62
	global_load_lds_dwordx4 v[210:211], off
	v_lshl_add_u64 v[210:211], s[70:71], 0, v[166:167]
	s_mov_b32 m0, s13
	s_nop 0
	global_load_lds_dwordx4 v[210:211], off
	v_lshl_add_u64 v[210:211], s[70:71], 0, v[170:171]
	s_add_i32 m0, s13, 0x2000
	s_nop 0
	global_load_lds_dwordx4 v[210:211], off
	v_lshl_add_u64 v[210:211], v[218:219], 0, s[86:87]
	s_mov_b32 m0, s49
	s_nop 0
	global_load_lds_dwordx4 v[210:211], off
	v_lshl_add_u64 v[210:211], v[220:221], 0, s[86:87]
	s_mov_b32 m0, s50
	s_nop 0
	global_load_lds_dwordx4 v[210:211], off
	s_waitcnt vmcnt(8)
	s_waitcnt lgkmcnt(0)
	s_barrier
	s_waitcnt lgkmcnt(0)
	v_mfma_f32_16x16x32_bf16 v[64:67], v[132:135], v[192:195], v[64:67]
	v_mfma_f32_16x16x32_bf16 v[60:63], v[140:143], v[192:195], v[60:63]
	v_mfma_f32_16x16x32_bf16 v[56:59], v[132:135], v[202:205], v[56:59]
	v_mfma_f32_16x16x32_bf16 v[52:55], v[140:143], v[202:205], v[52:55]
	v_mfma_f32_16x16x32_bf16 v[40:43], v[132:135], v[228:231], v[40:43]
	v_mfma_f32_16x16x32_bf16 v[36:39], v[140:143], v[228:231], v[36:39]
	v_mfma_f32_16x16x32_bf16 v[24:27], v[132:135], v[236:239], v[24:27]
	v_mfma_f32_16x16x32_bf16 v[20:23], v[140:143], v[236:239], v[20:23]
	v_mfma_f32_16x16x32_bf16 v[64:67], v[136:139], v[196:199], v[64:67]
	v_mfma_f32_16x16x32_bf16 v[60:63], v[144:147], v[196:199], v[60:63]
	v_mfma_f32_16x16x32_bf16 v[56:59], v[136:139], v[206:209], v[56:59]
	v_mfma_f32_16x16x32_bf16 v[52:55], v[144:147], v[206:209], v[52:55]
	v_mfma_f32_16x16x32_bf16 v[40:43], v[136:139], v[232:235], v[40:43]
	v_mfma_f32_16x16x32_bf16 v[36:39], v[144:147], v[232:235], v[36:39]
	v_mfma_f32_16x16x32_bf16 v[24:27], v[136:139], v[240:243], v[24:27]
	v_mfma_f32_16x16x32_bf16 v[20:23], v[144:147], v[240:243], v[20:23]
	v_mfma_f32_16x16x32_bf16 v[48:51], v[148:151], v[192:195], v[48:51]
	v_mfma_f32_16x16x32_bf16 v[44:47], v[156:159], v[192:195], v[44:47]
	v_mfma_f32_16x16x32_bf16 v[32:35], v[148:151], v[202:205], v[32:35]
	v_mfma_f32_16x16x32_bf16 v[28:31], v[156:159], v[202:205], v[28:31]
	v_mfma_f32_16x16x32_bf16 v[16:19], v[148:151], v[228:231], v[16:19]
	v_mfma_f32_16x16x32_bf16 v[12:15], v[156:159], v[228:231], v[12:15]
	v_mfma_f32_16x16x32_bf16 v[8:11], v[148:151], v[236:239], v[8:11]
	v_mfma_f32_16x16x32_bf16 v[4:7], v[156:159], v[236:239], v[4:7]
	v_mfma_f32_16x16x32_bf16 v[48:51], v[152:155], v[196:199], v[48:51]
	v_mfma_f32_16x16x32_bf16 v[44:47], v[160:163], v[196:199], v[44:47]
	v_mfma_f32_16x16x32_bf16 v[32:35], v[152:155], v[206:209], v[32:35]
	v_mfma_f32_16x16x32_bf16 v[28:31], v[160:163], v[206:209], v[28:31]
	v_mfma_f32_16x16x32_bf16 v[16:19], v[152:155], v[232:235], v[16:19]
	v_mfma_f32_16x16x32_bf16 v[12:15], v[160:163], v[232:235], v[12:15]
	v_mfma_f32_16x16x32_bf16 v[8:11], v[152:155], v[240:243], v[8:11]
	v_mfma_f32_16x16x32_bf16 v[4:7], v[160:163], v[240:243], v[4:7]
	s_barrier
	s_add_i32 s12, s12, 2
	s_add_u32 s0, s0, 0x100
	s_addc_u32 s7, s7, 0
	s_add_u32 s8, s8, 0x100
	s_addc_u32 s9, s9, 0
	s_cmp_gt_u32 s12, 29
	s_cbranch_scc0 .LBB6_497
	s_and_b64 vcc, exec, s[24:25]
	s_cbranch_vccz .LBB6_500
	s_barrier

.LBB6_694:
	s_add_u32 s20, s18, 0xfffc0080
	s_addc_u32 s21, s19, -1
	s_add_i32 s0, 0, 0x10000
	s_cmp_eq_u32 s13, 12
	s_cselect_b32 s23, s11, s21
	s_cselect_b32 s22, s10, s20
	s_cselect_b32 s21, s15, s12
	s_cselect_b32 s20, s14, s9
	s_add_i32 s33, 0, 0x14000
	v_add_u32_e32 v4, s0, v186
	v_add_u32_e32 v16, s33, v186
	ds_read_b128 v[20:23], v4
	ds_read_b128 v[24:27], v4 offset:1024
	ds_read_b128 v[28:31], v4 offset:2048
	ds_read_b128 v[32:35], v4 offset:3072
	ds_read_b128 v[4:7], v16
	ds_read_b128 v[8:11], v16 offset:1024
	ds_read_b128 v[12:15], v16 offset:2048
	ds_read_b128 v[16:19], v16 offset:3072
	v_lshl_add_u64 v[176:177], s[18:19], 0, v[174:175]
	s_add_i32 m0, s30, 0xc000
	ds_read_b128 v[188:191], v187
	ds_read_b128 v[192:195], v187 offset:1024
	ds_read_b128 v[196:199], v187 offset:2048
	ds_read_b128 v[200:203], v187 offset:3072
	ds_read_b128 v[204:207], v187 offset:4096
	ds_read_b128 v[208:211], v187 offset:5120
	ds_read_b128 v[228:231], v187 offset:6144
	ds_read_b128 v[232:235], v187 offset:7168
	global_load_lds_dwordx4 v[176:177], off
	v_lshl_add_u64 v[176:177], s[18:19], 0, v[172:173]
	s_add_i32 m0, s30, 0xe000
	s_nop 0
	global_load_lds_dwordx4 v[176:177], off
	s_waitcnt vmcnt(8)
	s_waitcnt lgkmcnt(0)
	s_barrier
	s_waitcnt lgkmcnt(0)
	v_mfma_f32_16x16x128_f8f6f4 v[160:163], v[20:27], v[188:195], v[160:163]
	v_mfma_f32_16x16x128_f8f6f4 v[156:159], v[28:35], v[188:195], v[156:159]
	v_mfma_f32_16x16x128_f8f6f4 v[144:147], v[20:27], v[196:203], v[144:147]
	v_mfma_f32_16x16x128_f8f6f4 v[140:143], v[28:35], v[196:203], v[140:143]
	v_mfma_f32_16x16x128_f8f6f4 v[128:131], v[20:27], v[204:211], v[128:131]
	v_mfma_f32_16x16x128_f8f6f4 v[124:127], v[28:35], v[204:211], v[124:127]
	v_mfma_f32_16x16x128_f8f6f4 v[112:115], v[20:27], v[228:235], v[112:115]
	v_mfma_f32_16x16x128_f8f6f4 v[108:111], v[28:35], v[228:235], v[108:111]
	v_mfma_f32_16x16x128_f8f6f4 v[152:155], v[4:11], v[188:195], v[152:155]
	v_mfma_f32_16x16x128_f8f6f4 v[148:151], v[12:19], v[188:195], v[148:151]
	v_mfma_f32_16x16x128_f8f6f4 v[136:139], v[4:11], v[196:203], v[136:139]
	v_mfma_f32_16x16x128_f8f6f4 v[132:135], v[12:19], v[196:203], v[132:135]
	v_mfma_f32_16x16x128_f8f6f4 v[120:123], v[4:11], v[204:211], v[120:123]
	v_mfma_f32_16x16x128_f8f6f4 v[116:119], v[12:19], v[204:211], v[116:119]
	v_mfma_f32_16x16x128_f8f6f4 v[104:107], v[4:11], v[228:235], v[104:107]
	v_mfma_f32_16x16x128_f8f6f4 v[100:103], v[12:19], v[228:235], v[100:103]
	s_barrier
	s_add_i32 s0, s0, s28
	v_lshl_add_u64 v[176:177], s[20:21], 0, v[2:3]
	s_mov_b32 m0, s0
	ds_read_b128 v[188:191], v187 offset:16384
	ds_read_b128 v[192:195], v187 offset:17408
	ds_read_b128 v[196:199], v187 offset:18432
	ds_read_b128 v[200:203], v187 offset:19456
	ds_read_b128 v[204:207], v187 offset:20480
	ds_read_b128 v[208:211], v187 offset:21504
	ds_read_b128 v[228:231], v187 offset:22528
	ds_read_b128 v[232:235], v187 offset:23552
	global_load_lds_dwordx4 v[176:177], off
	s_add_i32 m0, s0, 0x2000
	s_add_u32 s58, s20, 0x40000
	v_lshl_add_u64 v[178:179], s[20:21], 0, v[168:169]
	s_addc_u32 s59, s21, 0
	s_add_i32 s0, s33, s28
	global_load_lds_dwordx4 v[178:179], off
	v_lshl_add_u64 v[182:183], s[58:59], 0, v[2:3]
	s_mov_b32 m0, s0
	v_lshl_add_u64 v[184:185], s[22:23], 0, v[166:167]
	global_load_lds_dwordx4 v[182:183], off
	v_lshl_add_u64 v[182:183], s[58:59], 0, v[168:169]
	s_add_i32 m0, s0, 0x2000
	s_nop 0
	global_load_lds_dwordx4 v[182:183], off
	v_lshl_add_u64 v[182:183], s[22:23], 0, v[164:165]
	s_mov_b32 m0, s30
	s_nop 0
	global_load_lds_dwordx4 v[182:183], off
	s_mov_b32 m0, s31
	s_nop 0
	global_load_lds_dwordx4 v[184:185], off
	s_waitcnt vmcnt(8)
	s_waitcnt lgkmcnt(0)
	s_barrier
	s_waitcnt lgkmcnt(0)
	v_mfma_f32_16x16x128_f8f6f4 v[96:99], v[20:27], v[188:195], v[96:99]
	v_mfma_f32_16x16x128_f8f6f4 v[92:95], v[28:35], v[188:195], v[92:95]
	v_mfma_f32_16x16x128_f8f6f4 v[80:83], v[20:27], v[196:203], v[80:83]
	v_mfma_f32_16x16x128_f8f6f4 v[76:79], v[28:35], v[196:203], v[76:79]
	v_mfma_f32_16x16x128_f8f6f4 v[64:67], v[20:27], v[204:211], v[64:67]
	v_mfma_f32_16x16x128_f8f6f4 v[60:63], v[28:35], v[204:211], v[60:63]
	v_mfma_f32_16x16x128_f8f6f4 v[48:51], v[20:27], v[228:235], v[48:51]
	v_mfma_f32_16x16x128_f8f6f4 v[44:47], v[28:35], v[228:235], v[44:47]
	v_mfma_f32_16x16x128_f8f6f4 v[88:91], v[4:11], v[188:195], v[88:91]
	v_mfma_f32_16x16x128_f8f6f4 v[84:87], v[12:19], v[188:195], v[84:87]
	v_mfma_f32_16x16x128_f8f6f4 v[72:75], v[4:11], v[196:203], v[72:75]
	v_mfma_f32_16x16x128_f8f6f4 v[68:71], v[12:19], v[196:203], v[68:71]
	v_mfma_f32_16x16x128_f8f6f4 v[56:59], v[4:11], v[204:211], v[56:59]
	v_mfma_f32_16x16x128_f8f6f4 v[52:55], v[12:19], v[204:211], v[52:55]
	v_mfma_f32_16x16x128_f8f6f4 v[40:43], v[4:11], v[228:235], v[40:43]
	v_mfma_f32_16x16x128_f8f6f4 v[36:39], v[12:19], v[228:235], v[36:39]
	s_barrier
	s_add_i32 s0, 0, 0x18000
	s_add_i32 s33, 0, 0x1c000
	v_add_u32_e32 v16, s0, v186
	v_add_u32_e32 v32, s33, v186
	ds_read_b128 v[4:7], v16
	ds_read_b128 v[8:11], v16 offset:1024
	ds_read_b128 v[12:15], v16 offset:2048
	ds_read_b128 v[16:19], v16 offset:3072
	ds_read_b128 v[20:23], v32
	ds_read_b128 v[24:27], v32 offset:1024
	ds_read_b128 v[28:31], v32 offset:2048
	ds_read_b128 v[32:35], v32 offset:3072
	s_add_u32 s22, s22, 0x40000
	s_addc_u32 s23, s23, 0
	s_mov_b32 m0, s34
	v_lshl_add_u64 v[216:217], s[22:23], 0, v[164:165]
	ds_read_b128 v[188:191], v187 offset:32768
	ds_read_b128 v[192:195], v187 offset:33792
	ds_read_b128 v[196:199], v187 offset:34816
	ds_read_b128 v[200:203], v187 offset:35840
	ds_read_b128 v[204:207], v187 offset:36864
	ds_read_b128 v[208:211], v187 offset:37888
	ds_read_b128 v[228:231], v187 offset:38912
	ds_read_b128 v[232:235], v187 offset:39936
	global_load_lds_dwordx4 v[216:217], off
	v_lshl_add_u64 v[216:217], s[22:23], 0, v[166:167]
	s_mov_b32 m0, s35
	s_nop 0
	global_load_lds_dwordx4 v[216:217], off
	s_waitcnt vmcnt(8)
	s_waitcnt lgkmcnt(0)
	s_barrier
	s_waitcnt lgkmcnt(0)
	v_mfma_f32_16x16x128_f8f6f4 v[160:163], v[4:11], v[188:195], v[160:163]
	v_mfma_f32_16x16x128_f8f6f4 v[156:159], v[12:19], v[188:195], v[156:159]
	v_mfma_f32_16x16x128_f8f6f4 v[144:147], v[4:11], v[196:203], v[144:147]
	v_mfma_f32_16x16x128_f8f6f4 v[140:143], v[12:19], v[196:203], v[140:143]
	v_mfma_f32_16x16x128_f8f6f4 v[128:131], v[4:11], v[204:211], v[128:131]
	v_mfma_f32_16x16x128_f8f6f4 v[124:127], v[12:19], v[204:211], v[124:127]
	v_mfma_f32_16x16x128_f8f6f4 v[112:115], v[4:11], v[228:235], v[112:115]
	v_mfma_f32_16x16x128_f8f6f4 v[108:111], v[12:19], v[228:235], v[108:111]
	v_mfma_f32_16x16x128_f8f6f4 v[152:155], v[20:27], v[188:195], v[152:155]
	v_mfma_f32_16x16x128_f8f6f4 v[148:151], v[28:35], v[188:195], v[148:151]
	v_mfma_f32_16x16x128_f8f6f4 v[136:139], v[20:27], v[196:203], v[136:139]
	v_mfma_f32_16x16x128_f8f6f4 v[132:135], v[28:35], v[196:203], v[132:135]
	v_mfma_f32_16x16x128_f8f6f4 v[120:123], v[20:27], v[204:211], v[120:123]
	v_mfma_f32_16x16x128_f8f6f4 v[116:119], v[28:35], v[204:211], v[116:119]
	v_mfma_f32_16x16x128_f8f6f4 v[104:107], v[20:27], v[228:235], v[104:107]
	v_mfma_f32_16x16x128_f8f6f4 v[100:103], v[28:35], v[228:235], v[100:103]
	s_barrier
	s_add_i32 s0, s0, s28
	v_lshl_add_u64 v[176:177], v[176:177], 0, s[86:87]
	s_mov_b32 m0, s0
	ds_read_b128 v[188:191], v187 offset:49152
	ds_read_b128 v[192:195], v187 offset:50176
	ds_read_b128 v[196:199], v187 offset:51200
	ds_read_b128 v[200:203], v187 offset:52224
	ds_read_b128 v[204:207], v187 offset:53248
	ds_read_b128 v[208:211], v187 offset:54272
	ds_read_b128 v[228:231], v187 offset:55296
	ds_read_b128 v[232:235], v187 offset:56320
	global_load_lds_dwordx4 v[176:177], off
	s_add_i32 m0, s0, 0x2000
	s_add_u32 s20, s20, 0x40080
	v_lshl_add_u64 v[176:177], v[178:179], 0, s[86:87]
	s_addc_u32 s21, s21, 0
	s_add_i32 s0, s33, s28
	global_load_lds_dwordx4 v[176:177], off
	v_lshl_add_u64 v[176:177], s[20:21], 0, v[2:3]
	s_mov_b32 m0, s0
	s_nop 0
	global_load_lds_dwordx4 v[176:177], off
	v_lshl_add_u64 v[176:177], s[20:21], 0, v[168:169]
	s_add_i32 m0, s0, 0x2000
	s_nop 0
	global_load_lds_dwordx4 v[176:177], off
	v_lshl_add_u64 v[176:177], v[182:183], 0, s[86:87]
	s_mov_b32 m0, s36
	s_nop 0
	global_load_lds_dwordx4 v[176:177], off
	v_lshl_add_u64 v[176:177], v[184:185], 0, s[86:87]
	s_mov_b32 m0, s37
	s_nop 0
	global_load_lds_dwordx4 v[176:177], off
	s_waitcnt vmcnt(8)
	s_waitcnt lgkmcnt(0)
	s_barrier
	s_waitcnt lgkmcnt(0)
	v_mfma_f32_16x16x128_f8f6f4 v[96:99], v[4:11], v[188:195], v[96:99]
	v_mfma_f32_16x16x128_f8f6f4 v[92:95], v[12:19], v[188:195], v[92:95]
	v_mfma_f32_16x16x128_f8f6f4 v[80:83], v[4:11], v[196:203], v[80:83]
	v_mfma_f32_16x16x128_f8f6f4 v[76:79], v[12:19], v[196:203], v[76:79]
	v_mfma_f32_16x16x128_f8f6f4 v[64:67], v[4:11], v[204:211], v[64:67]
	v_mfma_f32_16x16x128_f8f6f4 v[60:63], v[12:19], v[204:211], v[60:63]
	v_mfma_f32_16x16x128_f8f6f4 v[48:51], v[4:11], v[228:235], v[48:51]
	v_mfma_f32_16x16x128_f8f6f4 v[44:47], v[12:19], v[228:235], v[44:47]
	v_mfma_f32_16x16x128_f8f6f4 v[88:91], v[20:27], v[188:195], v[88:91]
	v_mfma_f32_16x16x128_f8f6f4 v[84:87], v[28:35], v[188:195], v[84:87]
	v_mfma_f32_16x16x128_f8f6f4 v[72:75], v[20:27], v[196:203], v[72:75]
	v_mfma_f32_16x16x128_f8f6f4 v[68:71], v[28:35], v[196:203], v[68:71]
	v_mfma_f32_16x16x128_f8f6f4 v[56:59], v[20:27], v[204:211], v[56:59]
	v_mfma_f32_16x16x128_f8f6f4 v[52:55], v[28:35], v[204:211], v[52:55]
	v_mfma_f32_16x16x128_f8f6f4 v[40:43], v[20:27], v[228:235], v[40:43]
	v_mfma_f32_16x16x128_f8f6f4 v[36:39], v[28:35], v[228:235], v[36:39]
	s_barrier
	s_add_i32 s13, s13, 2
	s_add_u32 s9, s9, 0x100
	s_addc_u32 s12, s12, 0
	s_add_u32 s18, s18, 0x100
	s_addc_u32 s19, s19, 0
	s_cmp_gt_u32 s13, 13
	s_cbranch_scc0 .LBB6_694
	s_nop 7
	s_nop 7
	s_nop 7
	s_and_b64 vcc, exec, s[6:7]
	s_cbranch_vccz .LBB6_697
	s_barrier

.LBB6_770:
	s_add_u32 s6, s4, 0xfffe0080
	s_addc_u32 s7, s5, -1
	s_add_i32 s21, 0, 0x10000
	s_cmp_eq_u32 s13, 4
	s_cselect_b32 s31, s23, s7
	s_cselect_b32 s30, s22, s6
	v_add_u32_e32 v2, s21, v159
	s_cselect_b32 s7, s25, s1
	s_cselect_b32 s6, s24, s0
	s_add_i32 s33, 0, 0x14000
	ds_read_b128 v[132:135], v2
	ds_read_b128 v[136:139], v2 offset:1024
	ds_read_b128 v[140:143], v2 offset:2048
	ds_read_b128 v[144:147], v2 offset:3072
	v_add_u32_e32 v2, s33, v159
	ds_read_b128 v[166:169], v2
	ds_read_b128 v[170:173], v2 offset:1024
	ds_read_b128 v[174:177], v2 offset:2048
	ds_read_b128 v[184:187], v2 offset:3072
	v_lshl_add_u64 v[178:179], s[4:5], 0, v[164:165]
	s_add_i32 m0, s92, 0xc000
	ds_read_b128 v[188:191], v182
	ds_read_b128 v[192:195], v182 offset:1024
	ds_read_b128 v[196:199], v182 offset:2048
	ds_read_b128 v[200:203], v182 offset:3072
	ds_read_b128 v[204:207], v182 offset:4096
	ds_read_b128 v[208:211], v182 offset:5120
	ds_read_b128 v[228:231], v182 offset:6144
	ds_read_b128 v[232:235], v182 offset:7168
	global_load_lds_dwordx4 v[178:179], off
	v_lshl_add_u64 v[178:179], s[4:5], 0, v[162:163]
	s_add_i32 m0, s92, 0xe000
	s_nop 0
	global_load_lds_dwordx4 v[178:179], off
	s_waitcnt vmcnt(8)
	s_waitcnt lgkmcnt(0)
	s_barrier
	s_waitcnt lgkmcnt(0)
	v_mfma_f32_16x16x32_bf16 v[128:131], v[132:135], v[188:191], v[128:131]
	v_mfma_f32_16x16x32_bf16 v[124:127], v[140:143], v[188:191], v[124:127]
	v_mfma_f32_16x16x32_bf16 v[120:123], v[132:135], v[196:199], v[120:123]
	v_mfma_f32_16x16x32_bf16 v[116:119], v[140:143], v[196:199], v[116:119]
	v_mfma_f32_16x16x32_bf16 v[112:115], v[132:135], v[204:207], v[112:115]
	v_mfma_f32_16x16x32_bf16 v[108:111], v[140:143], v[204:207], v[108:111]
	v_mfma_f32_16x16x32_bf16 v[104:107], v[132:135], v[228:231], v[104:107]
	v_mfma_f32_16x16x32_bf16 v[100:103], v[140:143], v[228:231], v[100:103]
	v_mfma_f32_16x16x32_bf16 v[128:131], v[136:139], v[192:195], v[128:131]
	v_mfma_f32_16x16x32_bf16 v[124:127], v[144:147], v[192:195], v[124:127]
	v_mfma_f32_16x16x32_bf16 v[120:123], v[136:139], v[200:203], v[120:123]
	v_mfma_f32_16x16x32_bf16 v[116:119], v[144:147], v[200:203], v[116:119]
	v_mfma_f32_16x16x32_bf16 v[112:115], v[136:139], v[208:211], v[112:115]
	v_mfma_f32_16x16x32_bf16 v[108:111], v[144:147], v[208:211], v[108:111]
	v_mfma_f32_16x16x32_bf16 v[104:107], v[136:139], v[232:235], v[104:107]
	v_mfma_f32_16x16x32_bf16 v[100:103], v[144:147], v[232:235], v[100:103]
	v_mfma_f32_16x16x32_bf16 v[64:67], v[166:169], v[188:191], v[64:67]
	v_mfma_f32_16x16x32_bf16 v[60:63], v[174:177], v[188:191], v[60:63]
	v_mfma_f32_16x16x32_bf16 v[56:59], v[166:169], v[196:199], v[56:59]
	v_mfma_f32_16x16x32_bf16 v[52:55], v[174:177], v[196:199], v[52:55]
	v_mfma_f32_16x16x32_bf16 v[48:51], v[166:169], v[204:207], v[48:51]
	v_mfma_f32_16x16x32_bf16 v[44:47], v[174:177], v[204:207], v[44:47]
	v_mfma_f32_16x16x32_bf16 v[40:43], v[166:169], v[228:231], v[40:43]
	v_mfma_f32_16x16x32_bf16 v[36:39], v[174:177], v[228:231], v[36:39]
	v_mfma_f32_16x16x32_bf16 v[64:67], v[170:173], v[192:195], v[64:67]
	v_mfma_f32_16x16x32_bf16 v[60:63], v[184:187], v[192:195], v[60:63]
	v_mfma_f32_16x16x32_bf16 v[56:59], v[170:173], v[200:203], v[56:59]
	v_mfma_f32_16x16x32_bf16 v[52:55], v[184:187], v[200:203], v[52:55]
	v_mfma_f32_16x16x32_bf16 v[48:51], v[170:173], v[208:211], v[48:51]
	v_mfma_f32_16x16x32_bf16 v[44:47], v[184:187], v[208:211], v[44:47]
	v_mfma_f32_16x16x32_bf16 v[40:43], v[170:173], v[232:235], v[40:43]
	v_mfma_f32_16x16x32_bf16 v[36:39], v[184:187], v[232:235], v[36:39]
	s_barrier
	s_add_i32 s21, s21, s29
	v_lshl_add_u64 v[178:179], s[6:7], 0, v[150:151]
	s_mov_b32 m0, s21
	ds_read_b128 v[188:191], v182 offset:16384
	ds_read_b128 v[192:195], v182 offset:17408
	ds_read_b128 v[196:199], v182 offset:18432
	ds_read_b128 v[200:203], v182 offset:19456
	ds_read_b128 v[204:207], v182 offset:20480
	ds_read_b128 v[208:211], v182 offset:21504
	ds_read_b128 v[228:231], v182 offset:22528
	ds_read_b128 v[232:235], v182 offset:23552
	global_load_lds_dwordx4 v[178:179], off
	s_add_i32 m0, s21, 0x2000
	s_add_u32 s34, s6, 0x20000
	v_lshl_add_u64 v[216:217], s[6:7], 0, v[154:155]
	s_addc_u32 s35, s7, 0
	s_add_i32 s21, s33, s29
	global_load_lds_dwordx4 v[216:217], off
	v_lshl_add_u64 v[218:219], s[34:35], 0, v[150:151]
	s_mov_b32 m0, s21
	v_lshl_add_u64 v[220:221], s[30:31], 0, v[152:153]
	global_load_lds_dwordx4 v[218:219], off
	v_lshl_add_u64 v[218:219], s[34:35], 0, v[154:155]
	s_add_i32 m0, s21, 0x2000
	s_nop 0
	global_load_lds_dwordx4 v[218:219], off
	v_lshl_add_u64 v[218:219], s[30:31], 0, v[148:149]
	s_mov_b32 m0, s92
	s_nop 0
	global_load_lds_dwordx4 v[218:219], off
	s_mov_b32 m0, s93
	s_nop 0
	global_load_lds_dwordx4 v[220:221], off
	s_waitcnt vmcnt(8)
	s_waitcnt lgkmcnt(0)
	s_barrier
	s_waitcnt lgkmcnt(0)
	v_mfma_f32_16x16x32_bf16 v[96:99], v[132:135], v[188:191], v[96:99]
	v_mfma_f32_16x16x32_bf16 v[92:95], v[140:143], v[188:191], v[92:95]
	v_mfma_f32_16x16x32_bf16 v[88:91], v[132:135], v[196:199], v[88:91]
	v_mfma_f32_16x16x32_bf16 v[84:87], v[140:143], v[196:199], v[84:87]
	v_mfma_f32_16x16x32_bf16 v[80:83], v[132:135], v[204:207], v[80:83]
	v_mfma_f32_16x16x32_bf16 v[76:79], v[140:143], v[204:207], v[76:79]
	v_mfma_f32_16x16x32_bf16 v[72:75], v[132:135], v[228:231], v[72:75]
	v_mfma_f32_16x16x32_bf16 v[68:71], v[140:143], v[228:231], v[68:71]
	v_mfma_f32_16x16x32_bf16 v[96:99], v[136:139], v[192:195], v[96:99]
	v_mfma_f32_16x16x32_bf16 v[92:95], v[144:147], v[192:195], v[92:95]
	v_mfma_f32_16x16x32_bf16 v[88:91], v[136:139], v[200:203], v[88:91]
	v_mfma_f32_16x16x32_bf16 v[84:87], v[144:147], v[200:203], v[84:87]
	v_mfma_f32_16x16x32_bf16 v[80:83], v[136:139], v[208:211], v[80:83]
	v_mfma_f32_16x16x32_bf16 v[76:79], v[144:147], v[208:211], v[76:79]
	v_mfma_f32_16x16x32_bf16 v[72:75], v[136:139], v[232:235], v[72:75]
	v_mfma_f32_16x16x32_bf16 v[68:71], v[144:147], v[232:235], v[68:71]
	v_mfma_f32_16x16x32_bf16 v[32:35], v[166:169], v[188:191], v[32:35]
	v_mfma_f32_16x16x32_bf16 v[28:31], v[174:177], v[188:191], v[28:31]
	v_mfma_f32_16x16x32_bf16 v[24:27], v[166:169], v[196:199], v[24:27]
	v_mfma_f32_16x16x32_bf16 v[20:23], v[174:177], v[196:199], v[20:23]
	v_mfma_f32_16x16x32_bf16 v[16:19], v[166:169], v[204:207], v[16:19]
	v_mfma_f32_16x16x32_bf16 v[12:15], v[174:177], v[204:207], v[12:15]
	v_mfma_f32_16x16x32_bf16 v[8:11], v[166:169], v[228:231], v[8:11]
	v_mfma_f32_16x16x32_bf16 v[4:7], v[174:177], v[228:231], v[4:7]
	v_mfma_f32_16x16x32_bf16 v[32:35], v[170:173], v[192:195], v[32:35]
	v_mfma_f32_16x16x32_bf16 v[28:31], v[184:187], v[192:195], v[28:31]
	v_mfma_f32_16x16x32_bf16 v[24:27], v[170:173], v[200:203], v[24:27]
	v_mfma_f32_16x16x32_bf16 v[20:23], v[184:187], v[200:203], v[20:23]
	v_mfma_f32_16x16x32_bf16 v[16:19], v[170:173], v[208:211], v[16:19]
	v_mfma_f32_16x16x32_bf16 v[12:15], v[184:187], v[208:211], v[12:15]
	v_mfma_f32_16x16x32_bf16 v[8:11], v[170:173], v[232:235], v[8:11]
	v_mfma_f32_16x16x32_bf16 v[4:7], v[184:187], v[232:235], v[4:7]
	s_barrier
	s_add_i32 s21, 0, 0x18000
	v_add_u32_e32 v2, s21, v159
	s_add_i32 s33, 0, 0x1c000
	ds_read_b128 v[132:135], v2
	ds_read_b128 v[136:139], v2 offset:1024
	ds_read_b128 v[140:143], v2 offset:2048
	ds_read_b128 v[144:147], v2 offset:3072
	v_add_u32_e32 v2, s33, v159
	ds_read_b128 v[166:169], v2
	ds_read_b128 v[170:173], v2 offset:1024
	ds_read_b128 v[174:177], v2 offset:2048
	ds_read_b128 v[184:187], v2 offset:3072
	s_add_u32 s30, s30, 0x20000
	s_addc_u32 s31, s31, 0
	s_mov_b32 m0, s94
	v_lshl_add_u64 v[222:223], s[30:31], 0, v[148:149]
	ds_read_b128 v[188:191], v182 offset:32768
	ds_read_b128 v[192:195], v182 offset:33792
	ds_read_b128 v[196:199], v182 offset:34816
	ds_read_b128 v[200:203], v182 offset:35840
	ds_read_b128 v[204:207], v182 offset:36864
	ds_read_b128 v[208:211], v182 offset:37888
	ds_read_b128 v[228:231], v182 offset:38912
	ds_read_b128 v[232:235], v182 offset:39936
	global_load_lds_dwordx4 v[222:223], off
	v_lshl_add_u64 v[222:223], s[30:31], 0, v[152:153]
	s_mov_b32 m0, s95
	s_nop 0
	global_load_lds_dwordx4 v[222:223], off
	s_waitcnt vmcnt(8)
	s_waitcnt lgkmcnt(0)
	s_barrier
	s_waitcnt lgkmcnt(0)
	v_mfma_f32_16x16x32_bf16 v[128:131], v[132:135], v[188:191], v[128:131]
	v_mfma_f32_16x16x32_bf16 v[124:127], v[140:143], v[188:191], v[124:127]
	v_mfma_f32_16x16x32_bf16 v[120:123], v[132:135], v[196:199], v[120:123]
	v_mfma_f32_16x16x32_bf16 v[116:119], v[140:143], v[196:199], v[116:119]
	v_mfma_f32_16x16x32_bf16 v[112:115], v[132:135], v[204:207], v[112:115]
	v_mfma_f32_16x16x32_bf16 v[108:111], v[140:143], v[204:207], v[108:111]
	v_mfma_f32_16x16x32_bf16 v[104:107], v[132:135], v[228:231], v[104:107]
	v_mfma_f32_16x16x32_bf16 v[100:103], v[140:143], v[228:231], v[100:103]
	v_mfma_f32_16x16x32_bf16 v[128:131], v[136:139], v[192:195], v[128:131]
	v_mfma_f32_16x16x32_bf16 v[124:127], v[144:147], v[192:195], v[124:127]
	v_mfma_f32_16x16x32_bf16 v[120:123], v[136:139], v[200:203], v[120:123]
	v_mfma_f32_16x16x32_bf16 v[116:119], v[144:147], v[200:203], v[116:119]
	v_mfma_f32_16x16x32_bf16 v[112:115], v[136:139], v[208:211], v[112:115]
	v_mfma_f32_16x16x32_bf16 v[108:111], v[144:147], v[208:211], v[108:111]
	v_mfma_f32_16x16x32_bf16 v[104:107], v[136:139], v[232:235], v[104:107]
	v_mfma_f32_16x16x32_bf16 v[100:103], v[144:147], v[232:235], v[100:103]
	v_mfma_f32_16x16x32_bf16 v[64:67], v[166:169], v[188:191], v[64:67]
	v_mfma_f32_16x16x32_bf16 v[60:63], v[174:177], v[188:191], v[60:63]
	v_mfma_f32_16x16x32_bf16 v[56:59], v[166:169], v[196:199], v[56:59]
	v_mfma_f32_16x16x32_bf16 v[52:55], v[174:177], v[196:199], v[52:55]
	v_mfma_f32_16x16x32_bf16 v[48:51], v[166:169], v[204:207], v[48:51]
	v_mfma_f32_16x16x32_bf16 v[44:47], v[174:177], v[204:207], v[44:47]
	v_mfma_f32_16x16x32_bf16 v[40:43], v[166:169], v[228:231], v[40:43]
	v_mfma_f32_16x16x32_bf16 v[36:39], v[174:177], v[228:231], v[36:39]
	v_mfma_f32_16x16x32_bf16 v[64:67], v[170:173], v[192:195], v[64:67]
	v_mfma_f32_16x16x32_bf16 v[60:63], v[184:187], v[192:195], v[60:63]
	v_mfma_f32_16x16x32_bf16 v[56:59], v[170:173], v[200:203], v[56:59]
	v_mfma_f32_16x16x32_bf16 v[52:55], v[184:187], v[200:203], v[52:55]
	v_mfma_f32_16x16x32_bf16 v[48:51], v[170:173], v[208:211], v[48:51]
	v_mfma_f32_16x16x32_bf16 v[44:47], v[184:187], v[208:211], v[44:47]
	v_mfma_f32_16x16x32_bf16 v[40:43], v[170:173], v[232:235], v[40:43]
	v_mfma_f32_16x16x32_bf16 v[36:39], v[184:187], v[232:235], v[36:39]
	s_barrier
	s_add_i32 s21, s21, s29
	v_lshl_add_u64 v[178:179], v[178:179], 0, s[86:87]
	s_mov_b32 m0, s21
	ds_read_b128 v[188:191], v182 offset:49152
	ds_read_b128 v[192:195], v182 offset:50176
	ds_read_b128 v[196:199], v182 offset:51200
	ds_read_b128 v[200:203], v182 offset:52224
	ds_read_b128 v[204:207], v182 offset:53248
	ds_read_b128 v[208:211], v182 offset:54272
	ds_read_b128 v[228:231], v182 offset:55296
	ds_read_b128 v[232:235], v182 offset:56320
	global_load_lds_dwordx4 v[178:179], off
	s_add_i32 m0, s21, 0x2000
	s_add_u32 s6, s6, 0x20080
	v_lshl_add_u64 v[178:179], v[216:217], 0, s[86:87]
	s_addc_u32 s7, s7, 0
	s_add_i32 s21, s33, s29
	global_load_lds_dwordx4 v[178:179], off
	v_lshl_add_u64 v[178:179], s[6:7], 0, v[150:151]
	s_mov_b32 m0, s21
	s_nop 0
	global_load_lds_dwordx4 v[178:179], off
	v_lshl_add_u64 v[178:179], s[6:7], 0, v[154:155]
	s_add_i32 m0, s21, 0x2000
	s_nop 0
	global_load_lds_dwordx4 v[178:179], off
	v_lshl_add_u64 v[178:179], v[218:219], 0, s[86:87]
	s_mov_b32 m0, s47
	s_nop 0
	global_load_lds_dwordx4 v[178:179], off
	v_lshl_add_u64 v[178:179], v[220:221], 0, s[86:87]
	s_mov_b32 m0, s62
	s_nop 0
	global_load_lds_dwordx4 v[178:179], off
	s_waitcnt vmcnt(8)
	s_waitcnt lgkmcnt(0)
	s_barrier
	s_waitcnt lgkmcnt(0)
	v_mfma_f32_16x16x32_bf16 v[96:99], v[132:135], v[188:191], v[96:99]
	v_mfma_f32_16x16x32_bf16 v[92:95], v[140:143], v[188:191], v[92:95]
	v_mfma_f32_16x16x32_bf16 v[88:91], v[132:135], v[196:199], v[88:91]
	v_mfma_f32_16x16x32_bf16 v[84:87], v[140:143], v[196:199], v[84:87]
	v_mfma_f32_16x16x32_bf16 v[80:83], v[132:135], v[204:207], v[80:83]
	v_mfma_f32_16x16x32_bf16 v[76:79], v[140:143], v[204:207], v[76:79]
	v_mfma_f32_16x16x32_bf16 v[72:75], v[132:135], v[228:231], v[72:75]
	v_mfma_f32_16x16x32_bf16 v[68:71], v[140:143], v[228:231], v[68:71]
	v_mfma_f32_16x16x32_bf16 v[96:99], v[136:139], v[192:195], v[96:99]
	v_mfma_f32_16x16x32_bf16 v[92:95], v[144:147], v[192:195], v[92:95]
	v_mfma_f32_16x16x32_bf16 v[88:91], v[136:139], v[200:203], v[88:91]
	v_mfma_f32_16x16x32_bf16 v[84:87], v[144:147], v[200:203], v[84:87]
	v_mfma_f32_16x16x32_bf16 v[80:83], v[136:139], v[208:211], v[80:83]
	v_mfma_f32_16x16x32_bf16 v[76:79], v[144:147], v[208:211], v[76:79]
	v_mfma_f32_16x16x32_bf16 v[72:75], v[136:139], v[232:235], v[72:75]
	v_mfma_f32_16x16x32_bf16 v[68:71], v[144:147], v[232:235], v[68:71]
	v_mfma_f32_16x16x32_bf16 v[32:35], v[166:169], v[188:191], v[32:35]
	v_mfma_f32_16x16x32_bf16 v[28:31], v[174:177], v[188:191], v[28:31]
	v_mfma_f32_16x16x32_bf16 v[24:27], v[166:169], v[196:199], v[24:27]
	v_mfma_f32_16x16x32_bf16 v[20:23], v[174:177], v[196:199], v[20:23]
	v_mfma_f32_16x16x32_bf16 v[16:19], v[166:169], v[204:207], v[16:19]
	v_mfma_f32_16x16x32_bf16 v[12:15], v[174:177], v[204:207], v[12:15]
	v_mfma_f32_16x16x32_bf16 v[8:11], v[166:169], v[228:231], v[8:11]
	v_mfma_f32_16x16x32_bf16 v[4:7], v[174:177], v[228:231], v[4:7]
	v_mfma_f32_16x16x32_bf16 v[32:35], v[170:173], v[192:195], v[32:35]
	v_mfma_f32_16x16x32_bf16 v[28:31], v[184:187], v[192:195], v[28:31]
	v_mfma_f32_16x16x32_bf16 v[24:27], v[170:173], v[200:203], v[24:27]
	v_mfma_f32_16x16x32_bf16 v[20:23], v[184:187], v[200:203], v[20:23]
	v_mfma_f32_16x16x32_bf16 v[16:19], v[170:173], v[208:211], v[16:19]
	v_mfma_f32_16x16x32_bf16 v[12:15], v[184:187], v[208:211], v[12:15]
	v_mfma_f32_16x16x32_bf16 v[8:11], v[170:173], v[232:235], v[8:11]
	v_mfma_f32_16x16x32_bf16 v[4:7], v[184:187], v[232:235], v[4:7]
	s_barrier
	s_add_i32 s13, s13, 2
	s_add_u32 s0, s0, 0x100
	s_addc_u32 s1, s1, 0
	s_add_u32 s4, s4, 0x100
	s_addc_u32 s5, s5, 0
	s_cmp_gt_u32 s13, 5
	s_cbranch_scc0 .LBB6_770
	s_and_b64 vcc, exec, s[14:15]
	s_cbranch_vccz .LBB6_773
	s_barrier

.LBB6_1670:
	s_add_i32 s33, 0, 0x10000
	v_add_u32_e32 v2, s33, v177
	ds_read_b128 v[108:111], v2
	ds_read_b128 v[112:115], v2 offset:1024
	ds_read_b128 v[116:119], v2 offset:2048
	ds_read_b128 v[120:123], v2 offset:3072
	s_add_u32 s12, s4, 0x20080
	s_addc_u32 s13, s5, 0
	s_add_i32 s60, s26, 0xc000
	v_lshl_add_u64 v[4:5], s[12:13], 0, v[166:167]
	s_mov_b32 m0, s60
	s_add_i32 s1, s26, 0xe000
	ds_read_b128 v[102:105], v178
	ds_read_b128 v[124:127], v178 offset:1024
	ds_read_b128 v[128:131], v178 offset:2048
	ds_read_b128 v[132:135], v178 offset:3072
	ds_read_b128 v[136:139], v178 offset:4096
	ds_read_b128 v[140:143], v178 offset:5120
	ds_read_b128 v[144:147], v178 offset:6144
	ds_read_b128 v[148:151], v178 offset:7168
	global_load_lds_dwordx4 v[4:5], off
	v_lshl_add_u64 v[4:5], s[12:13], 0, v[170:171]
	s_mov_b32 m0, s1
	s_nop 0
	global_load_lds_dwordx4 v[4:5], off
	s_waitcnt vmcnt(6)
	s_waitcnt lgkmcnt(0)
	s_barrier
	s_waitcnt lgkmcnt(0)
	v_mfma_f32_16x16x32_bf16 v[152:155], v[108:111], v[102:105], 0
	v_mfma_f32_16x16x32_bf16 v[102:105], v[116:119], v[102:105], 0
	v_mfma_f32_16x16x32_bf16 v[152:155], v[112:115], v[124:127], v[152:155]
	v_mfma_f32_16x16x32_bf16 v[124:127], v[120:123], v[124:127], v[102:105]
	v_mfma_f32_16x16x32_bf16 v[102:105], v[108:111], v[128:131], 0
	v_mfma_f32_16x16x32_bf16 v[156:159], v[112:115], v[132:135], v[102:105]
	v_mfma_f32_16x16x32_bf16 v[102:105], v[116:119], v[128:131], 0
	v_mfma_f32_16x16x32_bf16 v[128:131], v[120:123], v[132:135], v[102:105]
	v_mfma_f32_16x16x32_bf16 v[102:105], v[108:111], v[136:139], 0
	v_mfma_f32_16x16x32_bf16 v[132:135], v[112:115], v[140:143], v[102:105]
	v_mfma_f32_16x16x32_bf16 v[102:105], v[116:119], v[136:139], 0
	v_mfma_f32_16x16x32_bf16 v[136:139], v[120:123], v[140:143], v[102:105]
	v_mfma_f32_16x16x32_bf16 v[102:105], v[108:111], v[144:147], 0
	v_mfma_f32_16x16x32_bf16 v[140:143], v[112:115], v[148:151], v[102:105]
	v_mfma_f32_16x16x32_bf16 v[102:105], v[116:119], v[144:147], 0
	v_mfma_f32_16x16x32_bf16 v[144:147], v[120:123], v[148:151], v[102:105]
	s_barrier
	v_lshl_add_u64 v[4:5], s[20:21], 0, v[168:169]
	s_mov_b64 s[64:65], 0x100
	s_add_i32 s33, s33, s7
	s_nop 1
	v_lshl_add_u64 v[102:103], v[4:5], 0, s[64:65]
	s_mov_b32 m0, s33
	ds_read_b128 v[148:151], v178 offset:16384
	ds_read_b128 v[160:163], v178 offset:17408
	ds_read_b128 v[184:187], v178 offset:18432
	ds_read_b128 v[188:191], v178 offset:19456
	ds_read_b128 v[192:195], v178 offset:20480
	ds_read_b128 v[196:199], v178 offset:21504
	ds_read_b128 v[200:203], v178 offset:22528
	ds_read_b128 v[204:207], v178 offset:23552
	global_load_lds_dwordx4 v[102:103], off
	v_lshl_add_u64 v[102:103], s[20:21], 0, v[172:173]
	s_add_i32 s12, s33, 0x2000
	v_lshl_add_u64 v[104:105], v[102:103], 0, s[64:65]
	s_mov_b32 m0, s12
	s_nop 0
	global_load_lds_dwordx4 v[104:105], off
	v_lshl_add_u64 v[104:105], s[4:5], 0, v[166:167]
	v_lshl_add_u64 v[106:107], v[104:105], 0, s[64:65]
	s_mov_b32 m0, s26
	s_nop 0
	global_load_lds_dwordx4 v[106:107], off
	v_lshl_add_u64 v[106:107], s[4:5], 0, v[170:171]
	v_lshl_add_u64 v[164:165], v[106:107], 0, s[64:65]
	s_mov_b32 m0, s27
	s_nop 0
	global_load_lds_dwordx4 v[164:165], off
	s_waitcnt vmcnt(6)
	s_waitcnt lgkmcnt(0)
	s_barrier
	s_waitcnt lgkmcnt(0)
	v_mfma_f32_16x16x32_bf16 v[208:211], v[108:111], v[148:151], 0
	v_mfma_f32_16x16x32_bf16 v[148:151], v[116:119], v[148:151], 0
	v_mfma_f32_16x16x32_bf16 v[208:211], v[112:115], v[160:163], v[208:211]
	v_mfma_f32_16x16x32_bf16 v[148:151], v[120:123], v[160:163], v[148:151]
	v_mfma_f32_16x16x32_bf16 v[160:163], v[108:111], v[184:187], 0
	v_mfma_f32_16x16x32_bf16 v[184:187], v[116:119], v[184:187], 0
	v_mfma_f32_16x16x32_bf16 v[160:163], v[112:115], v[188:191], v[160:163]
	v_mfma_f32_16x16x32_bf16 v[184:187], v[120:123], v[188:191], v[184:187]
	v_mfma_f32_16x16x32_bf16 v[188:191], v[108:111], v[192:195], 0
	v_mfma_f32_16x16x32_bf16 v[108:111], v[108:111], v[200:203], 0
	v_mfma_f32_16x16x32_bf16 v[188:191], v[112:115], v[196:199], v[188:191]
	v_mfma_f32_16x16x32_bf16 v[192:195], v[116:119], v[192:195], 0
	v_mfma_f32_16x16x32_bf16 v[110:113], v[112:115], v[204:207], v[108:111]
	v_mfma_f32_16x16x32_bf16 v[114:117], v[116:119], v[200:203], 0
	v_mfma_f32_16x16x32_bf16 v[114:117], v[120:123], v[204:207], v[114:117]
	v_mfma_f32_16x16x32_bf16 v[192:195], v[120:123], v[196:199], v[192:195]
	s_barrier
	s_add_i32 s13, 0, 0x18000
	v_add_u32_e32 v108, s13, v177
	ds_read_b128 v[118:121], v108
	ds_read_b128 v[196:199], v108 offset:1024
	ds_read_b128 v[200:203], v108 offset:2048
	ds_read_b128 v[204:207], v108 offset:3072
	s_add_u32 s20, s4, 0x20100
	s_addc_u32 s21, s5, 0
	s_mov_b32 m0, s28
	v_lshl_add_u64 v[122:123], s[20:21], 0, v[166:167]
	ds_read_b128 v[216:219], v178 offset:32768
	ds_read_b128 v[228:231], v178 offset:33792
	ds_read_b128 v[232:235], v178 offset:34816
	ds_read_b128 v[236:239], v178 offset:35840
	ds_read_b128 v[240:243], v178 offset:36864
	ds_read_b128 v[244:247], v178 offset:37888
	ds_read_b128 v[248:251], v178 offset:38912
	ds_read_b128 v[220:223], v178 offset:39936
	global_load_lds_dwordx4 v[122:123], off
	v_lshl_add_u64 v[122:123], s[20:21], 0, v[170:171]
	s_mov_b32 m0, s29
	s_nop 0
	global_load_lds_dwordx4 v[122:123], off
	s_waitcnt vmcnt(6)
	s_waitcnt lgkmcnt(0)
	s_barrier
	s_waitcnt lgkmcnt(0)
	v_mfma_f32_16x16x32_bf16 v[152:155], v[118:121], v[216:219], v[152:155]
	v_mfma_f32_16x16x32_bf16 v[122:125], v[200:203], v[216:219], v[124:127]
	v_mfma_f32_16x16x32_bf16 v[156:159], v[118:121], v[232:235], v[156:159]
	v_mfma_f32_16x16x32_bf16 v[126:129], v[200:203], v[232:235], v[128:131]
	v_mfma_f32_16x16x32_bf16 v[130:133], v[118:121], v[240:243], v[132:135]
	v_mfma_f32_16x16x32_bf16 v[134:137], v[200:203], v[240:243], v[136:139]
	v_mfma_f32_16x16x32_bf16 v[138:141], v[118:121], v[248:251], v[140:143]
	v_mfma_f32_16x16x32_bf16 v[142:145], v[200:203], v[248:251], v[144:147]
	v_mfma_f32_16x16x32_bf16 v[152:155], v[196:199], v[228:231], v[152:155]
	v_mfma_f32_16x16x32_bf16 v[122:125], v[204:207], v[228:231], v[122:125]
	v_mfma_f32_16x16x32_bf16 v[156:159], v[196:199], v[236:239], v[156:159]
	v_mfma_f32_16x16x32_bf16 v[126:129], v[204:207], v[236:239], v[126:129]
	v_mfma_f32_16x16x32_bf16 v[130:133], v[196:199], v[244:247], v[130:133]
	v_mfma_f32_16x16x32_bf16 v[134:137], v[204:207], v[244:247], v[134:137]
	v_mfma_f32_16x16x32_bf16 v[138:141], v[196:199], v[220:223], v[138:141]
	v_mfma_f32_16x16x32_bf16 v[142:145], v[204:207], v[220:223], v[142:145]
	s_barrier
	s_mov_b64 s[64:65], 0x180
	s_add_i32 s20, s13, s7
	v_lshl_add_u64 v[146:147], v[4:5], 0, s[64:65]
	s_mov_b32 m0, s20
	s_add_i32 s13, s20, 0x2000
	ds_read_b128 v[216:219], v178 offset:49152
	ds_read_b128 v[220:223], v178 offset:50176
	ds_read_b128 v[228:231], v178 offset:51200
	ds_read_b128 v[232:235], v178 offset:52224
	ds_read_b128 v[236:239], v178 offset:53248
	ds_read_b128 v[240:243], v178 offset:54272
	ds_read_b128 v[244:247], v178 offset:55296
	ds_read_b128 v[248:251], v178 offset:56320
	global_load_lds_dwordx4 v[146:147], off
	v_lshl_add_u64 v[146:147], v[102:103], 0, s[64:65]
	s_mov_b32 m0, s13
	s_nop 0
	global_load_lds_dwordx4 v[146:147], off
	v_lshl_add_u64 v[146:147], v[104:105], 0, s[64:65]
	s_mov_b32 m0, s36
	s_nop 0
	global_load_lds_dwordx4 v[146:147], off
	v_lshl_add_u64 v[146:147], v[106:107], 0, s[64:65]
	s_mov_b32 m0, s48
	s_nop 0
	global_load_lds_dwordx4 v[146:147], off
	s_waitcnt vmcnt(6)
	s_waitcnt lgkmcnt(0)
	s_barrier
	s_waitcnt lgkmcnt(0)
	v_mfma_f32_16x16x32_bf16 v[146:149], v[200:203], v[216:219], v[148:151]
	v_mfma_f32_16x16x32_bf16 v[160:163], v[118:121], v[228:231], v[160:163]
	v_mfma_f32_16x16x32_bf16 v[110:113], v[118:121], v[244:247], v[110:113]
	v_mfma_f32_16x16x32_bf16 v[114:117], v[200:203], v[244:247], v[114:117]
	v_mfma_f32_16x16x32_bf16 v[208:211], v[118:121], v[216:219], v[208:211]
	v_mfma_f32_16x16x32_bf16 v[146:149], v[204:207], v[220:223], v[146:149]
	v_mfma_f32_16x16x32_bf16 v[160:163], v[196:199], v[232:235], v[160:163]
	v_mfma_f32_16x16x32_bf16 v[184:187], v[200:203], v[228:231], v[184:187]
	v_mfma_f32_16x16x32_bf16 v[188:191], v[118:121], v[236:239], v[188:191]
	v_mfma_f32_16x16x32_bf16 v[192:195], v[200:203], v[236:239], v[192:195]
	v_mfma_f32_16x16x32_bf16 v[110:113], v[196:199], v[248:251], v[110:113]
	v_mfma_f32_16x16x32_bf16 v[114:117], v[204:207], v[248:251], v[114:117]
	v_mfma_f32_16x16x32_bf16 v[208:211], v[196:199], v[220:223], v[208:211]
	v_mfma_f32_16x16x32_bf16 v[184:187], v[204:207], v[232:235], v[184:187]
	v_mfma_f32_16x16x32_bf16 v[188:191], v[196:199], v[240:243], v[188:191]
	v_mfma_f32_16x16x32_bf16 v[192:195], v[204:207], v[240:243], v[192:195]
	s_barrier
	ds_read_b128 v[118:121], v2
	ds_read_b128 v[196:199], v2 offset:1024
	ds_read_b128 v[200:203], v2 offset:2048
	ds_read_b128 v[204:207], v2 offset:3072
	s_add_u32 s64, s4, 0x20180
	s_addc_u32 s65, s5, 0
	s_mov_b32 m0, s60
	v_lshl_add_u64 v[150:151], s[64:65], 0, v[166:167]
	ds_read_b128 v[216:219], v178
	ds_read_b128 v[220:223], v178 offset:1024
	ds_read_b128 v[228:231], v178 offset:2048
	ds_read_b128 v[232:235], v178 offset:3072
	ds_read_b128 v[236:239], v178 offset:4096
	ds_read_b128 v[240:243], v178 offset:5120
	ds_read_b128 v[244:247], v178 offset:6144
	ds_read_b128 v[248:251], v178 offset:7168
	global_load_lds_dwordx4 v[150:151], off
	v_lshl_add_u64 v[150:151], s[64:65], 0, v[170:171]
	s_mov_b32 m0, s1
	s_nop 0
	global_load_lds_dwordx4 v[150:151], off
	s_waitcnt vmcnt(6)
	s_waitcnt lgkmcnt(0)
	s_barrier
	s_waitcnt lgkmcnt(0)
	v_mfma_f32_16x16x32_bf16 v[150:153], v[118:121], v[216:219], v[152:155]
	v_mfma_f32_16x16x32_bf16 v[122:125], v[200:203], v[216:219], v[122:125]
	v_mfma_f32_16x16x32_bf16 v[154:157], v[118:121], v[228:231], v[156:159]
	v_mfma_f32_16x16x32_bf16 v[126:129], v[200:203], v[228:231], v[126:129]
	v_mfma_f32_16x16x32_bf16 v[130:133], v[118:121], v[236:239], v[130:133]
	v_mfma_f32_16x16x32_bf16 v[134:137], v[200:203], v[236:239], v[134:137]
	v_mfma_f32_16x16x32_bf16 v[138:141], v[118:121], v[244:247], v[138:141]
	v_mfma_f32_16x16x32_bf16 v[142:145], v[200:203], v[244:247], v[142:145]
	v_mfma_f32_16x16x32_bf16 v[150:153], v[196:199], v[220:223], v[150:153]
	v_mfma_f32_16x16x32_bf16 v[122:125], v[204:207], v[220:223], v[122:125]
	v_mfma_f32_16x16x32_bf16 v[154:157], v[196:199], v[232:235], v[154:157]
	v_mfma_f32_16x16x32_bf16 v[126:129], v[204:207], v[232:235], v[126:129]
	v_mfma_f32_16x16x32_bf16 v[130:133], v[196:199], v[240:243], v[130:133]
	v_mfma_f32_16x16x32_bf16 v[134:137], v[204:207], v[240:243], v[134:137]
	v_mfma_f32_16x16x32_bf16 v[138:141], v[196:199], v[248:251], v[138:141]
	v_mfma_f32_16x16x32_bf16 v[142:145], v[204:207], v[248:251], v[142:145]
	s_barrier
	s_mov_b32 m0, s33
	v_lshl_add_u64 v[158:159], v[4:5], 0, s[88:89]
	ds_read_b128 v[216:219], v178 offset:16384
	ds_read_b128 v[220:223], v178 offset:17408
	ds_read_b128 v[228:231], v178 offset:18432
	ds_read_b128 v[232:235], v178 offset:19456
	ds_read_b128 v[236:239], v178 offset:20480
	ds_read_b128 v[240:243], v178 offset:21504
	ds_read_b128 v[244:247], v178 offset:22528
	ds_read_b128 v[248:251], v178 offset:23552
	global_load_lds_dwordx4 v[158:159], off
	v_lshl_add_u64 v[158:159], v[102:103], 0, s[88:89]
	s_mov_b32 m0, s12
	s_nop 0
	global_load_lds_dwordx4 v[158:159], off
	v_lshl_add_u64 v[158:159], v[104:105], 0, s[88:89]
	s_mov_b32 m0, s26
	s_nop 0
	global_load_lds_dwordx4 v[158:159], off
	v_lshl_add_u64 v[158:159], v[106:107], 0, s[88:89]
	s_mov_b32 m0, s27
	s_nop 0
	global_load_lds_dwordx4 v[158:159], off
	s_waitcnt vmcnt(6)
	s_waitcnt lgkmcnt(0)
	s_barrier
	s_waitcnt lgkmcnt(0)
	v_mfma_f32_16x16x32_bf16 v[146:149], v[200:203], v[216:219], v[146:149]
	v_mfma_f32_16x16x32_bf16 v[158:161], v[118:121], v[228:231], v[160:163]
	v_mfma_f32_16x16x32_bf16 v[162:165], v[200:203], v[228:231], v[184:187]
	v_mfma_f32_16x16x32_bf16 v[110:113], v[118:121], v[244:247], v[110:113]
	v_mfma_f32_16x16x32_bf16 v[114:117], v[200:203], v[244:247], v[114:117]
	v_mfma_f32_16x16x32_bf16 v[208:211], v[118:121], v[216:219], v[208:211]
	v_mfma_f32_16x16x32_bf16 v[146:149], v[204:207], v[220:223], v[146:149]
	v_mfma_f32_16x16x32_bf16 v[158:161], v[196:199], v[232:235], v[158:161]
	v_mfma_f32_16x16x32_bf16 v[162:165], v[204:207], v[232:235], v[162:165]
	v_mfma_f32_16x16x32_bf16 v[184:187], v[118:121], v[236:239], v[188:191]
	v_mfma_f32_16x16x32_bf16 v[188:191], v[200:203], v[236:239], v[192:195]
	v_mfma_f32_16x16x32_bf16 v[110:113], v[196:199], v[248:251], v[110:113]
	v_mfma_f32_16x16x32_bf16 v[114:117], v[204:207], v[248:251], v[114:117]
	v_mfma_f32_16x16x32_bf16 v[208:211], v[196:199], v[220:223], v[208:211]
	v_mfma_f32_16x16x32_bf16 v[184:187], v[196:199], v[240:243], v[184:187]
	v_mfma_f32_16x16x32_bf16 v[188:191], v[204:207], v[240:243], v[188:191]
	s_barrier
	ds_read_b128 v[118:121], v108
	ds_read_b128 v[192:195], v108 offset:1024
	ds_read_b128 v[196:199], v108 offset:2048
	ds_read_b128 v[200:203], v108 offset:3072
	s_add_u32 s64, s4, 0x20200
	s_addc_u32 s65, s5, 0
	s_mov_b32 m0, s28
	v_lshl_add_u64 v[174:175], s[64:65], 0, v[166:167]
	ds_read_b128 v[204:207], v178 offset:32768
	ds_read_b128 v[216:219], v178 offset:33792
	ds_read_b128 v[220:223], v178 offset:34816
	ds_read_b128 v[228:231], v178 offset:35840
	ds_read_b128 v[232:235], v178 offset:36864
	ds_read_b128 v[236:239], v178 offset:37888
	ds_read_b128 v[240:243], v178 offset:38912
	ds_read_b128 v[244:247], v178 offset:39936
	global_load_lds_dwordx4 v[174:175], off
	v_lshl_add_u64 v[174:175], s[64:65], 0, v[170:171]
	s_mov_b32 m0, s29
	s_nop 0
	global_load_lds_dwordx4 v[174:175], off
	s_waitcnt vmcnt(6)
	s_waitcnt lgkmcnt(0)
	s_barrier
	s_waitcnt lgkmcnt(0)
	v_mfma_f32_16x16x32_bf16 v[150:153], v[118:121], v[204:207], v[150:153]
	v_mfma_f32_16x16x32_bf16 v[122:125], v[196:199], v[204:207], v[122:125]
	v_mfma_f32_16x16x32_bf16 v[154:157], v[118:121], v[220:223], v[154:157]
	v_mfma_f32_16x16x32_bf16 v[126:129], v[196:199], v[220:223], v[126:129]
	v_mfma_f32_16x16x32_bf16 v[130:133], v[118:121], v[232:235], v[130:133]
	v_mfma_f32_16x16x32_bf16 v[134:137], v[196:199], v[232:235], v[134:137]
	v_mfma_f32_16x16x32_bf16 v[138:141], v[118:121], v[240:243], v[138:141]
	v_mfma_f32_16x16x32_bf16 v[142:145], v[196:199], v[240:243], v[142:145]
	v_mfma_f32_16x16x32_bf16 v[150:153], v[192:195], v[216:219], v[150:153]
	v_mfma_f32_16x16x32_bf16 v[122:125], v[200:203], v[216:219], v[122:125]
	v_mfma_f32_16x16x32_bf16 v[154:157], v[192:195], v[228:231], v[154:157]
	v_mfma_f32_16x16x32_bf16 v[126:129], v[200:203], v[228:231], v[126:129]
	v_mfma_f32_16x16x32_bf16 v[130:133], v[192:195], v[236:239], v[130:133]
	v_mfma_f32_16x16x32_bf16 v[134:137], v[200:203], v[236:239], v[134:137]
	v_mfma_f32_16x16x32_bf16 v[138:141], v[192:195], v[244:247], v[138:141]
	v_mfma_f32_16x16x32_bf16 v[142:145], v[200:203], v[244:247], v[142:145]
	s_barrier
	s_mov_b64 s[64:65], 0x280
	s_mov_b32 m0, s20
	v_lshl_add_u64 v[174:175], v[4:5], 0, s[64:65]
	ds_read_b128 v[204:207], v178 offset:49152
	ds_read_b128 v[216:219], v178 offset:50176
	ds_read_b128 v[220:223], v178 offset:51200
	ds_read_b128 v[228:231], v178 offset:52224
	ds_read_b128 v[232:235], v178 offset:53248
	ds_read_b128 v[236:239], v178 offset:54272
	ds_read_b128 v[240:243], v178 offset:55296
	ds_read_b128 v[244:247], v178 offset:56320
	global_load_lds_dwordx4 v[174:175], off
	v_lshl_add_u64 v[174:175], v[102:103], 0, s[64:65]
	s_mov_b32 m0, s13
	s_nop 0
	global_load_lds_dwordx4 v[174:175], off
	v_lshl_add_u64 v[174:175], v[104:105], 0, s[64:65]
	s_mov_b32 m0, s36
	s_nop 0
	global_load_lds_dwordx4 v[174:175], off
	v_lshl_add_u64 v[174:175], v[106:107], 0, s[64:65]
	s_mov_b32 m0, s48
	s_nop 0
	global_load_lds_dwordx4 v[174:175], off
	s_waitcnt vmcnt(6)
	s_waitcnt lgkmcnt(0)
	s_barrier
	s_waitcnt lgkmcnt(0)
	v_mfma_f32_16x16x32_bf16 v[146:149], v[196:199], v[204:207], v[146:149]
	v_mfma_f32_16x16x32_bf16 v[158:161], v[118:121], v[220:223], v[158:161]
	v_mfma_f32_16x16x32_bf16 v[162:165], v[196:199], v[220:223], v[162:165]
	v_mfma_f32_16x16x32_bf16 v[110:113], v[118:121], v[240:243], v[110:113]
	v_mfma_f32_16x16x32_bf16 v[114:117], v[196:199], v[240:243], v[114:117]
	v_mfma_f32_16x16x32_bf16 v[208:211], v[118:121], v[204:207], v[208:211]
	v_mfma_f32_16x16x32_bf16 v[146:149], v[200:203], v[216:219], v[146:149]
	v_mfma_f32_16x16x32_bf16 v[158:161], v[192:195], v[228:231], v[158:161]
	v_mfma_f32_16x16x32_bf16 v[162:165], v[200:203], v[228:231], v[162:165]
	v_mfma_f32_16x16x32_bf16 v[184:187], v[118:121], v[232:235], v[184:187]
	v_mfma_f32_16x16x32_bf16 v[188:191], v[196:199], v[232:235], v[188:191]
	v_mfma_f32_16x16x32_bf16 v[110:113], v[192:195], v[244:247], v[110:113]
	v_mfma_f32_16x16x32_bf16 v[114:117], v[200:203], v[244:247], v[114:117]
	v_mfma_f32_16x16x32_bf16 v[208:211], v[192:195], v[216:219], v[208:211]
	v_mfma_f32_16x16x32_bf16 v[184:187], v[192:195], v[236:239], v[184:187]
	v_mfma_f32_16x16x32_bf16 v[188:191], v[200:203], v[236:239], v[188:191]
	s_barrier
	ds_read_b128 v[118:121], v2
	ds_read_b128 v[192:195], v2 offset:1024
	ds_read_b128 v[196:199], v2 offset:2048
	ds_read_b128 v[200:203], v2 offset:3072
	s_add_u32 s64, s4, 0x20280
	s_addc_u32 s65, s5, 0
	s_mov_b32 m0, s60
	v_lshl_add_u64 v[174:175], s[64:65], 0, v[166:167]
	ds_read_b128 v[204:207], v178
	ds_read_b128 v[216:219], v178 offset:1024
	ds_read_b128 v[220:223], v178 offset:2048
	ds_read_b128 v[228:231], v178 offset:3072
	ds_read_b128 v[232:235], v178 offset:4096
	ds_read_b128 v[236:239], v178 offset:5120
	ds_read_b128 v[240:243], v178 offset:6144
	ds_read_b128 v[244:247], v178 offset:7168
	global_load_lds_dwordx4 v[174:175], off
	v_lshl_add_u64 v[174:175], s[64:65], 0, v[170:171]
	s_mov_b32 m0, s1
	s_nop 0
	global_load_lds_dwordx4 v[174:175], off
	s_waitcnt vmcnt(6)
	s_waitcnt lgkmcnt(0)
	s_barrier
	s_waitcnt lgkmcnt(0)
	v_mfma_f32_16x16x32_bf16 v[150:153], v[118:121], v[204:207], v[150:153]
	v_mfma_f32_16x16x32_bf16 v[122:125], v[196:199], v[204:207], v[122:125]
	v_mfma_f32_16x16x32_bf16 v[154:157], v[118:121], v[220:223], v[154:157]
	v_mfma_f32_16x16x32_bf16 v[126:129], v[196:199], v[220:223], v[126:129]
	v_mfma_f32_16x16x32_bf16 v[130:133], v[118:121], v[232:235], v[130:133]
	v_mfma_f32_16x16x32_bf16 v[134:137], v[196:199], v[232:235], v[134:137]
	v_mfma_f32_16x16x32_bf16 v[138:141], v[118:121], v[240:243], v[138:141]
	v_mfma_f32_16x16x32_bf16 v[142:145], v[196:199], v[240:243], v[142:145]
	v_mfma_f32_16x16x32_bf16 v[150:153], v[192:195], v[216:219], v[150:153]
	v_mfma_f32_16x16x32_bf16 v[122:125], v[200:203], v[216:219], v[122:125]
	v_mfma_f32_16x16x32_bf16 v[154:157], v[192:195], v[228:231], v[154:157]
	v_mfma_f32_16x16x32_bf16 v[126:129], v[200:203], v[228:231], v[126:129]
	v_mfma_f32_16x16x32_bf16 v[130:133], v[192:195], v[236:239], v[130:133]
	v_mfma_f32_16x16x32_bf16 v[134:137], v[200:203], v[236:239], v[134:137]
	v_mfma_f32_16x16x32_bf16 v[138:141], v[192:195], v[244:247], v[138:141]
	v_mfma_f32_16x16x32_bf16 v[142:145], v[200:203], v[244:247], v[142:145]
	s_barrier
	s_mov_b64 s[64:65], 0x300
	s_mov_b32 m0, s33
	v_lshl_add_u64 v[174:175], v[4:5], 0, s[64:65]
	ds_read_b128 v[204:207], v178 offset:16384
	ds_read_b128 v[216:219], v178 offset:17408
	ds_read_b128 v[220:223], v178 offset:18432
	ds_read_b128 v[228:231], v178 offset:19456
	ds_read_b128 v[232:235], v178 offset:20480
	ds_read_b128 v[236:239], v178 offset:21504
	ds_read_b128 v[240:243], v178 offset:22528
	ds_read_b128 v[244:247], v178 offset:23552
	global_load_lds_dwordx4 v[174:175], off
	v_lshl_add_u64 v[174:175], v[102:103], 0, s[64:65]
	s_mov_b32 m0, s12
	s_nop 0
	global_load_lds_dwordx4 v[174:175], off
	v_lshl_add_u64 v[174:175], v[104:105], 0, s[64:65]
	s_mov_b32 m0, s26
	s_nop 0
	global_load_lds_dwordx4 v[174:175], off
	v_lshl_add_u64 v[174:175], v[106:107], 0, s[64:65]
	s_mov_b32 m0, s27
	s_nop 0
	global_load_lds_dwordx4 v[174:175], off
	s_waitcnt vmcnt(6)
	s_waitcnt lgkmcnt(0)
	s_barrier
	s_waitcnt lgkmcnt(0)
	v_mfma_f32_16x16x32_bf16 v[146:149], v[196:199], v[204:207], v[146:149]
	v_mfma_f32_16x16x32_bf16 v[158:161], v[118:121], v[220:223], v[158:161]
	v_mfma_f32_16x16x32_bf16 v[162:165], v[196:199], v[220:223], v[162:165]
	v_mfma_f32_16x16x32_bf16 v[110:113], v[118:121], v[240:243], v[110:113]
	v_mfma_f32_16x16x32_bf16 v[114:117], v[196:199], v[240:243], v[114:117]
	v_mfma_f32_16x16x32_bf16 v[208:211], v[118:121], v[204:207], v[208:211]
	v_mfma_f32_16x16x32_bf16 v[146:149], v[200:203], v[216:219], v[146:149]
	v_mfma_f32_16x16x32_bf16 v[158:161], v[192:195], v[228:231], v[158:161]
	v_mfma_f32_16x16x32_bf16 v[162:165], v[200:203], v[228:231], v[162:165]
	v_mfma_f32_16x16x32_bf16 v[184:187], v[118:121], v[232:235], v[184:187]
	v_mfma_f32_16x16x32_bf16 v[188:191], v[196:199], v[232:235], v[188:191]
	v_mfma_f32_16x16x32_bf16 v[110:113], v[192:195], v[244:247], v[110:113]
	v_mfma_f32_16x16x32_bf16 v[114:117], v[200:203], v[244:247], v[114:117]
	v_mfma_f32_16x16x32_bf16 v[208:211], v[192:195], v[216:219], v[208:211]
	v_mfma_f32_16x16x32_bf16 v[184:187], v[192:195], v[236:239], v[184:187]
	v_mfma_f32_16x16x32_bf16 v[188:191], v[200:203], v[236:239], v[188:191]
	s_barrier
	ds_read_b128 v[118:121], v108
	ds_read_b128 v[192:195], v108 offset:1024
	ds_read_b128 v[196:199], v108 offset:2048
	ds_read_b128 v[200:203], v108 offset:3072
	s_add_u32 s64, s4, 0x20300
	s_addc_u32 s65, s5, 0
	s_mov_b32 m0, s28
	v_lshl_add_u64 v[174:175], s[64:65], 0, v[166:167]
	ds_read_b128 v[204:207], v178 offset:32768
	ds_read_b128 v[216:219], v178 offset:33792
	ds_read_b128 v[220:223], v178 offset:34816
	ds_read_b128 v[228:231], v178 offset:35840
	ds_read_b128 v[232:235], v178 offset:36864
	ds_read_b128 v[236:239], v178 offset:37888
	ds_read_b128 v[240:243], v178 offset:38912
	ds_read_b128 v[244:247], v178 offset:39936
	global_load_lds_dwordx4 v[174:175], off
	v_lshl_add_u64 v[174:175], s[64:65], 0, v[170:171]
	s_mov_b32 m0, s29
	s_nop 0
	global_load_lds_dwordx4 v[174:175], off
	s_waitcnt vmcnt(6)
	s_waitcnt lgkmcnt(0)
	s_barrier
	s_waitcnt lgkmcnt(0)
	v_mfma_f32_16x16x32_bf16 v[150:153], v[118:121], v[204:207], v[150:153]
	v_mfma_f32_16x16x32_bf16 v[122:125], v[196:199], v[204:207], v[122:125]
	v_mfma_f32_16x16x32_bf16 v[154:157], v[118:121], v[220:223], v[154:157]
	v_mfma_f32_16x16x32_bf16 v[126:129], v[196:199], v[220:223], v[126:129]
	v_mfma_f32_16x16x32_bf16 v[130:133], v[118:121], v[232:235], v[130:133]
	v_mfma_f32_16x16x32_bf16 v[134:137], v[196:199], v[232:235], v[134:137]
	v_mfma_f32_16x16x32_bf16 v[138:141], v[118:121], v[240:243], v[138:141]
	v_mfma_f32_16x16x32_bf16 v[142:145], v[196:199], v[240:243], v[142:145]
	v_mfma_f32_16x16x32_bf16 v[150:153], v[192:195], v[216:219], v[150:153]
	v_mfma_f32_16x16x32_bf16 v[122:125], v[200:203], v[216:219], v[122:125]
	v_mfma_f32_16x16x32_bf16 v[154:157], v[192:195], v[228:231], v[154:157]
	v_mfma_f32_16x16x32_bf16 v[126:129], v[200:203], v[228:231], v[126:129]
	v_mfma_f32_16x16x32_bf16 v[130:133], v[192:195], v[236:239], v[130:133]
	v_mfma_f32_16x16x32_bf16 v[134:137], v[200:203], v[236:239], v[134:137]
	v_mfma_f32_16x16x32_bf16 v[138:141], v[192:195], v[244:247], v[138:141]
	v_mfma_f32_16x16x32_bf16 v[142:145], v[200:203], v[244:247], v[142:145]
	s_barrier
	s_mov_b64 s[64:65], 0x380
	s_mov_b32 m0, s20
	v_lshl_add_u64 v[4:5], v[4:5], 0, s[64:65]
	ds_read_b128 v[204:207], v178 offset:49152
	ds_read_b128 v[216:219], v178 offset:50176
	ds_read_b128 v[220:223], v178 offset:51200
	ds_read_b128 v[228:231], v178 offset:52224
	ds_read_b128 v[232:235], v178 offset:53248
	ds_read_b128 v[236:239], v178 offset:54272
	ds_read_b128 v[240:243], v178 offset:55296
	ds_read_b128 v[244:247], v178 offset:56320
	global_load_lds_dwordx4 v[4:5], off
	v_lshl_add_u64 v[4:5], v[102:103], 0, s[64:65]
	s_mov_b32 m0, s13
	s_nop 0
	global_load_lds_dwordx4 v[4:5], off
	v_lshl_add_u64 v[4:5], v[104:105], 0, s[64:65]
	s_mov_b32 m0, s36
	s_nop 0
	global_load_lds_dwordx4 v[4:5], off
	v_lshl_add_u64 v[4:5], v[106:107], 0, s[64:65]
	s_mov_b32 m0, s48
	s_nop 0
	global_load_lds_dwordx4 v[4:5], off
	s_waitcnt vmcnt(6)
	s_waitcnt lgkmcnt(0)
	s_barrier
	s_waitcnt lgkmcnt(0)
	v_mfma_f32_16x16x32_bf16 v[102:105], v[118:121], v[204:207], v[208:211]
	v_mfma_f32_16x16x32_bf16 v[146:149], v[196:199], v[204:207], v[146:149]
	v_mfma_f32_16x16x32_bf16 v[158:161], v[118:121], v[220:223], v[158:161]
	v_mfma_f32_16x16x32_bf16 v[162:165], v[196:199], v[220:223], v[162:165]
	v_mfma_f32_16x16x32_bf16 v[110:113], v[118:121], v[240:243], v[110:113]
	v_mfma_f32_16x16x32_bf16 v[114:117], v[196:199], v[240:243], v[114:117]
	v_mfma_f32_16x16x32_bf16 v[102:105], v[192:195], v[216:219], v[102:105]
	v_mfma_f32_16x16x32_bf16 v[146:149], v[200:203], v[216:219], v[146:149]
	v_mfma_f32_16x16x32_bf16 v[158:161], v[192:195], v[228:231], v[158:161]
	v_mfma_f32_16x16x32_bf16 v[162:165], v[200:203], v[228:231], v[162:165]
	v_mfma_f32_16x16x32_bf16 v[184:187], v[118:121], v[232:235], v[184:187]
	v_mfma_f32_16x16x32_bf16 v[188:191], v[196:199], v[232:235], v[188:191]
	v_mfma_f32_16x16x32_bf16 v[110:113], v[192:195], v[244:247], v[110:113]
	v_mfma_f32_16x16x32_bf16 v[114:117], v[200:203], v[244:247], v[114:117]
	v_mfma_f32_16x16x32_bf16 v[184:187], v[192:195], v[236:239], v[184:187]
	v_mfma_f32_16x16x32_bf16 v[188:191], v[200:203], v[236:239], v[188:191]
	s_barrier
	ds_read_b128 v[118:121], v2
	ds_read_b128 v[192:195], v2 offset:1024
	ds_read_b128 v[196:199], v2 offset:2048
	ds_read_b128 v[200:203], v2 offset:3072
	s_add_u32 s4, s4, 0x20380
	s_addc_u32 s5, s5, 0
	s_mov_b32 m0, s60
	v_lshl_add_u64 v[4:5], s[4:5], 0, v[166:167]
	ds_read_b128 v[204:207], v178
	ds_read_b128 v[208:211], v178 offset:1024
	ds_read_b128 v[216:219], v178 offset:2048
	ds_read_b128 v[220:223], v178 offset:3072
	ds_read_b128 v[228:231], v178 offset:4096
	ds_read_b128 v[232:235], v178 offset:5120
	ds_read_b128 v[236:239], v178 offset:6144
	ds_read_b128 v[240:243], v178 offset:7168
	global_load_lds_dwordx4 v[4:5], off
	v_lshl_add_u64 v[4:5], s[4:5], 0, v[170:171]
	s_mov_b32 m0, s1
	s_nop 0
	global_load_lds_dwordx4 v[4:5], off
	s_waitcnt vmcnt(6)
	s_waitcnt lgkmcnt(0)
	s_barrier
	s_waitcnt lgkmcnt(0)
	v_mfma_f32_16x16x32_bf16 v[150:153], v[118:121], v[204:207], v[150:153]
	v_mfma_f32_16x16x32_bf16 v[122:125], v[196:199], v[204:207], v[122:125]
	v_mfma_f32_16x16x32_bf16 v[154:157], v[118:121], v[216:219], v[154:157]
	v_mfma_f32_16x16x32_bf16 v[126:129], v[196:199], v[216:219], v[126:129]
	v_mfma_f32_16x16x32_bf16 v[130:133], v[118:121], v[228:231], v[130:133]
	v_mfma_f32_16x16x32_bf16 v[134:137], v[196:199], v[228:231], v[134:137]
	v_mfma_f32_16x16x32_bf16 v[138:141], v[118:121], v[236:239], v[138:141]
	v_mfma_f32_16x16x32_bf16 v[150:153], v[192:195], v[208:211], v[150:153]
	v_mfma_f32_16x16x32_bf16 v[122:125], v[200:203], v[208:211], v[122:125]
	v_mfma_f32_16x16x32_bf16 v[154:157], v[192:195], v[220:223], v[154:157]
	v_mfma_f32_16x16x32_bf16 v[126:129], v[200:203], v[220:223], v[126:129]
	v_mfma_f32_16x16x32_bf16 v[130:133], v[192:195], v[232:235], v[130:133]
	v_mfma_f32_16x16x32_bf16 v[134:137], v[200:203], v[232:235], v[134:137]
	v_mfma_f32_16x16x32_bf16 v[138:141], v[192:195], v[240:243], v[138:141]
	v_mfma_f32_16x16x32_bf16 v[142:145], v[196:199], v[236:239], v[142:145]
	v_mfma_f32_16x16x32_bf16 v[204:207], v[200:203], v[240:243], v[142:145]
	s_barrier
	s_mov_b32 m0, s33
	v_lshl_add_u64 v[4:5], s[18:19], 0, v[168:169]
	s_nop 2
	ds_read_b128 v[142:145], v178 offset:16384
	ds_read_b128 v[208:211], v178 offset:17408
	ds_read_b128 v[216:219], v178 offset:18432
	ds_read_b128 v[220:223], v178 offset:19456
	ds_read_b128 v[228:231], v178 offset:20480
	ds_read_b128 v[232:235], v178 offset:21504
	ds_read_b128 v[236:239], v178 offset:22528
	ds_read_b128 v[240:243], v178 offset:23552
	global_load_lds_dwordx4 v[4:5], off
	v_lshl_add_u64 v[174:175], s[18:19], 0, v[172:173]
	s_mov_b32 m0, s12
	v_lshl_add_u64 v[252:253], s[16:17], 0, v[166:167]
	global_load_lds_dwordx4 v[174:175], off
	s_mov_b32 m0, s26
	v_lshl_add_u64 v[224:225], s[16:17], 0, v[170:171]
	global_load_lds_dwordx4 v[252:253], off
	s_mov_b32 m0, s27
	s_nop 0
	global_load_lds_dwordx4 v[224:225], off
	s_waitcnt vmcnt(6)
	s_waitcnt lgkmcnt(0)
	s_barrier
	s_waitcnt lgkmcnt(0)
	v_mfma_f32_16x16x32_bf16 v[102:105], v[118:121], v[142:145], v[102:105]
	v_mfma_f32_16x16x32_bf16 v[142:145], v[196:199], v[142:145], v[146:149]
	v_mfma_f32_16x16x32_bf16 v[102:105], v[192:195], v[208:211], v[102:105]
	v_mfma_f32_16x16x32_bf16 v[208:211], v[200:203], v[208:211], v[142:145]
	v_mfma_f32_16x16x32_bf16 v[142:145], v[118:121], v[216:219], v[158:161]
	v_mfma_f32_16x16x32_bf16 v[244:247], v[192:195], v[220:223], v[142:145]
	v_mfma_f32_16x16x32_bf16 v[142:145], v[196:199], v[216:219], v[162:165]
	v_mfma_f32_16x16x32_bf16 v[216:219], v[200:203], v[220:223], v[142:145]
	v_mfma_f32_16x16x32_bf16 v[142:145], v[118:121], v[228:231], v[184:187]
	v_mfma_f32_16x16x32_bf16 v[110:113], v[118:121], v[236:239], v[110:113]
	v_mfma_f32_16x16x32_bf16 v[184:187], v[192:195], v[232:235], v[142:145]
	v_mfma_f32_16x16x32_bf16 v[142:145], v[196:199], v[228:231], v[188:191]
	v_mfma_f32_16x16x32_bf16 v[192:195], v[192:195], v[240:243], v[110:113]
	v_mfma_f32_16x16x32_bf16 v[110:113], v[196:199], v[236:239], v[114:117]
	v_mfma_f32_16x16x32_bf16 v[188:191], v[200:203], v[232:235], v[142:145]
	v_mfma_f32_16x16x32_bf16 v[196:199], v[200:203], v[240:243], v[110:113]
	s_barrier
	ds_read_b128 v[200:203], v108
	ds_read_b128 v[220:223], v108 offset:1024
	ds_read_b128 v[228:231], v108 offset:2048
	ds_read_b128 v[232:235], v108 offset:3072
	s_add_u32 s4, s16, 0x20000
	s_addc_u32 s5, s17, 0
	s_mov_b32 m0, s28
	v_lshl_add_u64 v[146:147], s[4:5], 0, v[166:167]
	ds_read_b128 v[106:109], v178 offset:32768
	ds_read_b128 v[110:113], v178 offset:33792
	ds_read_b128 v[114:117], v178 offset:34816
	ds_read_b128 v[118:121], v178 offset:35840
	ds_read_b128 v[142:145], v178 offset:36864
	ds_read_b128 v[236:239], v178 offset:37888
	ds_read_b128 v[240:243], v178 offset:38912
	ds_read_b128 v[248:251], v178 offset:39936
	global_load_lds_dwordx4 v[146:147], off
	v_lshl_add_u64 v[146:147], s[4:5], 0, v[170:171]
	s_mov_b32 m0, s29
	s_nop 0
	global_load_lds_dwordx4 v[146:147], off
	s_waitcnt vmcnt(6)
	s_waitcnt lgkmcnt(0)
	s_barrier
	s_waitcnt lgkmcnt(0)
	v_mfma_f32_16x16x32_bf16 v[146:149], v[200:203], v[106:109], v[150:153]
	v_mfma_f32_16x16x32_bf16 v[106:109], v[228:231], v[106:109], v[122:125]
	v_mfma_f32_16x16x32_bf16 v[158:161], v[232:235], v[110:113], v[106:109]
	v_mfma_f32_16x16x32_bf16 v[106:109], v[200:203], v[114:117], v[154:157]
	v_mfma_f32_16x16x32_bf16 v[154:157], v[220:223], v[118:121], v[106:109]
	v_mfma_f32_16x16x32_bf16 v[106:109], v[228:231], v[114:117], v[126:129]
	v_mfma_f32_16x16x32_bf16 v[150:153], v[232:235], v[118:121], v[106:109]
	v_mfma_f32_16x16x32_bf16 v[106:109], v[200:203], v[142:145], v[130:133]
	v_mfma_f32_16x16x32_bf16 v[162:165], v[220:223], v[110:113], v[146:149]
	v_mfma_f32_16x16x32_bf16 v[146:149], v[220:223], v[236:239], v[106:109]
	v_mfma_f32_16x16x32_bf16 v[106:109], v[228:231], v[142:145], v[134:137]
	v_mfma_f32_16x16x32_bf16 v[142:145], v[232:235], v[236:239], v[106:109]
	v_mfma_f32_16x16x32_bf16 v[106:109], v[200:203], v[240:243], v[138:141]
	v_mfma_f32_16x16x32_bf16 v[138:141], v[220:223], v[248:251], v[106:109]
	v_mfma_f32_16x16x32_bf16 v[106:109], v[228:231], v[240:243], v[204:207]
	v_mfma_f32_16x16x32_bf16 v[130:133], v[232:235], v[248:251], v[106:109]
	s_barrier
	s_mov_b32 m0, s20
	v_lshl_add_u64 v[4:5], v[4:5], 0, s[86:87]
	s_nop 2
	ds_read_b128 v[106:109], v178 offset:49152
	ds_read_b128 v[110:113], v178 offset:50176
	ds_read_b128 v[114:117], v178 offset:51200
	ds_read_b128 v[118:121], v178 offset:52224
	ds_read_b128 v[204:207], v178 offset:53248
	ds_read_b128 v[236:239], v178 offset:54272
	ds_read_b128 v[240:243], v178 offset:55296
	ds_read_b128 v[248:251], v178 offset:56320
	global_load_lds_dwordx4 v[4:5], off
	v_lshl_add_u64 v[4:5], v[174:175], 0, s[86:87]
	s_mov_b32 m0, s13
	s_nop 0
	global_load_lds_dwordx4 v[4:5], off
	v_lshl_add_u64 v[4:5], v[252:253], 0, s[86:87]
	s_mov_b32 m0, s36
	s_nop 0
	global_load_lds_dwordx4 v[4:5], off
	v_lshl_add_u64 v[4:5], v[224:225], 0, s[86:87]
	s_mov_b32 m0, s48
	s_nop 0
	global_load_lds_dwordx4 v[4:5], off
	s_waitcnt vmcnt(6)
	s_waitcnt lgkmcnt(0)
	s_barrier
	s_waitcnt lgkmcnt(0)
	v_mfma_f32_16x16x32_bf16 v[102:105], v[200:203], v[106:109], v[102:105]
	v_mfma_f32_16x16x32_bf16 v[134:137], v[220:223], v[110:113], v[102:105]
	v_mfma_f32_16x16x32_bf16 v[102:105], v[228:231], v[106:109], v[208:211]
	v_mfma_f32_16x16x32_bf16 v[126:129], v[232:235], v[110:113], v[102:105]
	v_mfma_f32_16x16x32_bf16 v[102:105], v[200:203], v[114:117], v[244:247]
	v_mfma_f32_16x16x32_bf16 v[122:125], v[220:223], v[118:121], v[102:105]
	v_mfma_f32_16x16x32_bf16 v[102:105], v[228:231], v[114:117], v[216:219]
	v_mfma_f32_16x16x32_bf16 v[118:121], v[232:235], v[118:121], v[102:105]
	v_mfma_f32_16x16x32_bf16 v[102:105], v[200:203], v[204:207], v[184:187]
	v_mfma_f32_16x16x32_bf16 v[114:117], v[220:223], v[236:239], v[102:105]
	v_mfma_f32_16x16x32_bf16 v[102:105], v[228:231], v[204:207], v[188:191]
	v_mfma_f32_16x16x32_bf16 v[110:113], v[232:235], v[236:239], v[102:105]
	v_mfma_f32_16x16x32_bf16 v[102:105], v[200:203], v[240:243], v[192:195]
	v_mfma_f32_16x16x32_bf16 v[106:109], v[220:223], v[248:251], v[102:105]
	v_mfma_f32_16x16x32_bf16 v[102:105], v[228:231], v[240:243], v[196:199]
	v_mfma_f32_16x16x32_bf16 v[102:105], v[232:235], v[248:251], v[102:105]
	s_barrier
	s_andn2_b64 vcc, exec, s[8:9]
	s_cbranch_vccnz .LBB6_1672
	s_barrier

.LBB6_1775:
	s_add_u32 s24, s22, 0x100
	s_addc_u32 s25, s23, 0
	s_add_i32 s13, 0, 0x10000
	s_cmp_eq_u32 s12, 28
	s_cselect_b32 s29, s17, s25
	s_cselect_b32 s28, s16, s24
	s_cselect_b32 s27, s19, s11
	s_cselect_b32 s26, s18, s0
	s_add_i32 s21, 0, 0x14000
	v_add_u32_e32 v150, s13, v159
	v_add_u32_e32 v170, s21, v159
	ds_read_b128 v[132:135], v150
	ds_read_b128 v[136:139], v150 offset:1024
	ds_read_b128 v[140:143], v150 offset:2048
	ds_read_b128 v[150:153], v150 offset:3072
	ds_read_b128 v[154:157], v170
	ds_read_b128 v[162:165], v170 offset:1024
	ds_read_b128 v[166:169], v170 offset:2048
	ds_read_b128 v[170:173], v170 offset:3072
	v_lshl_add_u64 v[178:179], s[22:23], 0, v[148:149]
	s_add_i32 m0, s48, 0xc000
	ds_read_b128 v[174:177], v161
	ds_read_b128 v[182:185], v161 offset:1024
	ds_read_b128 v[186:189], v161 offset:2048
	ds_read_b128 v[190:193], v161 offset:3072
	ds_read_b128 v[194:197], v161 offset:4096
	ds_read_b128 v[198:201], v161 offset:5120
	ds_read_b128 v[202:205], v161 offset:6144
	ds_read_b128 v[206:209], v161 offset:7168
	global_load_lds_dwordx4 v[178:179], off
	v_lshl_add_u64 v[178:179], s[22:23], 0, v[146:147]
	s_add_i32 m0, s48, 0xe000
	s_nop 0
	global_load_lds_dwordx4 v[178:179], off
	s_waitcnt vmcnt(8)
	s_waitcnt lgkmcnt(0)
	s_barrier
	s_waitcnt lgkmcnt(0)
	v_mfma_f32_16x16x32_bf16 v[128:131], v[132:135], v[174:177], v[128:131]
	v_mfma_f32_16x16x32_bf16 v[124:127], v[140:143], v[174:177], v[124:127]
	v_mfma_f32_16x16x32_bf16 v[120:123], v[132:135], v[186:189], v[120:123]
	v_mfma_f32_16x16x32_bf16 v[108:111], v[140:143], v[186:189], v[108:111]
	v_mfma_f32_16x16x32_bf16 v[104:107], v[132:135], v[194:197], v[104:107]
	v_mfma_f32_16x16x32_bf16 v[92:95], v[140:143], v[194:197], v[92:95]
	v_mfma_f32_16x16x32_bf16 v[88:91], v[132:135], v[202:205], v[88:91]
	v_mfma_f32_16x16x32_bf16 v[76:79], v[140:143], v[202:205], v[76:79]
	v_mfma_f32_16x16x32_bf16 v[128:131], v[136:139], v[182:185], v[128:131]
	v_mfma_f32_16x16x32_bf16 v[124:127], v[150:153], v[182:185], v[124:127]
	v_mfma_f32_16x16x32_bf16 v[120:123], v[136:139], v[190:193], v[120:123]
	v_mfma_f32_16x16x32_bf16 v[108:111], v[150:153], v[190:193], v[108:111]
	v_mfma_f32_16x16x32_bf16 v[104:107], v[136:139], v[198:201], v[104:107]
	v_mfma_f32_16x16x32_bf16 v[92:95], v[150:153], v[198:201], v[92:95]
	v_mfma_f32_16x16x32_bf16 v[88:91], v[136:139], v[206:209], v[88:91]
	v_mfma_f32_16x16x32_bf16 v[76:79], v[150:153], v[206:209], v[76:79]
	v_mfma_f32_16x16x32_bf16 v[116:119], v[154:157], v[174:177], v[116:119]
	v_mfma_f32_16x16x32_bf16 v[112:115], v[166:169], v[174:177], v[112:115]
	v_mfma_f32_16x16x32_bf16 v[100:103], v[154:157], v[186:189], v[100:103]
	v_mfma_f32_16x16x32_bf16 v[96:99], v[166:169], v[186:189], v[96:99]
	v_mfma_f32_16x16x32_bf16 v[84:87], v[154:157], v[194:197], v[84:87]
	v_mfma_f32_16x16x32_bf16 v[80:83], v[166:169], v[194:197], v[80:83]
	v_mfma_f32_16x16x32_bf16 v[72:75], v[154:157], v[202:205], v[72:75]
	v_mfma_f32_16x16x32_bf16 v[68:71], v[166:169], v[202:205], v[68:71]
	v_mfma_f32_16x16x32_bf16 v[116:119], v[162:165], v[182:185], v[116:119]
	v_mfma_f32_16x16x32_bf16 v[112:115], v[170:173], v[182:185], v[112:115]
	v_mfma_f32_16x16x32_bf16 v[100:103], v[162:165], v[190:193], v[100:103]
	v_mfma_f32_16x16x32_bf16 v[96:99], v[170:173], v[190:193], v[96:99]
	v_mfma_f32_16x16x32_bf16 v[84:87], v[162:165], v[198:201], v[84:87]
	v_mfma_f32_16x16x32_bf16 v[80:83], v[170:173], v[198:201], v[80:83]
	v_mfma_f32_16x16x32_bf16 v[72:75], v[162:165], v[206:209], v[72:75]
	v_mfma_f32_16x16x32_bf16 v[68:71], v[170:173], v[206:209], v[68:71]
	s_barrier
	s_add_i32 s13, s13, s47
	v_lshl_add_u64 v[178:179], s[26:27], 0, v[2:3]
	s_mov_b32 m0, s13
	ds_read_b128 v[174:177], v161 offset:16384
	ds_read_b128 v[182:185], v161 offset:17408
	ds_read_b128 v[186:189], v161 offset:18432
	ds_read_b128 v[190:193], v161 offset:19456
	ds_read_b128 v[194:197], v161 offset:20480
	ds_read_b128 v[198:201], v161 offset:21504
	ds_read_b128 v[202:205], v161 offset:22528
	ds_read_b128 v[206:209], v161 offset:23552
	global_load_lds_dwordx4 v[178:179], off
	s_add_i32 m0, s13, 0x2000
	s_add_u32 s22, s26, 0x80000
	v_lshl_add_u64 v[210:211], s[26:27], 0, v[144:145]
	s_addc_u32 s23, s27, 0
	s_add_i32 s13, s21, s47
	global_load_lds_dwordx4 v[210:211], off
	v_lshl_add_u64 v[216:217], s[22:23], 0, v[2:3]
	s_mov_b32 m0, s13
	v_lshl_add_u64 v[218:219], s[28:29], 0, v[144:145]
	global_load_lds_dwordx4 v[216:217], off
	v_lshl_add_u64 v[216:217], s[22:23], 0, v[144:145]
	s_add_i32 m0, s13, 0x2000
	s_nop 0
	global_load_lds_dwordx4 v[216:217], off
	v_lshl_add_u64 v[216:217], s[28:29], 0, v[2:3]
	s_mov_b32 m0, s48
	s_nop 0
	global_load_lds_dwordx4 v[216:217], off
	s_mov_b32 m0, s49
	s_nop 0
	global_load_lds_dwordx4 v[218:219], off
	s_waitcnt vmcnt(8)
	s_waitcnt lgkmcnt(0)
	s_barrier
	s_waitcnt lgkmcnt(0)
	v_mfma_f32_16x16x32_bf16 v[64:67], v[132:135], v[174:177], v[64:67]
	v_mfma_f32_16x16x32_bf16 v[60:63], v[140:143], v[174:177], v[60:63]
	v_mfma_f32_16x16x32_bf16 v[56:59], v[132:135], v[186:189], v[56:59]
	v_mfma_f32_16x16x32_bf16 v[44:47], v[140:143], v[186:189], v[44:47]
	v_mfma_f32_16x16x32_bf16 v[40:43], v[132:135], v[194:197], v[40:43]
	v_mfma_f32_16x16x32_bf16 v[28:31], v[140:143], v[194:197], v[28:31]
	v_mfma_f32_16x16x32_bf16 v[24:27], v[132:135], v[202:205], v[24:27]
	v_mfma_f32_16x16x32_bf16 v[12:15], v[140:143], v[202:205], v[12:15]
	v_mfma_f32_16x16x32_bf16 v[64:67], v[136:139], v[182:185], v[64:67]
	v_mfma_f32_16x16x32_bf16 v[60:63], v[150:153], v[182:185], v[60:63]
	v_mfma_f32_16x16x32_bf16 v[56:59], v[136:139], v[190:193], v[56:59]
	v_mfma_f32_16x16x32_bf16 v[44:47], v[150:153], v[190:193], v[44:47]
	v_mfma_f32_16x16x32_bf16 v[40:43], v[136:139], v[198:201], v[40:43]
	v_mfma_f32_16x16x32_bf16 v[28:31], v[150:153], v[198:201], v[28:31]
	v_mfma_f32_16x16x32_bf16 v[24:27], v[136:139], v[206:209], v[24:27]
	v_mfma_f32_16x16x32_bf16 v[12:15], v[150:153], v[206:209], v[12:15]
	v_mfma_f32_16x16x32_bf16 v[52:55], v[154:157], v[174:177], v[52:55]
	v_mfma_f32_16x16x32_bf16 v[48:51], v[166:169], v[174:177], v[48:51]
	v_mfma_f32_16x16x32_bf16 v[36:39], v[154:157], v[186:189], v[36:39]
	v_mfma_f32_16x16x32_bf16 v[32:35], v[166:169], v[186:189], v[32:35]
	v_mfma_f32_16x16x32_bf16 v[20:23], v[154:157], v[194:197], v[20:23]
	v_mfma_f32_16x16x32_bf16 v[16:19], v[166:169], v[194:197], v[16:19]
	v_mfma_f32_16x16x32_bf16 v[8:11], v[154:157], v[202:205], v[8:11]
	v_mfma_f32_16x16x32_bf16 v[4:7], v[166:169], v[202:205], v[4:7]
	v_mfma_f32_16x16x32_bf16 v[52:55], v[162:165], v[182:185], v[52:55]
	v_mfma_f32_16x16x32_bf16 v[48:51], v[170:173], v[182:185], v[48:51]
	v_mfma_f32_16x16x32_bf16 v[36:39], v[162:165], v[190:193], v[36:39]
	v_mfma_f32_16x16x32_bf16 v[32:35], v[170:173], v[190:193], v[32:35]
	v_mfma_f32_16x16x32_bf16 v[20:23], v[162:165], v[198:201], v[20:23]
	v_mfma_f32_16x16x32_bf16 v[16:19], v[170:173], v[198:201], v[16:19]
	v_mfma_f32_16x16x32_bf16 v[8:11], v[162:165], v[206:209], v[8:11]
	v_mfma_f32_16x16x32_bf16 v[4:7], v[170:173], v[206:209], v[4:7]
	s_barrier
	s_add_i32 s13, 0, 0x18000
	s_add_i32 s21, 0, 0x1c000
	v_add_u32_e32 v150, s13, v159
	v_add_u32_e32 v170, s21, v159
	ds_read_b128 v[132:135], v150
	ds_read_b128 v[136:139], v150 offset:1024
	ds_read_b128 v[140:143], v150 offset:2048
	ds_read_b128 v[150:153], v150 offset:3072
	ds_read_b128 v[154:157], v170
	ds_read_b128 v[162:165], v170 offset:1024
	ds_read_b128 v[166:169], v170 offset:2048
	ds_read_b128 v[170:173], v170 offset:3072
	s_add_u32 s22, s28, 0x80000
	s_addc_u32 s23, s29, 0
	s_mov_b32 m0, s50
	v_lshl_add_u64 v[220:221], s[22:23], 0, v[2:3]
	ds_read_b128 v[174:177], v161 offset:32768
	ds_read_b128 v[182:185], v161 offset:33792
	ds_read_b128 v[186:189], v161 offset:34816
	ds_read_b128 v[190:193], v161 offset:35840
	ds_read_b128 v[194:197], v161 offset:36864
	ds_read_b128 v[198:201], v161 offset:37888
	ds_read_b128 v[202:205], v161 offset:38912
	ds_read_b128 v[206:209], v161 offset:39936
	global_load_lds_dwordx4 v[220:221], off
	v_lshl_add_u64 v[220:221], s[22:23], 0, v[144:145]
	s_mov_b32 m0, s51
	s_nop 0
	global_load_lds_dwordx4 v[220:221], off
	s_waitcnt vmcnt(8)
	s_waitcnt lgkmcnt(0)
	s_barrier
	s_waitcnt lgkmcnt(0)
	v_mfma_f32_16x16x32_bf16 v[128:131], v[132:135], v[174:177], v[128:131]
	v_mfma_f32_16x16x32_bf16 v[124:127], v[140:143], v[174:177], v[124:127]
	v_mfma_f32_16x16x32_bf16 v[120:123], v[132:135], v[186:189], v[120:123]
	v_mfma_f32_16x16x32_bf16 v[108:111], v[140:143], v[186:189], v[108:111]
	v_mfma_f32_16x16x32_bf16 v[104:107], v[132:135], v[194:197], v[104:107]
	v_mfma_f32_16x16x32_bf16 v[92:95], v[140:143], v[194:197], v[92:95]
	v_mfma_f32_16x16x32_bf16 v[88:91], v[132:135], v[202:205], v[88:91]
	v_mfma_f32_16x16x32_bf16 v[76:79], v[140:143], v[202:205], v[76:79]
	v_mfma_f32_16x16x32_bf16 v[128:131], v[136:139], v[182:185], v[128:131]
	v_mfma_f32_16x16x32_bf16 v[124:127], v[150:153], v[182:185], v[124:127]
	v_mfma_f32_16x16x32_bf16 v[120:123], v[136:139], v[190:193], v[120:123]
	v_mfma_f32_16x16x32_bf16 v[108:111], v[150:153], v[190:193], v[108:111]
	v_mfma_f32_16x16x32_bf16 v[104:107], v[136:139], v[198:201], v[104:107]
	v_mfma_f32_16x16x32_bf16 v[92:95], v[150:153], v[198:201], v[92:95]
	v_mfma_f32_16x16x32_bf16 v[88:91], v[136:139], v[206:209], v[88:91]
	v_mfma_f32_16x16x32_bf16 v[76:79], v[150:153], v[206:209], v[76:79]
	v_mfma_f32_16x16x32_bf16 v[116:119], v[154:157], v[174:177], v[116:119]
	v_mfma_f32_16x16x32_bf16 v[112:115], v[166:169], v[174:177], v[112:115]
	v_mfma_f32_16x16x32_bf16 v[100:103], v[154:157], v[186:189], v[100:103]
	v_mfma_f32_16x16x32_bf16 v[96:99], v[166:169], v[186:189], v[96:99]
	v_mfma_f32_16x16x32_bf16 v[84:87], v[154:157], v[194:197], v[84:87]
	v_mfma_f32_16x16x32_bf16 v[80:83], v[166:169], v[194:197], v[80:83]
	v_mfma_f32_16x16x32_bf16 v[72:75], v[154:157], v[202:205], v[72:75]
	v_mfma_f32_16x16x32_bf16 v[68:71], v[166:169], v[202:205], v[68:71]
	v_mfma_f32_16x16x32_bf16 v[116:119], v[162:165], v[182:185], v[116:119]
	v_mfma_f32_16x16x32_bf16 v[112:115], v[170:173], v[182:185], v[112:115]
	v_mfma_f32_16x16x32_bf16 v[100:103], v[162:165], v[190:193], v[100:103]
	v_mfma_f32_16x16x32_bf16 v[96:99], v[170:173], v[190:193], v[96:99]
	v_mfma_f32_16x16x32_bf16 v[84:87], v[162:165], v[198:201], v[84:87]
	v_mfma_f32_16x16x32_bf16 v[80:83], v[170:173], v[198:201], v[80:83]
	v_mfma_f32_16x16x32_bf16 v[72:75], v[162:165], v[206:209], v[72:75]
	v_mfma_f32_16x16x32_bf16 v[68:71], v[170:173], v[206:209], v[68:71]
	s_barrier
	s_add_i32 s13, s13, s47
	v_lshl_add_u64 v[178:179], v[178:179], 0, s[86:87]
	s_mov_b32 m0, s13
	ds_read_b128 v[174:177], v161 offset:49152
	ds_read_b128 v[182:185], v161 offset:50176
	ds_read_b128 v[186:189], v161 offset:51200
	ds_read_b128 v[190:193], v161 offset:52224
	ds_read_b128 v[194:197], v161 offset:53248
	ds_read_b128 v[198:201], v161 offset:54272
	ds_read_b128 v[202:205], v161 offset:55296
	ds_read_b128 v[206:209], v161 offset:56320
	global_load_lds_dwordx4 v[178:179], off
	s_add_i32 m0, s13, 0x2000
	s_add_u32 s22, s26, 0x80080
	v_lshl_add_u64 v[178:179], v[210:211], 0, s[86:87]
	s_addc_u32 s23, s27, 0
	s_add_i32 s13, s21, s47
	global_load_lds_dwordx4 v[178:179], off
	v_lshl_add_u64 v[178:179], s[22:23], 0, v[2:3]
	s_mov_b32 m0, s13
	s_nop 0
	global_load_lds_dwordx4 v[178:179], off
	v_lshl_add_u64 v[178:179], s[22:23], 0, v[144:145]
	s_add_i32 m0, s13, 0x2000
	s_nop 0
	global_load_lds_dwordx4 v[178:179], off
	v_lshl_add_u64 v[178:179], v[216:217], 0, s[86:87]
	s_mov_b32 m0, s58
	s_nop 0
	global_load_lds_dwordx4 v[178:179], off
	v_lshl_add_u64 v[178:179], v[218:219], 0, s[86:87]
	s_mov_b32 m0, s59
	s_nop 0
	global_load_lds_dwordx4 v[178:179], off
	s_waitcnt vmcnt(8)
	s_waitcnt lgkmcnt(0)
	s_barrier
	s_waitcnt lgkmcnt(0)
	v_mfma_f32_16x16x32_bf16 v[64:67], v[132:135], v[174:177], v[64:67]
	v_mfma_f32_16x16x32_bf16 v[60:63], v[140:143], v[174:177], v[60:63]
	v_mfma_f32_16x16x32_bf16 v[56:59], v[132:135], v[186:189], v[56:59]
	v_mfma_f32_16x16x32_bf16 v[44:47], v[140:143], v[186:189], v[44:47]
	v_mfma_f32_16x16x32_bf16 v[40:43], v[132:135], v[194:197], v[40:43]
	v_mfma_f32_16x16x32_bf16 v[28:31], v[140:143], v[194:197], v[28:31]
	v_mfma_f32_16x16x32_bf16 v[24:27], v[132:135], v[202:205], v[24:27]
	v_mfma_f32_16x16x32_bf16 v[12:15], v[140:143], v[202:205], v[12:15]
	v_mfma_f32_16x16x32_bf16 v[64:67], v[136:139], v[182:185], v[64:67]
	v_mfma_f32_16x16x32_bf16 v[60:63], v[150:153], v[182:185], v[60:63]
	v_mfma_f32_16x16x32_bf16 v[56:59], v[136:139], v[190:193], v[56:59]
	v_mfma_f32_16x16x32_bf16 v[44:47], v[150:153], v[190:193], v[44:47]
	v_mfma_f32_16x16x32_bf16 v[40:43], v[136:139], v[198:201], v[40:43]
	v_mfma_f32_16x16x32_bf16 v[28:31], v[150:153], v[198:201], v[28:31]
	v_mfma_f32_16x16x32_bf16 v[24:27], v[136:139], v[206:209], v[24:27]
	v_mfma_f32_16x16x32_bf16 v[12:15], v[150:153], v[206:209], v[12:15]
	v_mfma_f32_16x16x32_bf16 v[52:55], v[154:157], v[174:177], v[52:55]
	v_mfma_f32_16x16x32_bf16 v[48:51], v[166:169], v[174:177], v[48:51]
	v_mfma_f32_16x16x32_bf16 v[36:39], v[154:157], v[186:189], v[36:39]
	v_mfma_f32_16x16x32_bf16 v[32:35], v[166:169], v[186:189], v[32:35]
	v_mfma_f32_16x16x32_bf16 v[20:23], v[154:157], v[194:197], v[20:23]
	v_mfma_f32_16x16x32_bf16 v[16:19], v[166:169], v[194:197], v[16:19]
	v_mfma_f32_16x16x32_bf16 v[8:11], v[154:157], v[202:205], v[8:11]
	v_mfma_f32_16x16x32_bf16 v[4:7], v[166:169], v[202:205], v[4:7]
	v_mfma_f32_16x16x32_bf16 v[52:55], v[162:165], v[182:185], v[52:55]
	v_mfma_f32_16x16x32_bf16 v[48:51], v[170:173], v[182:185], v[48:51]
	v_mfma_f32_16x16x32_bf16 v[36:39], v[162:165], v[190:193], v[36:39]
	v_mfma_f32_16x16x32_bf16 v[32:35], v[170:173], v[190:193], v[32:35]
	v_mfma_f32_16x16x32_bf16 v[20:23], v[162:165], v[198:201], v[20:23]
	v_mfma_f32_16x16x32_bf16 v[16:19], v[170:173], v[198:201], v[16:19]
	v_mfma_f32_16x16x32_bf16 v[8:11], v[162:165], v[206:209], v[8:11]
	v_mfma_f32_16x16x32_bf16 v[4:7], v[170:173], v[206:209], v[4:7]
	s_barrier
	s_add_i32 s12, s12, 2
	s_add_u32 s0, s0, 0x100
	s_addc_u32 s11, s11, 0
	s_cmp_gt_u32 s12, 29
	s_mov_b64 s[22:23], s[24:25]
	s_cbranch_scc0 .LBB6_1775
	s_and_b64 vcc, exec, s[8:9]
	s_cbranch_vccz .LBB6_1778
	s_barrier

.LBB6_1891:
	s_add_u32 s13, s24, 0xfffc0080
	s_addc_u32 s15, s25, -1
	s_add_i32 s0, 0, 0x10000
	s_cmp_eq_u32 s12, 12
	s_cselect_b32 s29, s17, s15
	s_cselect_b32 s28, s16, s13
	s_cselect_b32 s27, s19, s11
	s_cselect_b32 s26, s18, s1
	s_add_i32 s13, 0, 0x14000
	v_add_u32_e32 v4, s0, v185
	v_add_u32_e32 v16, s13, v185
	ds_read_b128 v[20:23], v4
	ds_read_b128 v[24:27], v4 offset:1024
	ds_read_b128 v[28:31], v4 offset:2048
	ds_read_b128 v[32:35], v4 offset:3072
	ds_read_b128 v[4:7], v16
	ds_read_b128 v[8:11], v16 offset:1024
	ds_read_b128 v[12:15], v16 offset:2048
	ds_read_b128 v[16:19], v16 offset:3072
	v_lshl_add_u64 v[174:175], s[24:25], 0, v[172:173]
	s_add_i32 m0, s21, 0xc000
	ds_read_b128 v[188:191], v187
	ds_read_b128 v[192:195], v187 offset:1024
	ds_read_b128 v[196:199], v187 offset:2048
	ds_read_b128 v[200:203], v187 offset:3072
	ds_read_b128 v[204:207], v187 offset:4096
	ds_read_b128 v[208:211], v187 offset:5120
	ds_read_b128 v[228:231], v187 offset:6144
	ds_read_b128 v[232:235], v187 offset:7168
	global_load_lds_dwordx4 v[174:175], off
	v_lshl_add_u64 v[174:175], s[24:25], 0, v[170:171]
	s_add_i32 m0, s21, 0xe000
	s_nop 0
	global_load_lds_dwordx4 v[174:175], off
	s_waitcnt vmcnt(8)
	s_waitcnt lgkmcnt(0)
	s_barrier
	s_waitcnt lgkmcnt(0)
	v_mfma_f32_16x16x128_f8f6f4 v[160:163], v[20:27], v[188:195], v[160:163]
	v_mfma_f32_16x16x128_f8f6f4 v[156:159], v[28:35], v[188:195], v[156:159]
	v_mfma_f32_16x16x128_f8f6f4 v[144:147], v[20:27], v[196:203], v[144:147]
	v_mfma_f32_16x16x128_f8f6f4 v[140:143], v[28:35], v[196:203], v[140:143]
	v_mfma_f32_16x16x128_f8f6f4 v[128:131], v[20:27], v[204:211], v[128:131]
	v_mfma_f32_16x16x128_f8f6f4 v[124:127], v[28:35], v[204:211], v[124:127]
	v_mfma_f32_16x16x128_f8f6f4 v[112:115], v[20:27], v[228:235], v[112:115]
	v_mfma_f32_16x16x128_f8f6f4 v[108:111], v[28:35], v[228:235], v[108:111]
	v_mfma_f32_16x16x128_f8f6f4 v[152:155], v[4:11], v[188:195], v[152:155]
	v_mfma_f32_16x16x128_f8f6f4 v[148:151], v[12:19], v[188:195], v[148:151]
	v_mfma_f32_16x16x128_f8f6f4 v[136:139], v[4:11], v[196:203], v[136:139]
	v_mfma_f32_16x16x128_f8f6f4 v[132:135], v[12:19], v[196:203], v[132:135]
	v_mfma_f32_16x16x128_f8f6f4 v[120:123], v[4:11], v[204:211], v[120:123]
	v_mfma_f32_16x16x128_f8f6f4 v[116:119], v[12:19], v[204:211], v[116:119]
	v_mfma_f32_16x16x128_f8f6f4 v[104:107], v[4:11], v[228:235], v[104:107]
	v_mfma_f32_16x16x128_f8f6f4 v[100:103], v[12:19], v[228:235], v[100:103]
	s_barrier
	s_add_i32 s0, s0, s65
	v_lshl_add_u64 v[174:175], s[26:27], 0, v[2:3]
	s_mov_b32 m0, s0
	ds_read_b128 v[188:191], v187 offset:16384
	ds_read_b128 v[192:195], v187 offset:17408
	ds_read_b128 v[196:199], v187 offset:18432
	ds_read_b128 v[200:203], v187 offset:19456
	ds_read_b128 v[204:207], v187 offset:20480
	ds_read_b128 v[208:211], v187 offset:21504
	ds_read_b128 v[228:231], v187 offset:22528
	ds_read_b128 v[232:235], v187 offset:23552
	global_load_lds_dwordx4 v[174:175], off
	s_add_i32 m0, s0, 0x2000
	s_add_u32 s70, s26, 0x40000
	v_lshl_add_u64 v[176:177], s[26:27], 0, v[164:165]
	s_addc_u32 s71, s27, 0
	s_add_i32 s0, s13, s65
	global_load_lds_dwordx4 v[176:177], off
	v_lshl_add_u64 v[178:179], s[70:71], 0, v[2:3]
	s_mov_b32 m0, s0
	v_lshl_add_u64 v[182:183], s[28:29], 0, v[166:167]
	global_load_lds_dwordx4 v[178:179], off
	v_lshl_add_u64 v[178:179], s[70:71], 0, v[164:165]
	s_add_i32 m0, s0, 0x2000
	s_nop 0
	global_load_lds_dwordx4 v[178:179], off
	v_lshl_add_u64 v[178:179], s[28:29], 0, v[168:169]
	s_mov_b32 m0, s21
	s_nop 0
	global_load_lds_dwordx4 v[178:179], off
	s_mov_b32 m0, s23
	s_nop 0
	global_load_lds_dwordx4 v[182:183], off
	s_waitcnt vmcnt(8)
	s_waitcnt lgkmcnt(0)
	s_barrier
	s_waitcnt lgkmcnt(0)
	v_mfma_f32_16x16x128_f8f6f4 v[96:99], v[20:27], v[188:195], v[96:99]
	v_mfma_f32_16x16x128_f8f6f4 v[92:95], v[28:35], v[188:195], v[92:95]
	v_mfma_f32_16x16x128_f8f6f4 v[80:83], v[20:27], v[196:203], v[80:83]
	v_mfma_f32_16x16x128_f8f6f4 v[76:79], v[28:35], v[196:203], v[76:79]
	v_mfma_f32_16x16x128_f8f6f4 v[64:67], v[20:27], v[204:211], v[64:67]
	v_mfma_f32_16x16x128_f8f6f4 v[60:63], v[28:35], v[204:211], v[60:63]
	v_mfma_f32_16x16x128_f8f6f4 v[48:51], v[20:27], v[228:235], v[48:51]
	v_mfma_f32_16x16x128_f8f6f4 v[44:47], v[28:35], v[228:235], v[44:47]
	v_mfma_f32_16x16x128_f8f6f4 v[88:91], v[4:11], v[188:195], v[88:91]
	v_mfma_f32_16x16x128_f8f6f4 v[84:87], v[12:19], v[188:195], v[84:87]
	v_mfma_f32_16x16x128_f8f6f4 v[72:75], v[4:11], v[196:203], v[72:75]
	v_mfma_f32_16x16x128_f8f6f4 v[68:71], v[12:19], v[196:203], v[68:71]
	v_mfma_f32_16x16x128_f8f6f4 v[56:59], v[4:11], v[204:211], v[56:59]
	v_mfma_f32_16x16x128_f8f6f4 v[52:55], v[12:19], v[204:211], v[52:55]
	v_mfma_f32_16x16x128_f8f6f4 v[40:43], v[4:11], v[228:235], v[40:43]
	v_mfma_f32_16x16x128_f8f6f4 v[36:39], v[12:19], v[228:235], v[36:39]
	s_barrier
	s_add_i32 s0, 0, 0x18000
	s_add_i32 s13, 0, 0x1c000
	v_add_u32_e32 v16, s0, v185
	v_add_u32_e32 v32, s13, v185
	ds_read_b128 v[4:7], v16
	ds_read_b128 v[8:11], v16 offset:1024
	ds_read_b128 v[12:15], v16 offset:2048
	ds_read_b128 v[16:19], v16 offset:3072
	ds_read_b128 v[20:23], v32
	ds_read_b128 v[24:27], v32 offset:1024
	ds_read_b128 v[28:31], v32 offset:2048
	ds_read_b128 v[32:35], v32 offset:3072
	s_add_u32 s28, s28, 0x40000
	s_addc_u32 s29, s29, 0
	s_mov_b32 m0, s81
	v_lshl_add_u64 v[216:217], s[28:29], 0, v[168:169]
	ds_read_b128 v[188:191], v187 offset:32768
	ds_read_b128 v[192:195], v187 offset:33792
	ds_read_b128 v[196:199], v187 offset:34816
	ds_read_b128 v[200:203], v187 offset:35840
	ds_read_b128 v[204:207], v187 offset:36864
	ds_read_b128 v[208:211], v187 offset:37888
	ds_read_b128 v[228:231], v187 offset:38912
	ds_read_b128 v[232:235], v187 offset:39936
	global_load_lds_dwordx4 v[216:217], off
	v_lshl_add_u64 v[216:217], s[28:29], 0, v[166:167]
	s_mov_b32 m0, s84
	s_nop 0
	global_load_lds_dwordx4 v[216:217], off
	s_waitcnt vmcnt(8)
	s_waitcnt lgkmcnt(0)
	s_barrier
	s_waitcnt lgkmcnt(0)
	v_mfma_f32_16x16x128_f8f6f4 v[160:163], v[4:11], v[188:195], v[160:163]
	v_mfma_f32_16x16x128_f8f6f4 v[156:159], v[12:19], v[188:195], v[156:159]
	v_mfma_f32_16x16x128_f8f6f4 v[144:147], v[4:11], v[196:203], v[144:147]
	v_mfma_f32_16x16x128_f8f6f4 v[140:143], v[12:19], v[196:203], v[140:143]
	v_mfma_f32_16x16x128_f8f6f4 v[128:131], v[4:11], v[204:211], v[128:131]
	v_mfma_f32_16x16x128_f8f6f4 v[124:127], v[12:19], v[204:211], v[124:127]
	v_mfma_f32_16x16x128_f8f6f4 v[112:115], v[4:11], v[228:235], v[112:115]
	v_mfma_f32_16x16x128_f8f6f4 v[108:111], v[12:19], v[228:235], v[108:111]
	v_mfma_f32_16x16x128_f8f6f4 v[152:155], v[20:27], v[188:195], v[152:155]
	v_mfma_f32_16x16x128_f8f6f4 v[148:151], v[28:35], v[188:195], v[148:151]
	v_mfma_f32_16x16x128_f8f6f4 v[136:139], v[20:27], v[196:203], v[136:139]
	v_mfma_f32_16x16x128_f8f6f4 v[132:135], v[28:35], v[196:203], v[132:135]
	v_mfma_f32_16x16x128_f8f6f4 v[120:123], v[20:27], v[204:211], v[120:123]
	v_mfma_f32_16x16x128_f8f6f4 v[116:119], v[28:35], v[204:211], v[116:119]
	v_mfma_f32_16x16x128_f8f6f4 v[104:107], v[20:27], v[228:235], v[104:107]
	v_mfma_f32_16x16x128_f8f6f4 v[100:103], v[28:35], v[228:235], v[100:103]
	s_barrier
	s_add_i32 s0, s0, s65
	v_lshl_add_u64 v[174:175], v[174:175], 0, s[86:87]
	s_mov_b32 m0, s0
	ds_read_b128 v[188:191], v187 offset:49152
	ds_read_b128 v[192:195], v187 offset:50176
	ds_read_b128 v[196:199], v187 offset:51200
	ds_read_b128 v[200:203], v187 offset:52224
	ds_read_b128 v[204:207], v187 offset:53248
	ds_read_b128 v[208:211], v187 offset:54272
	ds_read_b128 v[228:231], v187 offset:55296
	ds_read_b128 v[232:235], v187 offset:56320
	global_load_lds_dwordx4 v[174:175], off
	s_add_i32 m0, s0, 0x2000
	s_add_u32 s26, s26, 0x40080
	v_lshl_add_u64 v[174:175], v[176:177], 0, s[86:87]
	s_addc_u32 s27, s27, 0
	s_add_i32 s0, s13, s65
	global_load_lds_dwordx4 v[174:175], off
	v_lshl_add_u64 v[174:175], s[26:27], 0, v[2:3]
	s_mov_b32 m0, s0
	s_nop 0
	global_load_lds_dwordx4 v[174:175], off
	v_lshl_add_u64 v[174:175], s[26:27], 0, v[164:165]
	s_add_i32 m0, s0, 0x2000
	s_nop 0
	global_load_lds_dwordx4 v[174:175], off
	v_lshl_add_u64 v[174:175], v[178:179], 0, s[86:87]
	s_mov_b32 m0, s90
	s_nop 0
	global_load_lds_dwordx4 v[174:175], off
	v_lshl_add_u64 v[174:175], v[182:183], 0, s[86:87]
	s_mov_b32 m0, s91
	s_nop 0
	global_load_lds_dwordx4 v[174:175], off
	s_waitcnt vmcnt(8)
	s_waitcnt lgkmcnt(0)
	s_barrier
	s_waitcnt lgkmcnt(0)
	v_mfma_f32_16x16x128_f8f6f4 v[96:99], v[4:11], v[188:195], v[96:99]
	v_mfma_f32_16x16x128_f8f6f4 v[92:95], v[12:19], v[188:195], v[92:95]
	v_mfma_f32_16x16x128_f8f6f4 v[80:83], v[4:11], v[196:203], v[80:83]
	v_mfma_f32_16x16x128_f8f6f4 v[76:79], v[12:19], v[196:203], v[76:79]
	v_mfma_f32_16x16x128_f8f6f4 v[64:67], v[4:11], v[204:211], v[64:67]
	v_mfma_f32_16x16x128_f8f6f4 v[60:63], v[12:19], v[204:211], v[60:63]
	v_mfma_f32_16x16x128_f8f6f4 v[48:51], v[4:11], v[228:235], v[48:51]
	v_mfma_f32_16x16x128_f8f6f4 v[44:47], v[12:19], v[228:235], v[44:47]
	v_mfma_f32_16x16x128_f8f6f4 v[88:91], v[20:27], v[188:195], v[88:91]
	v_mfma_f32_16x16x128_f8f6f4 v[84:87], v[28:35], v[188:195], v[84:87]
	v_mfma_f32_16x16x128_f8f6f4 v[72:75], v[20:27], v[196:203], v[72:75]
	v_mfma_f32_16x16x128_f8f6f4 v[68:71], v[28:35], v[196:203], v[68:71]
	v_mfma_f32_16x16x128_f8f6f4 v[56:59], v[20:27], v[204:211], v[56:59]
	v_mfma_f32_16x16x128_f8f6f4 v[52:55], v[28:35], v[204:211], v[52:55]
	v_mfma_f32_16x16x128_f8f6f4 v[40:43], v[20:27], v[228:235], v[40:43]
	v_mfma_f32_16x16x128_f8f6f4 v[36:39], v[28:35], v[228:235], v[36:39]
	s_barrier
	s_add_i32 s12, s12, 2
	s_add_u32 s1, s1, 0x100
	s_addc_u32 s11, s11, 0
	s_add_u32 s24, s24, 0x100
	s_addc_u32 s25, s25, 0
	s_cmp_gt_u32 s12, 13
	s_cbranch_scc0 .LBB6_1891
	s_nop 7
	s_nop 7
	s_nop 7
	s_and_b64 vcc, exec, s[8:9]
	s_cbranch_vccz .LBB6_1894
	s_barrier

.LBB6_1951:
	s_add_u32 s20, s18, 0x100
	s_addc_u32 s21, s19, 0
	s_add_i32 s45, 0, 0x10000
	s_cmp_eq_u32 s0, 40
	s_cselect_b32 s25, s15, s21
	s_cselect_b32 s24, s14, s20
	s_cselect_b32 s23, s17, vcc_hi
	s_cselect_b32 s22, s16, vcc_lo
	s_add_i32 s69, 0, 0x14000
	v_add_u32_e32 v4, s45, v185
	v_add_u32_e32 v16, s69, v185
	ds_read_b128 v[20:23], v4
	ds_read_b128 v[24:27], v4 offset:1024
	ds_read_b128 v[28:31], v4 offset:2048
	ds_read_b128 v[32:35], v4 offset:3072
	ds_read_b128 v[4:7], v16
	ds_read_b128 v[8:11], v16 offset:1024
	ds_read_b128 v[12:15], v16 offset:2048
	ds_read_b128 v[16:19], v16 offset:3072
	v_lshl_add_u64 v[174:175], s[18:19], 0, v[172:173]
	s_add_i32 m0, s94, 0xc000
	ds_read_b128 v[188:191], v187
	ds_read_b128 v[192:195], v187 offset:1024
	ds_read_b128 v[196:199], v187 offset:2048
	ds_read_b128 v[200:203], v187 offset:3072
	ds_read_b128 v[204:207], v187 offset:4096
	ds_read_b128 v[208:211], v187 offset:5120
	ds_read_b128 v[228:231], v187 offset:6144
	ds_read_b128 v[232:235], v187 offset:7168
	global_load_lds_dwordx4 v[174:175], off
	v_lshl_add_u64 v[174:175], s[18:19], 0, v[170:171]
	s_add_i32 m0, s94, 0xe000
	s_nop 0
	global_load_lds_dwordx4 v[174:175], off
	s_waitcnt vmcnt(8)
	s_waitcnt lgkmcnt(0)
	s_barrier
	s_waitcnt lgkmcnt(0)
	v_mfma_f32_16x16x128_f8f6f4 v[160:163], v[20:27], v[188:195], v[160:163]
	v_mfma_f32_16x16x128_f8f6f4 v[156:159], v[28:35], v[188:195], v[156:159]
	v_mfma_f32_16x16x128_f8f6f4 v[152:155], v[20:27], v[196:203], v[152:155]
	v_mfma_f32_16x16x128_f8f6f4 v[144:147], v[28:35], v[196:203], v[144:147]
	v_mfma_f32_16x16x128_f8f6f4 v[136:139], v[20:27], v[204:211], v[136:139]
	v_mfma_f32_16x16x128_f8f6f4 v[128:131], v[28:35], v[204:211], v[128:131]
	v_mfma_f32_16x16x128_f8f6f4 v[120:123], v[20:27], v[228:235], v[120:123]
	v_mfma_f32_16x16x128_f8f6f4 v[112:115], v[28:35], v[228:235], v[112:115]
	v_mfma_f32_16x16x128_f8f6f4 v[148:151], v[4:11], v[188:195], v[148:151]
	v_mfma_f32_16x16x128_f8f6f4 v[140:143], v[12:19], v[188:195], v[140:143]
	v_mfma_f32_16x16x128_f8f6f4 v[132:135], v[4:11], v[196:203], v[132:135]
	v_mfma_f32_16x16x128_f8f6f4 v[124:127], v[12:19], v[196:203], v[124:127]
	v_mfma_f32_16x16x128_f8f6f4 v[116:119], v[4:11], v[204:211], v[116:119]
	v_mfma_f32_16x16x128_f8f6f4 v[108:111], v[12:19], v[204:211], v[108:111]
	v_mfma_f32_16x16x128_f8f6f4 v[104:107], v[4:11], v[228:235], v[104:107]
	v_mfma_f32_16x16x128_f8f6f4 v[100:103], v[12:19], v[228:235], v[100:103]
	s_barrier
	s_add_i32 s18, s45, s75
	v_lshl_add_u64 v[174:175], s[22:23], 0, v[2:3]
	s_mov_b32 m0, s18
	ds_read_b128 v[188:191], v187 offset:16384
	ds_read_b128 v[192:195], v187 offset:17408
	ds_read_b128 v[196:199], v187 offset:18432
	ds_read_b128 v[200:203], v187 offset:19456
	ds_read_b128 v[204:207], v187 offset:20480
	ds_read_b128 v[208:211], v187 offset:21504
	ds_read_b128 v[228:231], v187 offset:22528
	ds_read_b128 v[232:235], v187 offset:23552
	global_load_lds_dwordx4 v[174:175], off
	s_add_i32 m0, s18, 0x2000
	s_add_u32 s18, s22, 0xb0000
	v_lshl_add_u64 v[176:177], s[22:23], 0, v[164:165]
	s_addc_u32 s19, s23, 0
	s_add_i32 s45, s69, s75
	global_load_lds_dwordx4 v[176:177], off
	v_lshl_add_u64 v[178:179], s[18:19], 0, v[2:3]
	s_mov_b32 m0, s45
	v_lshl_add_u64 v[182:183], s[24:25], 0, v[166:167]
	global_load_lds_dwordx4 v[178:179], off
	v_lshl_add_u64 v[178:179], s[18:19], 0, v[164:165]
	s_add_i32 m0, s45, 0x2000
	s_nop 0
	global_load_lds_dwordx4 v[178:179], off
	v_lshl_add_u64 v[178:179], s[24:25], 0, v[168:169]
	s_mov_b32 m0, s94
	s_nop 0
	global_load_lds_dwordx4 v[178:179], off
	s_mov_b32 m0, s95
	s_nop 0
	global_load_lds_dwordx4 v[182:183], off
	s_waitcnt vmcnt(8)
	s_waitcnt lgkmcnt(0)
	s_barrier
	s_waitcnt lgkmcnt(0)
	v_mfma_f32_16x16x128_f8f6f4 v[96:99], v[20:27], v[188:195], v[96:99]
	v_mfma_f32_16x16x128_f8f6f4 v[92:95], v[28:35], v[188:195], v[92:95]
	v_mfma_f32_16x16x128_f8f6f4 v[88:91], v[20:27], v[196:203], v[88:91]
	v_mfma_f32_16x16x128_f8f6f4 v[80:83], v[28:35], v[196:203], v[80:83]
	v_mfma_f32_16x16x128_f8f6f4 v[72:75], v[20:27], v[204:211], v[72:75]
	v_mfma_f32_16x16x128_f8f6f4 v[64:67], v[28:35], v[204:211], v[64:67]
	v_mfma_f32_16x16x128_f8f6f4 v[56:59], v[20:27], v[228:235], v[56:59]
	v_mfma_f32_16x16x128_f8f6f4 v[48:51], v[28:35], v[228:235], v[48:51]
	v_mfma_f32_16x16x128_f8f6f4 v[84:87], v[4:11], v[188:195], v[84:87]
	v_mfma_f32_16x16x128_f8f6f4 v[76:79], v[12:19], v[188:195], v[76:79]
	v_mfma_f32_16x16x128_f8f6f4 v[68:71], v[4:11], v[196:203], v[68:71]
	v_mfma_f32_16x16x128_f8f6f4 v[60:63], v[12:19], v[196:203], v[60:63]
	v_mfma_f32_16x16x128_f8f6f4 v[52:55], v[4:11], v[204:211], v[52:55]
	v_mfma_f32_16x16x128_f8f6f4 v[44:47], v[12:19], v[204:211], v[44:47]
	v_mfma_f32_16x16x128_f8f6f4 v[40:43], v[4:11], v[228:235], v[40:43]
	v_mfma_f32_16x16x128_f8f6f4 v[36:39], v[12:19], v[228:235], v[36:39]
	s_barrier
	s_add_i32 s45, 0, 0x18000
	s_add_i32 s69, 0, 0x1c000
	v_add_u32_e32 v16, s45, v185
	v_add_u32_e32 v32, s69, v185
	ds_read_b128 v[4:7], v16
	ds_read_b128 v[8:11], v16 offset:1024
	ds_read_b128 v[12:15], v16 offset:2048
	ds_read_b128 v[16:19], v16 offset:3072
	ds_read_b128 v[20:23], v32
	ds_read_b128 v[24:27], v32 offset:1024
	ds_read_b128 v[28:31], v32 offset:2048
	ds_read_b128 v[32:35], v32 offset:3072
	s_add_u32 s18, s24, 0xb0000
	s_addc_u32 s19, s25, 0
	s_mov_b32 m0, s12
	v_lshl_add_u64 v[216:217], s[18:19], 0, v[168:169]
	ds_read_b128 v[188:191], v187 offset:32768
	ds_read_b128 v[192:195], v187 offset:33792
	ds_read_b128 v[196:199], v187 offset:34816
	ds_read_b128 v[200:203], v187 offset:35840
	ds_read_b128 v[204:207], v187 offset:36864
	ds_read_b128 v[208:211], v187 offset:37888
	ds_read_b128 v[228:231], v187 offset:38912
	ds_read_b128 v[232:235], v187 offset:39936
	global_load_lds_dwordx4 v[216:217], off
	v_lshl_add_u64 v[216:217], s[18:19], 0, v[166:167]
	s_mov_b32 m0, s13
	s_nop 0
	global_load_lds_dwordx4 v[216:217], off
	s_waitcnt vmcnt(8)
	s_waitcnt lgkmcnt(0)
	s_barrier
	s_waitcnt lgkmcnt(0)
	v_mfma_f32_16x16x128_f8f6f4 v[160:163], v[4:11], v[188:195], v[160:163]
	v_mfma_f32_16x16x128_f8f6f4 v[156:159], v[12:19], v[188:195], v[156:159]
	v_mfma_f32_16x16x128_f8f6f4 v[152:155], v[4:11], v[196:203], v[152:155]
	v_mfma_f32_16x16x128_f8f6f4 v[144:147], v[12:19], v[196:203], v[144:147]
	v_mfma_f32_16x16x128_f8f6f4 v[136:139], v[4:11], v[204:211], v[136:139]
	v_mfma_f32_16x16x128_f8f6f4 v[128:131], v[12:19], v[204:211], v[128:131]
	v_mfma_f32_16x16x128_f8f6f4 v[120:123], v[4:11], v[228:235], v[120:123]
	v_mfma_f32_16x16x128_f8f6f4 v[112:115], v[12:19], v[228:235], v[112:115]
	v_mfma_f32_16x16x128_f8f6f4 v[148:151], v[20:27], v[188:195], v[148:151]
	v_mfma_f32_16x16x128_f8f6f4 v[140:143], v[28:35], v[188:195], v[140:143]
	v_mfma_f32_16x16x128_f8f6f4 v[132:135], v[20:27], v[196:203], v[132:135]
	v_mfma_f32_16x16x128_f8f6f4 v[124:127], v[28:35], v[196:203], v[124:127]
	v_mfma_f32_16x16x128_f8f6f4 v[116:119], v[20:27], v[204:211], v[116:119]
	v_mfma_f32_16x16x128_f8f6f4 v[108:111], v[28:35], v[204:211], v[108:111]
	v_mfma_f32_16x16x128_f8f6f4 v[104:107], v[20:27], v[228:235], v[104:107]
	v_mfma_f32_16x16x128_f8f6f4 v[100:103], v[28:35], v[228:235], v[100:103]
	s_barrier
	s_add_i32 s18, s45, s75
	v_lshl_add_u64 v[174:175], v[174:175], 0, s[86:87]
	s_mov_b32 m0, s18
	ds_read_b128 v[188:191], v187 offset:49152
	ds_read_b128 v[192:195], v187 offset:50176
	ds_read_b128 v[196:199], v187 offset:51200
	ds_read_b128 v[200:203], v187 offset:52224
	ds_read_b128 v[204:207], v187 offset:53248
	ds_read_b128 v[208:211], v187 offset:54272
	ds_read_b128 v[228:231], v187 offset:55296
	ds_read_b128 v[232:235], v187 offset:56320
	global_load_lds_dwordx4 v[174:175], off
	s_add_i32 m0, s18, 0x2000
	s_add_u32 s18, s22, 0xb0080
	v_lshl_add_u64 v[174:175], v[176:177], 0, s[86:87]
	s_addc_u32 s19, s23, 0
	s_add_i32 s22, s69, s75
	global_load_lds_dwordx4 v[174:175], off
	v_lshl_add_u64 v[174:175], s[18:19], 0, v[2:3]
	s_mov_b32 m0, s22
	s_nop 0
	global_load_lds_dwordx4 v[174:175], off
	v_lshl_add_u64 v[174:175], s[18:19], 0, v[164:165]
	s_add_i32 m0, s22, 0x2000
	s_nop 0
	global_load_lds_dwordx4 v[174:175], off
	v_lshl_add_u64 v[174:175], v[178:179], 0, s[86:87]
	s_mov_b32 m0, s76
	s_nop 0
	global_load_lds_dwordx4 v[174:175], off
	v_lshl_add_u64 v[174:175], v[182:183], 0, s[86:87]
	s_mov_b32 m0, s77
	s_nop 0
	global_load_lds_dwordx4 v[174:175], off
	s_waitcnt vmcnt(8)
	s_waitcnt lgkmcnt(0)
	s_barrier
	s_waitcnt lgkmcnt(0)
	v_mfma_f32_16x16x128_f8f6f4 v[96:99], v[4:11], v[188:195], v[96:99]
	v_mfma_f32_16x16x128_f8f6f4 v[92:95], v[12:19], v[188:195], v[92:95]
	v_mfma_f32_16x16x128_f8f6f4 v[88:91], v[4:11], v[196:203], v[88:91]
	v_mfma_f32_16x16x128_f8f6f4 v[80:83], v[12:19], v[196:203], v[80:83]
	v_mfma_f32_16x16x128_f8f6f4 v[72:75], v[4:11], v[204:211], v[72:75]
	v_mfma_f32_16x16x128_f8f6f4 v[64:67], v[12:19], v[204:211], v[64:67]
	v_mfma_f32_16x16x128_f8f6f4 v[56:59], v[4:11], v[228:235], v[56:59]
	v_mfma_f32_16x16x128_f8f6f4 v[48:51], v[12:19], v[228:235], v[48:51]
	v_mfma_f32_16x16x128_f8f6f4 v[84:87], v[20:27], v[188:195], v[84:87]
	v_mfma_f32_16x16x128_f8f6f4 v[76:79], v[28:35], v[188:195], v[76:79]
	v_mfma_f32_16x16x128_f8f6f4 v[68:71], v[20:27], v[196:203], v[68:71]
	v_mfma_f32_16x16x128_f8f6f4 v[60:63], v[28:35], v[196:203], v[60:63]
	v_mfma_f32_16x16x128_f8f6f4 v[52:55], v[20:27], v[204:211], v[52:55]
	v_mfma_f32_16x16x128_f8f6f4 v[44:47], v[28:35], v[204:211], v[44:47]
	v_mfma_f32_16x16x128_f8f6f4 v[40:43], v[20:27], v[228:235], v[40:43]
	v_mfma_f32_16x16x128_f8f6f4 v[36:39], v[28:35], v[228:235], v[36:39]
	s_barrier
	s_add_i32 s0, s0, 2
	s_add_u32 vcc_lo, vcc_lo, 0x100
	s_addc_u32 vcc_hi, vcc_hi, 0
	s_cmp_gt_u32 s0, 41
	s_mov_b64 s[18:19], s[20:21]
	s_cbranch_scc0 .LBB6_1951
	s_nop 7
	s_nop 7
	s_nop 7
	s_and_b64 vcc, exec, s[10:11]
	s_cbranch_vccz .LBB6_1954
	s_barrier

.LBB6_1968:
	s_add_u32 s18, s16, 0x100
	s_addc_u32 s19, s17, 0
	s_add_i32 s45, 0, 0x10000
	v_add_u32_e32 v94, s45, v79
	ds_read_b128 v[82:85], v94
	ds_read_b128 v[86:89], v94 offset:1024
	ds_read_b128 v[90:93], v94 offset:2048
	ds_read_b128 v[94:97], v94 offset:3072
	s_cmp_eq_u32 s81, 40
	s_cselect_b32 s21, s11, s19
	s_cselect_b32 s20, s10, s18
	s_cselect_b32 s23, s15, s80
	s_cselect_b32 s22, s14, s77
	v_lshl_add_u64 v[130:131], s[16:17], 0, v[76:77]
	s_add_i32 m0, s58, 0xc000
	ds_read_b128 v[98:101], v81
	ds_read_b128 v[102:105], v81 offset:1024
	ds_read_b128 v[106:109], v81 offset:2048
	ds_read_b128 v[110:113], v81 offset:3072
	ds_read_b128 v[114:117], v81 offset:4096
	ds_read_b128 v[118:121], v81 offset:5120
	ds_read_b128 v[122:125], v81 offset:6144
	ds_read_b128 v[126:129], v81 offset:7168
	global_load_lds_dwordx4 v[130:131], off
	v_lshl_add_u64 v[130:131], s[16:17], 0, v[74:75]
	s_add_i32 m0, s58, 0xe000
	s_nop 0
	global_load_lds_dwordx4 v[130:131], off
	s_waitcnt vmcnt(6)
	s_waitcnt lgkmcnt(0)
	s_barrier
	s_waitcnt lgkmcnt(0)
	v_mfma_f32_16x16x128_f8f6f4 v[64:67], v[82:89], v[98:105], v[64:67]
	v_mfma_f32_16x16x128_f8f6f4 v[60:63], v[90:97], v[98:105], v[60:63]
	v_mfma_f32_16x16x128_f8f6f4 v[56:59], v[82:89], v[106:113], v[56:59]
	v_mfma_f32_16x16x128_f8f6f4 v[52:55], v[90:97], v[106:113], v[52:55]
	v_mfma_f32_16x16x128_f8f6f4 v[48:51], v[82:89], v[114:121], v[48:51]
	v_mfma_f32_16x16x128_f8f6f4 v[44:47], v[90:97], v[114:121], v[44:47]
	v_mfma_f32_16x16x128_f8f6f4 v[40:43], v[82:89], v[122:129], v[40:43]
	v_mfma_f32_16x16x128_f8f6f4 v[36:39], v[90:97], v[122:129], v[36:39]
	s_barrier
	s_add_i32 s16, s45, s13
	v_lshl_add_u64 v[130:131], s[22:23], 0, v[2:3]
	s_mov_b32 m0, s16
	ds_read_b128 v[98:101], v81 offset:16384
	ds_read_b128 v[102:105], v81 offset:17408
	ds_read_b128 v[106:109], v81 offset:18432
	ds_read_b128 v[110:113], v81 offset:19456
	ds_read_b128 v[114:117], v81 offset:20480
	ds_read_b128 v[118:121], v81 offset:21504
	ds_read_b128 v[122:125], v81 offset:22528
	ds_read_b128 v[126:129], v81 offset:23552
	global_load_lds_dwordx4 v[130:131], off
	v_lshl_add_u64 v[132:133], s[22:23], 0, v[68:69]
	s_add_i32 m0, s16, 0x2000
	v_lshl_add_u64 v[134:135], s[20:21], 0, v[72:73]
	global_load_lds_dwordx4 v[132:133], off
	s_mov_b32 m0, s58
	v_lshl_add_u64 v[136:137], s[20:21], 0, v[70:71]
	global_load_lds_dwordx4 v[134:135], off
	s_mov_b32 m0, s64
	s_nop 0
	global_load_lds_dwordx4 v[136:137], off
	s_waitcnt vmcnt(6)
	s_waitcnt lgkmcnt(0)
	s_barrier
	s_waitcnt lgkmcnt(0)
	v_mfma_f32_16x16x128_f8f6f4 v[28:31], v[82:89], v[98:105], v[28:31]
	v_mfma_f32_16x16x128_f8f6f4 v[32:35], v[90:97], v[98:105], v[32:35]
	v_mfma_f32_16x16x128_f8f6f4 v[24:27], v[82:89], v[106:113], v[24:27]
	v_mfma_f32_16x16x128_f8f6f4 v[20:23], v[90:97], v[106:113], v[20:23]
	v_mfma_f32_16x16x128_f8f6f4 v[16:19], v[82:89], v[114:121], v[16:19]
	v_mfma_f32_16x16x128_f8f6f4 v[12:15], v[90:97], v[114:121], v[12:15]
	v_mfma_f32_16x16x128_f8f6f4 v[8:11], v[82:89], v[122:129], v[8:11]
	v_mfma_f32_16x16x128_f8f6f4 v[4:7], v[90:97], v[122:129], v[4:7]
	s_barrier
	s_add_i32 s22, 0, 0x18000
	v_add_u32_e32 v94, s22, v79
	ds_read_b128 v[82:85], v94
	ds_read_b128 v[86:89], v94 offset:1024
	ds_read_b128 v[90:93], v94 offset:2048
	ds_read_b128 v[94:97], v94 offset:3072
	s_add_u32 s16, s20, 0xb0000
	s_addc_u32 s17, s21, 0
	s_mov_b32 m0, s65
	v_lshl_add_u64 v[138:139], s[16:17], 0, v[72:73]
	ds_read_b128 v[98:101], v81 offset:32768
	ds_read_b128 v[102:105], v81 offset:33792
	ds_read_b128 v[106:109], v81 offset:34816
	ds_read_b128 v[110:113], v81 offset:35840
	ds_read_b128 v[114:117], v81 offset:36864
	ds_read_b128 v[118:121], v81 offset:37888
	ds_read_b128 v[122:125], v81 offset:38912
	ds_read_b128 v[126:129], v81 offset:39936
	global_load_lds_dwordx4 v[138:139], off
	v_lshl_add_u64 v[138:139], s[16:17], 0, v[70:71]
	s_mov_b32 m0, s66
	s_nop 0
	global_load_lds_dwordx4 v[138:139], off
	s_waitcnt vmcnt(6)
	s_waitcnt lgkmcnt(0)
	s_barrier
	s_waitcnt lgkmcnt(0)
	v_mfma_f32_16x16x128_f8f6f4 v[64:67], v[82:89], v[98:105], v[64:67]
	v_mfma_f32_16x16x128_f8f6f4 v[60:63], v[90:97], v[98:105], v[60:63]
	v_mfma_f32_16x16x128_f8f6f4 v[56:59], v[82:89], v[106:113], v[56:59]
	v_mfma_f32_16x16x128_f8f6f4 v[52:55], v[90:97], v[106:113], v[52:55]
	v_mfma_f32_16x16x128_f8f6f4 v[48:51], v[82:89], v[114:121], v[48:51]
	v_mfma_f32_16x16x128_f8f6f4 v[44:47], v[90:97], v[114:121], v[44:47]
	v_mfma_f32_16x16x128_f8f6f4 v[40:43], v[82:89], v[122:129], v[40:43]
	v_mfma_f32_16x16x128_f8f6f4 v[36:39], v[90:97], v[122:129], v[36:39]
	s_barrier
	s_add_i32 s16, s22, s13
	v_lshl_add_u64 v[130:131], v[130:131], 0, s[86:87]
	s_mov_b32 m0, s16
	ds_read_b128 v[98:101], v81 offset:49152
	ds_read_b128 v[102:105], v81 offset:50176
	ds_read_b128 v[106:109], v81 offset:51200
	ds_read_b128 v[110:113], v81 offset:52224
	ds_read_b128 v[114:117], v81 offset:53248
	ds_read_b128 v[118:121], v81 offset:54272
	ds_read_b128 v[122:125], v81 offset:55296
	ds_read_b128 v[126:129], v81 offset:56320
	global_load_lds_dwordx4 v[130:131], off
	v_lshl_add_u64 v[130:131], v[132:133], 0, s[86:87]
	s_add_i32 m0, s16, 0x2000
	s_nop 0
	global_load_lds_dwordx4 v[130:131], off
	v_lshl_add_u64 v[130:131], v[134:135], 0, s[86:87]
	s_mov_b32 m0, s67
	s_nop 0
	global_load_lds_dwordx4 v[130:131], off
	v_lshl_add_u64 v[130:131], v[136:137], 0, s[86:87]
	s_mov_b32 m0, s68
	s_nop 0
	global_load_lds_dwordx4 v[130:131], off
	s_waitcnt vmcnt(6)
	s_waitcnt lgkmcnt(0)
	s_barrier
	s_waitcnt lgkmcnt(0)
	v_mfma_f32_16x16x128_f8f6f4 v[28:31], v[82:89], v[98:105], v[28:31]
	v_mfma_f32_16x16x128_f8f6f4 v[32:35], v[90:97], v[98:105], v[32:35]
	v_mfma_f32_16x16x128_f8f6f4 v[24:27], v[82:89], v[106:113], v[24:27]
	v_mfma_f32_16x16x128_f8f6f4 v[20:23], v[90:97], v[106:113], v[20:23]
	v_mfma_f32_16x16x128_f8f6f4 v[16:19], v[82:89], v[114:121], v[16:19]
	v_mfma_f32_16x16x128_f8f6f4 v[12:15], v[90:97], v[114:121], v[12:15]
	v_mfma_f32_16x16x128_f8f6f4 v[8:11], v[82:89], v[122:129], v[8:11]
	v_mfma_f32_16x16x128_f8f6f4 v[4:7], v[90:97], v[122:129], v[4:7]
	s_barrier
	s_add_i32 s81, s81, 2
	s_add_u32 s77, s77, 0x100
	s_addc_u32 s80, s80, 0
	s_cmp_gt_u32 s81, 41
	s_mov_b64 s[16:17], s[18:19]
	s_cbranch_scc0 .LBB6_1968
	s_nop 7
	s_nop 7
	s_nop 7
	s_and_b64 vcc, exec, s[8:9]
	s_cbranch_vccz .LBB6_1971
	s_barrier

.LBB6_2080:
	s_add_u32 s22, s20, 0xfff80080
	s_addc_u32 s23, s21, -1
	s_add_i32 s45, 0, 0x10000
	s_cmp_eq_u32 s33, 28
	s_cselect_b32 s25, s11, s23
	s_cselect_b32 s24, s10, s22
	v_add_u32_e32 v165, s45, v143
	s_cselect_b32 s23, s15, s9
	s_cselect_b32 s22, s14, s0
	s_add_i32 s49, 0, 0x14000
	ds_read_b128 v[146:149], v165
	ds_read_b128 v[150:153], v165 offset:1024
	ds_read_b128 v[154:157], v165 offset:2048
	ds_read_b128 v[166:169], v165 offset:3072
	v_add_u32_e32 v165, s49, v143
	ds_read_b128 v[170:173], v165
	ds_read_b128 v[174:177], v165 offset:1024
	ds_read_b128 v[182:185], v165 offset:2048
	ds_read_b128 v[186:189], v165 offset:3072
	v_lshl_add_u64 v[178:179], s[20:21], 0, v[140:141]
	s_add_i32 m0, s19, 0xc000
	ds_read_b128 v[190:193], v145
	ds_read_b128 v[194:197], v145 offset:1024
	ds_read_b128 v[198:201], v145 offset:2048
	ds_read_b128 v[202:205], v145 offset:3072
	ds_read_b128 v[206:209], v145 offset:4096
	ds_read_b128 v[216:219], v145 offset:5120
	ds_read_b128 v[220:223], v145 offset:6144
	ds_read_b128 v[228:231], v145 offset:7168
	global_load_lds_dwordx4 v[178:179], off
	v_lshl_add_u64 v[178:179], s[20:21], 0, v[138:139]
	s_add_i32 m0, s19, 0xe000
	s_nop 0
	global_load_lds_dwordx4 v[178:179], off
	s_waitcnt vmcnt(8)
	s_waitcnt lgkmcnt(0)
	s_barrier
	s_waitcnt lgkmcnt(0)
	v_mfma_f32_16x16x32_bf16 v[128:131], v[146:149], v[190:193], v[128:131]
	v_mfma_f32_16x16x32_bf16 v[124:127], v[154:157], v[190:193], v[124:127]
	v_mfma_f32_16x16x32_bf16 v[112:115], v[146:149], v[198:201], v[112:115]
	v_mfma_f32_16x16x32_bf16 v[108:111], v[154:157], v[198:201], v[108:111]
	v_mfma_f32_16x16x32_bf16 v[96:99], v[146:149], v[206:209], v[96:99]
	v_mfma_f32_16x16x32_bf16 v[92:95], v[154:157], v[206:209], v[92:95]
	v_mfma_f32_16x16x32_bf16 v[80:83], v[146:149], v[220:223], v[80:83]
	v_mfma_f32_16x16x32_bf16 v[76:79], v[154:157], v[220:223], v[76:79]
	v_mfma_f32_16x16x32_bf16 v[128:131], v[150:153], v[194:197], v[128:131]
	v_mfma_f32_16x16x32_bf16 v[124:127], v[166:169], v[194:197], v[124:127]
	v_mfma_f32_16x16x32_bf16 v[112:115], v[150:153], v[202:205], v[112:115]
	v_mfma_f32_16x16x32_bf16 v[108:111], v[166:169], v[202:205], v[108:111]
	v_mfma_f32_16x16x32_bf16 v[96:99], v[150:153], v[216:219], v[96:99]
	v_mfma_f32_16x16x32_bf16 v[92:95], v[166:169], v[216:219], v[92:95]
	v_mfma_f32_16x16x32_bf16 v[80:83], v[150:153], v[228:231], v[80:83]
	v_mfma_f32_16x16x32_bf16 v[76:79], v[166:169], v[228:231], v[76:79]
	v_mfma_f32_16x16x32_bf16 v[120:123], v[170:173], v[190:193], v[120:123]
	v_mfma_f32_16x16x32_bf16 v[116:119], v[182:185], v[190:193], v[116:119]
	v_mfma_f32_16x16x32_bf16 v[104:107], v[170:173], v[198:201], v[104:107]
	v_mfma_f32_16x16x32_bf16 v[100:103], v[182:185], v[198:201], v[100:103]
	v_mfma_f32_16x16x32_bf16 v[88:91], v[170:173], v[206:209], v[88:91]
	v_mfma_f32_16x16x32_bf16 v[84:87], v[182:185], v[206:209], v[84:87]
	v_mfma_f32_16x16x32_bf16 v[72:75], v[170:173], v[220:223], v[72:75]
	v_mfma_f32_16x16x32_bf16 v[68:71], v[182:185], v[220:223], v[68:71]
	v_mfma_f32_16x16x32_bf16 v[120:123], v[174:177], v[194:197], v[120:123]
	v_mfma_f32_16x16x32_bf16 v[116:119], v[186:189], v[194:197], v[116:119]
	v_mfma_f32_16x16x32_bf16 v[104:107], v[174:177], v[202:205], v[104:107]
	v_mfma_f32_16x16x32_bf16 v[100:103], v[186:189], v[202:205], v[100:103]
	v_mfma_f32_16x16x32_bf16 v[88:91], v[174:177], v[216:219], v[88:91]
	v_mfma_f32_16x16x32_bf16 v[84:87], v[186:189], v[216:219], v[84:87]
	v_mfma_f32_16x16x32_bf16 v[72:75], v[174:177], v[228:231], v[72:75]
	v_mfma_f32_16x16x32_bf16 v[68:71], v[186:189], v[228:231], v[68:71]
	s_barrier
	s_add_i32 s45, s45, s34
	v_lshl_add_u64 v[178:179], s[22:23], 0, v[2:3]
	s_mov_b32 m0, s45
	ds_read_b128 v[190:193], v145 offset:16384
	ds_read_b128 v[194:197], v145 offset:17408
	ds_read_b128 v[198:201], v145 offset:18432
	ds_read_b128 v[202:205], v145 offset:19456
	ds_read_b128 v[206:209], v145 offset:20480
	ds_read_b128 v[216:219], v145 offset:21504
	ds_read_b128 v[220:223], v145 offset:22528
	ds_read_b128 v[228:231], v145 offset:23552
	global_load_lds_dwordx4 v[178:179], off
	s_add_i32 m0, s45, 0x2000
	s_add_u32 s50, s22, 0x80000
	v_lshl_add_u64 v[210:211], s[22:23], 0, v[132:133]
	s_addc_u32 s51, s23, 0
	s_add_i32 s45, s49, s34
	global_load_lds_dwordx4 v[210:211], off
	v_lshl_add_u64 v[224:225], s[50:51], 0, v[2:3]
	s_mov_b32 m0, s45
	v_lshl_add_u64 v[232:233], s[24:25], 0, v[134:135]
	global_load_lds_dwordx4 v[224:225], off
	v_lshl_add_u64 v[224:225], s[50:51], 0, v[132:133]
	s_add_i32 m0, s45, 0x2000
	s_nop 0
	global_load_lds_dwordx4 v[224:225], off
	v_lshl_add_u64 v[224:225], s[24:25], 0, v[136:137]
	s_mov_b32 m0, s19
	s_nop 0
	global_load_lds_dwordx4 v[224:225], off
	s_mov_b32 m0, s35
	s_nop 0
	global_load_lds_dwordx4 v[232:233], off
	s_waitcnt vmcnt(8)
	s_waitcnt lgkmcnt(0)
	s_barrier
	s_waitcnt lgkmcnt(0)
	v_mfma_f32_16x16x32_bf16 v[64:67], v[146:149], v[190:193], v[64:67]
	v_mfma_f32_16x16x32_bf16 v[60:63], v[154:157], v[190:193], v[60:63]
	v_mfma_f32_16x16x32_bf16 v[48:51], v[146:149], v[198:201], v[48:51]
	v_mfma_f32_16x16x32_bf16 v[44:47], v[154:157], v[198:201], v[44:47]
	v_mfma_f32_16x16x32_bf16 v[32:35], v[146:149], v[206:209], v[32:35]
	v_mfma_f32_16x16x32_bf16 v[28:31], v[154:157], v[206:209], v[28:31]
	v_mfma_f32_16x16x32_bf16 v[16:19], v[146:149], v[220:223], v[16:19]
	v_mfma_f32_16x16x32_bf16 v[12:15], v[154:157], v[220:223], v[12:15]
	v_mfma_f32_16x16x32_bf16 v[64:67], v[150:153], v[194:197], v[64:67]
	v_mfma_f32_16x16x32_bf16 v[60:63], v[166:169], v[194:197], v[60:63]
	v_mfma_f32_16x16x32_bf16 v[48:51], v[150:153], v[202:205], v[48:51]
	v_mfma_f32_16x16x32_bf16 v[44:47], v[166:169], v[202:205], v[44:47]
	v_mfma_f32_16x16x32_bf16 v[32:35], v[150:153], v[216:219], v[32:35]
	v_mfma_f32_16x16x32_bf16 v[28:31], v[166:169], v[216:219], v[28:31]
	v_mfma_f32_16x16x32_bf16 v[16:19], v[150:153], v[228:231], v[16:19]
	v_mfma_f32_16x16x32_bf16 v[12:15], v[166:169], v[228:231], v[12:15]
	v_mfma_f32_16x16x32_bf16 v[56:59], v[170:173], v[190:193], v[56:59]
	v_mfma_f32_16x16x32_bf16 v[52:55], v[182:185], v[190:193], v[52:55]
	v_mfma_f32_16x16x32_bf16 v[40:43], v[170:173], v[198:201], v[40:43]
	v_mfma_f32_16x16x32_bf16 v[36:39], v[182:185], v[198:201], v[36:39]
	v_mfma_f32_16x16x32_bf16 v[24:27], v[170:173], v[206:209], v[24:27]
	v_mfma_f32_16x16x32_bf16 v[20:23], v[182:185], v[206:209], v[20:23]
	v_mfma_f32_16x16x32_bf16 v[8:11], v[170:173], v[220:223], v[8:11]
	v_mfma_f32_16x16x32_bf16 v[4:7], v[182:185], v[220:223], v[4:7]
	v_mfma_f32_16x16x32_bf16 v[56:59], v[174:177], v[194:197], v[56:59]
	v_mfma_f32_16x16x32_bf16 v[52:55], v[186:189], v[194:197], v[52:55]
	v_mfma_f32_16x16x32_bf16 v[40:43], v[174:177], v[202:205], v[40:43]
	v_mfma_f32_16x16x32_bf16 v[36:39], v[186:189], v[202:205], v[36:39]
	v_mfma_f32_16x16x32_bf16 v[24:27], v[174:177], v[216:219], v[24:27]
	v_mfma_f32_16x16x32_bf16 v[20:23], v[186:189], v[216:219], v[20:23]
	v_mfma_f32_16x16x32_bf16 v[8:11], v[174:177], v[228:231], v[8:11]
	v_mfma_f32_16x16x32_bf16 v[4:7], v[186:189], v[228:231], v[4:7]
	s_barrier
	s_add_i32 s45, 0, 0x18000
	v_add_u32_e32 v165, s45, v143
	s_add_i32 s49, 0, 0x1c000
	ds_read_b128 v[146:149], v165
	ds_read_b128 v[150:153], v165 offset:1024
	ds_read_b128 v[154:157], v165 offset:2048
	ds_read_b128 v[166:169], v165 offset:3072
	v_add_u32_e32 v165, s49, v143
	ds_read_b128 v[170:173], v165
	ds_read_b128 v[174:177], v165 offset:1024
	ds_read_b128 v[182:185], v165 offset:2048
	ds_read_b128 v[186:189], v165 offset:3072
	s_add_u32 s24, s24, 0x80000
	s_addc_u32 s25, s25, 0
	s_mov_b32 m0, s36
	v_lshl_add_u64 v[234:235], s[24:25], 0, v[136:137]
	ds_read_b128 v[190:193], v145 offset:32768
	ds_read_b128 v[194:197], v145 offset:33792
	ds_read_b128 v[198:201], v145 offset:34816
	ds_read_b128 v[202:205], v145 offset:35840
	ds_read_b128 v[206:209], v145 offset:36864
	ds_read_b128 v[216:219], v145 offset:37888
	ds_read_b128 v[220:223], v145 offset:38912
	ds_read_b128 v[228:231], v145 offset:39936
	global_load_lds_dwordx4 v[234:235], off
	v_lshl_add_u64 v[234:235], s[24:25], 0, v[134:135]
	s_mov_b32 m0, s37
	s_nop 0
	global_load_lds_dwordx4 v[234:235], off
	s_waitcnt vmcnt(8)
	s_waitcnt lgkmcnt(0)
	s_barrier
	s_waitcnt lgkmcnt(0)
	v_mfma_f32_16x16x32_bf16 v[128:131], v[146:149], v[190:193], v[128:131]
	v_mfma_f32_16x16x32_bf16 v[124:127], v[154:157], v[190:193], v[124:127]
	v_mfma_f32_16x16x32_bf16 v[112:115], v[146:149], v[198:201], v[112:115]
	v_mfma_f32_16x16x32_bf16 v[108:111], v[154:157], v[198:201], v[108:111]
	v_mfma_f32_16x16x32_bf16 v[96:99], v[146:149], v[206:209], v[96:99]
	v_mfma_f32_16x16x32_bf16 v[92:95], v[154:157], v[206:209], v[92:95]
	v_mfma_f32_16x16x32_bf16 v[80:83], v[146:149], v[220:223], v[80:83]
	v_mfma_f32_16x16x32_bf16 v[76:79], v[154:157], v[220:223], v[76:79]
	v_mfma_f32_16x16x32_bf16 v[128:131], v[150:153], v[194:197], v[128:131]
	v_mfma_f32_16x16x32_bf16 v[124:127], v[166:169], v[194:197], v[124:127]
	v_mfma_f32_16x16x32_bf16 v[112:115], v[150:153], v[202:205], v[112:115]
	v_mfma_f32_16x16x32_bf16 v[108:111], v[166:169], v[202:205], v[108:111]
	v_mfma_f32_16x16x32_bf16 v[96:99], v[150:153], v[216:219], v[96:99]
	v_mfma_f32_16x16x32_bf16 v[92:95], v[166:169], v[216:219], v[92:95]
	v_mfma_f32_16x16x32_bf16 v[80:83], v[150:153], v[228:231], v[80:83]
	v_mfma_f32_16x16x32_bf16 v[76:79], v[166:169], v[228:231], v[76:79]
	v_mfma_f32_16x16x32_bf16 v[120:123], v[170:173], v[190:193], v[120:123]
	v_mfma_f32_16x16x32_bf16 v[116:119], v[182:185], v[190:193], v[116:119]
	v_mfma_f32_16x16x32_bf16 v[104:107], v[170:173], v[198:201], v[104:107]
	v_mfma_f32_16x16x32_bf16 v[100:103], v[182:185], v[198:201], v[100:103]
	v_mfma_f32_16x16x32_bf16 v[88:91], v[170:173], v[206:209], v[88:91]
	v_mfma_f32_16x16x32_bf16 v[84:87], v[182:185], v[206:209], v[84:87]
	v_mfma_f32_16x16x32_bf16 v[72:75], v[170:173], v[220:223], v[72:75]
	v_mfma_f32_16x16x32_bf16 v[68:71], v[182:185], v[220:223], v[68:71]
	v_mfma_f32_16x16x32_bf16 v[120:123], v[174:177], v[194:197], v[120:123]
	v_mfma_f32_16x16x32_bf16 v[116:119], v[186:189], v[194:197], v[116:119]
	v_mfma_f32_16x16x32_bf16 v[104:107], v[174:177], v[202:205], v[104:107]
	v_mfma_f32_16x16x32_bf16 v[100:103], v[186:189], v[202:205], v[100:103]
	v_mfma_f32_16x16x32_bf16 v[88:91], v[174:177], v[216:219], v[88:91]
	v_mfma_f32_16x16x32_bf16 v[84:87], v[186:189], v[216:219], v[84:87]
	v_mfma_f32_16x16x32_bf16 v[72:75], v[174:177], v[228:231], v[72:75]
	v_mfma_f32_16x16x32_bf16 v[68:71], v[186:189], v[228:231], v[68:71]
	s_barrier
	s_add_i32 s24, s45, s34
	v_lshl_add_u64 v[178:179], v[178:179], 0, s[86:87]
	s_mov_b32 m0, s24
	ds_read_b128 v[190:193], v145 offset:49152
	ds_read_b128 v[194:197], v145 offset:50176
	ds_read_b128 v[198:201], v145 offset:51200
	ds_read_b128 v[202:205], v145 offset:52224
	ds_read_b128 v[206:209], v145 offset:53248
	ds_read_b128 v[216:219], v145 offset:54272
	ds_read_b128 v[220:223], v145 offset:55296
	ds_read_b128 v[228:231], v145 offset:56320
	global_load_lds_dwordx4 v[178:179], off
	s_add_i32 m0, s24, 0x2000
	s_add_u32 s22, s22, 0x80080
	v_lshl_add_u64 v[178:179], v[210:211], 0, s[86:87]
	s_addc_u32 s23, s23, 0
	s_add_i32 s24, s49, s34
	global_load_lds_dwordx4 v[178:179], off
	v_lshl_add_u64 v[178:179], s[22:23], 0, v[2:3]
	s_mov_b32 m0, s24
	s_nop 0
	global_load_lds_dwordx4 v[178:179], off
	v_lshl_add_u64 v[178:179], s[22:23], 0, v[132:133]
	s_add_i32 m0, s24, 0x2000
	s_nop 0
	global_load_lds_dwordx4 v[178:179], off
	v_lshl_add_u64 v[178:179], v[224:225], 0, s[86:87]
	s_mov_b32 m0, s12
	s_nop 0
	global_load_lds_dwordx4 v[178:179], off
	v_lshl_add_u64 v[178:179], v[232:233], 0, s[86:87]
	s_mov_b32 m0, s13
	s_nop 0
	global_load_lds_dwordx4 v[178:179], off
	s_waitcnt vmcnt(8)
	s_waitcnt lgkmcnt(0)
	s_barrier
	s_waitcnt lgkmcnt(0)
	v_mfma_f32_16x16x32_bf16 v[64:67], v[146:149], v[190:193], v[64:67]
	v_mfma_f32_16x16x32_bf16 v[60:63], v[154:157], v[190:193], v[60:63]
	v_mfma_f32_16x16x32_bf16 v[48:51], v[146:149], v[198:201], v[48:51]
	v_mfma_f32_16x16x32_bf16 v[44:47], v[154:157], v[198:201], v[44:47]
	v_mfma_f32_16x16x32_bf16 v[32:35], v[146:149], v[206:209], v[32:35]
	v_mfma_f32_16x16x32_bf16 v[28:31], v[154:157], v[206:209], v[28:31]
	v_mfma_f32_16x16x32_bf16 v[16:19], v[146:149], v[220:223], v[16:19]
	v_mfma_f32_16x16x32_bf16 v[12:15], v[154:157], v[220:223], v[12:15]
	v_mfma_f32_16x16x32_bf16 v[64:67], v[150:153], v[194:197], v[64:67]
	v_mfma_f32_16x16x32_bf16 v[60:63], v[166:169], v[194:197], v[60:63]
	v_mfma_f32_16x16x32_bf16 v[48:51], v[150:153], v[202:205], v[48:51]
	v_mfma_f32_16x16x32_bf16 v[44:47], v[166:169], v[202:205], v[44:47]
	v_mfma_f32_16x16x32_bf16 v[32:35], v[150:153], v[216:219], v[32:35]
	v_mfma_f32_16x16x32_bf16 v[28:31], v[166:169], v[216:219], v[28:31]
	v_mfma_f32_16x16x32_bf16 v[16:19], v[150:153], v[228:231], v[16:19]
	v_mfma_f32_16x16x32_bf16 v[12:15], v[166:169], v[228:231], v[12:15]
	v_mfma_f32_16x16x32_bf16 v[56:59], v[170:173], v[190:193], v[56:59]
	v_mfma_f32_16x16x32_bf16 v[52:55], v[182:185], v[190:193], v[52:55]
	v_mfma_f32_16x16x32_bf16 v[40:43], v[170:173], v[198:201], v[40:43]
	v_mfma_f32_16x16x32_bf16 v[36:39], v[182:185], v[198:201], v[36:39]
	v_mfma_f32_16x16x32_bf16 v[24:27], v[170:173], v[206:209], v[24:27]
	v_mfma_f32_16x16x32_bf16 v[20:23], v[182:185], v[206:209], v[20:23]
	v_mfma_f32_16x16x32_bf16 v[8:11], v[170:173], v[220:223], v[8:11]
	v_mfma_f32_16x16x32_bf16 v[4:7], v[182:185], v[220:223], v[4:7]
	v_mfma_f32_16x16x32_bf16 v[56:59], v[174:177], v[194:197], v[56:59]
	v_mfma_f32_16x16x32_bf16 v[52:55], v[186:189], v[194:197], v[52:55]
	v_mfma_f32_16x16x32_bf16 v[40:43], v[174:177], v[202:205], v[40:43]
	v_mfma_f32_16x16x32_bf16 v[36:39], v[186:189], v[202:205], v[36:39]
	v_mfma_f32_16x16x32_bf16 v[24:27], v[174:177], v[216:219], v[24:27]
	v_mfma_f32_16x16x32_bf16 v[20:23], v[186:189], v[216:219], v[20:23]
	v_mfma_f32_16x16x32_bf16 v[8:11], v[174:177], v[228:231], v[8:11]
	v_mfma_f32_16x16x32_bf16 v[4:7], v[186:189], v[228:231], v[4:7]
	s_barrier
	s_add_i32 s33, s33, 2
	s_add_u32 s0, s0, 0x100
	s_addc_u32 s9, s9, 0
	s_add_u32 s20, s20, 0x100
	s_addc_u32 s21, s21, 0
	s_cmp_gt_u32 s33, 29
	s_cbranch_scc0 .LBB6_2080
	s_and_b64 vcc, exec, s[6:7]
	s_cbranch_vccz .LBB6_2083
	s_barrier

.LBB6_2159:
	s_add_u32 s18, s16, 0x100
	s_addc_u32 s19, s17, 0
	s_add_i32 s45, 0, 0x10000
	s_cmpk_eq_i32 s33, 0x54
	s_cselect_b32 s23, s11, s19
	s_cselect_b32 s22, s10, s18
	s_cselect_b32 s21, s15, s13
	s_cselect_b32 s20, s14, s0
	s_add_i32 s51, 0, 0x14000
	v_add_u32_e32 v150, s45, v166
	v_add_u32_e32 v169, s51, v166
	ds_read_b128 v[132:135], v150
	ds_read_b128 v[136:139], v150 offset:1024
	ds_read_b128 v[140:143], v150 offset:2048
	ds_read_b128 v[150:153], v150 offset:3072
	ds_read_b128 v[154:157], v169
	ds_read_b128 v[170:173], v169 offset:1024
	ds_read_b128 v[174:177], v169 offset:2048
	ds_read_b128 v[182:185], v169 offset:3072
	v_lshl_add_u64 v[178:179], s[16:17], 0, v[148:149]
	s_add_i32 m0, s31, 0xc000
	ds_read_b128 v[186:189], v168
	ds_read_b128 v[190:193], v168 offset:1024
	ds_read_b128 v[194:197], v168 offset:2048
	ds_read_b128 v[198:201], v168 offset:3072
	ds_read_b128 v[202:205], v168 offset:4096
	ds_read_b128 v[206:209], v168 offset:5120
	ds_read_b128 v[216:219], v168 offset:6144
	ds_read_b128 v[220:223], v168 offset:7168
	global_load_lds_dwordx4 v[178:179], off
	v_lshl_add_u64 v[178:179], s[16:17], 0, v[146:147]
	s_add_i32 m0, s31, 0xe000
	s_nop 0
	global_load_lds_dwordx4 v[178:179], off
	s_waitcnt vmcnt(8)
	s_waitcnt lgkmcnt(0)
	s_barrier
	s_waitcnt lgkmcnt(0)
	v_mfma_f32_16x16x32_bf16 v[128:131], v[132:135], v[186:189], v[128:131]
	v_mfma_f32_16x16x32_bf16 v[124:127], v[140:143], v[186:189], v[124:127]
	v_mfma_f32_16x16x32_bf16 v[120:123], v[132:135], v[194:197], v[120:123]
	v_mfma_f32_16x16x32_bf16 v[108:111], v[140:143], v[194:197], v[108:111]
	v_mfma_f32_16x16x32_bf16 v[104:107], v[132:135], v[202:205], v[104:107]
	v_mfma_f32_16x16x32_bf16 v[92:95], v[140:143], v[202:205], v[92:95]
	v_mfma_f32_16x16x32_bf16 v[88:91], v[132:135], v[216:219], v[88:91]
	v_mfma_f32_16x16x32_bf16 v[76:79], v[140:143], v[216:219], v[76:79]
	v_mfma_f32_16x16x32_bf16 v[128:131], v[136:139], v[190:193], v[128:131]
	v_mfma_f32_16x16x32_bf16 v[124:127], v[150:153], v[190:193], v[124:127]
	v_mfma_f32_16x16x32_bf16 v[120:123], v[136:139], v[198:201], v[120:123]
	v_mfma_f32_16x16x32_bf16 v[108:111], v[150:153], v[198:201], v[108:111]
	v_mfma_f32_16x16x32_bf16 v[104:107], v[136:139], v[206:209], v[104:107]
	v_mfma_f32_16x16x32_bf16 v[92:95], v[150:153], v[206:209], v[92:95]
	v_mfma_f32_16x16x32_bf16 v[88:91], v[136:139], v[220:223], v[88:91]
	v_mfma_f32_16x16x32_bf16 v[76:79], v[150:153], v[220:223], v[76:79]
	v_mfma_f32_16x16x32_bf16 v[116:119], v[154:157], v[186:189], v[116:119]
	v_mfma_f32_16x16x32_bf16 v[112:115], v[174:177], v[186:189], v[112:115]
	v_mfma_f32_16x16x32_bf16 v[100:103], v[154:157], v[194:197], v[100:103]
	v_mfma_f32_16x16x32_bf16 v[96:99], v[174:177], v[194:197], v[96:99]
	v_mfma_f32_16x16x32_bf16 v[84:87], v[154:157], v[202:205], v[84:87]
	v_mfma_f32_16x16x32_bf16 v[80:83], v[174:177], v[202:205], v[80:83]
	v_mfma_f32_16x16x32_bf16 v[72:75], v[154:157], v[216:219], v[72:75]
	v_mfma_f32_16x16x32_bf16 v[68:71], v[174:177], v[216:219], v[68:71]
	v_mfma_f32_16x16x32_bf16 v[116:119], v[170:173], v[190:193], v[116:119]
	v_mfma_f32_16x16x32_bf16 v[112:115], v[182:185], v[190:193], v[112:115]
	v_mfma_f32_16x16x32_bf16 v[100:103], v[170:173], v[198:201], v[100:103]
	v_mfma_f32_16x16x32_bf16 v[96:99], v[182:185], v[198:201], v[96:99]
	v_mfma_f32_16x16x32_bf16 v[84:87], v[170:173], v[206:209], v[84:87]
	v_mfma_f32_16x16x32_bf16 v[80:83], v[182:185], v[206:209], v[80:83]
	v_mfma_f32_16x16x32_bf16 v[72:75], v[170:173], v[220:223], v[72:75]
	v_mfma_f32_16x16x32_bf16 v[68:71], v[182:185], v[220:223], v[68:71]
	s_barrier
	s_add_i32 s16, s45, s30
	v_lshl_add_u64 v[178:179], s[20:21], 0, v[2:3]
	s_mov_b32 m0, s16
	ds_read_b128 v[186:189], v168 offset:16384
	ds_read_b128 v[190:193], v168 offset:17408
	ds_read_b128 v[194:197], v168 offset:18432
	ds_read_b128 v[198:201], v168 offset:19456
	ds_read_b128 v[202:205], v168 offset:20480
	ds_read_b128 v[206:209], v168 offset:21504
	ds_read_b128 v[216:219], v168 offset:22528
	ds_read_b128 v[220:223], v168 offset:23552
	global_load_lds_dwordx4 v[178:179], off
	s_add_i32 m0, s16, 0x2000
	s_add_u32 s16, s20, 0x160000
	v_lshl_add_u64 v[210:211], s[20:21], 0, v[144:145]
	s_addc_u32 s17, s21, 0
	s_add_i32 s45, s51, s30
	global_load_lds_dwordx4 v[210:211], off
	v_lshl_add_u64 v[224:225], s[16:17], 0, v[2:3]
	s_mov_b32 m0, s45
	v_lshl_add_u64 v[228:229], s[22:23], 0, v[144:145]
	global_load_lds_dwordx4 v[224:225], off
	v_lshl_add_u64 v[224:225], s[16:17], 0, v[144:145]
	s_add_i32 m0, s45, 0x2000
	s_nop 0
	global_load_lds_dwordx4 v[224:225], off
	v_lshl_add_u64 v[224:225], s[22:23], 0, v[2:3]
	s_mov_b32 m0, s31
	s_nop 0
	global_load_lds_dwordx4 v[224:225], off
	s_mov_b32 m0, s34
	s_nop 0
	global_load_lds_dwordx4 v[228:229], off
	s_waitcnt vmcnt(8)
	s_waitcnt lgkmcnt(0)
	s_barrier
	s_waitcnt lgkmcnt(0)
	v_mfma_f32_16x16x32_bf16 v[64:67], v[132:135], v[186:189], v[64:67]
	v_mfma_f32_16x16x32_bf16 v[60:63], v[140:143], v[186:189], v[60:63]
	v_mfma_f32_16x16x32_bf16 v[56:59], v[132:135], v[194:197], v[56:59]
	v_mfma_f32_16x16x32_bf16 v[44:47], v[140:143], v[194:197], v[44:47]
	v_mfma_f32_16x16x32_bf16 v[40:43], v[132:135], v[202:205], v[40:43]
	v_mfma_f32_16x16x32_bf16 v[28:31], v[140:143], v[202:205], v[28:31]
	v_mfma_f32_16x16x32_bf16 v[24:27], v[132:135], v[216:219], v[24:27]
	v_mfma_f32_16x16x32_bf16 v[12:15], v[140:143], v[216:219], v[12:15]
	v_mfma_f32_16x16x32_bf16 v[64:67], v[136:139], v[190:193], v[64:67]
	v_mfma_f32_16x16x32_bf16 v[60:63], v[150:153], v[190:193], v[60:63]
	v_mfma_f32_16x16x32_bf16 v[56:59], v[136:139], v[198:201], v[56:59]
	v_mfma_f32_16x16x32_bf16 v[44:47], v[150:153], v[198:201], v[44:47]
	v_mfma_f32_16x16x32_bf16 v[40:43], v[136:139], v[206:209], v[40:43]
	v_mfma_f32_16x16x32_bf16 v[28:31], v[150:153], v[206:209], v[28:31]
	v_mfma_f32_16x16x32_bf16 v[24:27], v[136:139], v[220:223], v[24:27]
	v_mfma_f32_16x16x32_bf16 v[12:15], v[150:153], v[220:223], v[12:15]
	v_mfma_f32_16x16x32_bf16 v[52:55], v[154:157], v[186:189], v[52:55]
	v_mfma_f32_16x16x32_bf16 v[48:51], v[174:177], v[186:189], v[48:51]
	v_mfma_f32_16x16x32_bf16 v[36:39], v[154:157], v[194:197], v[36:39]
	v_mfma_f32_16x16x32_bf16 v[32:35], v[174:177], v[194:197], v[32:35]
	v_mfma_f32_16x16x32_bf16 v[20:23], v[154:157], v[202:205], v[20:23]
	v_mfma_f32_16x16x32_bf16 v[16:19], v[174:177], v[202:205], v[16:19]
	v_mfma_f32_16x16x32_bf16 v[8:11], v[154:157], v[216:219], v[8:11]
	v_mfma_f32_16x16x32_bf16 v[4:7], v[174:177], v[216:219], v[4:7]
	v_mfma_f32_16x16x32_bf16 v[52:55], v[170:173], v[190:193], v[52:55]
	v_mfma_f32_16x16x32_bf16 v[48:51], v[182:185], v[190:193], v[48:51]
	v_mfma_f32_16x16x32_bf16 v[36:39], v[170:173], v[198:201], v[36:39]
	v_mfma_f32_16x16x32_bf16 v[32:35], v[182:185], v[198:201], v[32:35]
	v_mfma_f32_16x16x32_bf16 v[20:23], v[170:173], v[206:209], v[20:23]
	v_mfma_f32_16x16x32_bf16 v[16:19], v[182:185], v[206:209], v[16:19]
	v_mfma_f32_16x16x32_bf16 v[8:11], v[170:173], v[220:223], v[8:11]
	v_mfma_f32_16x16x32_bf16 v[4:7], v[182:185], v[220:223], v[4:7]
	s_barrier
	s_add_i32 s45, 0, 0x18000
	s_add_i32 s51, 0, 0x1c000
	v_add_u32_e32 v150, s45, v166
	v_add_u32_e32 v169, s51, v166
	ds_read_b128 v[132:135], v150
	ds_read_b128 v[136:139], v150 offset:1024
	ds_read_b128 v[140:143], v150 offset:2048
	ds_read_b128 v[150:153], v150 offset:3072
	ds_read_b128 v[154:157], v169
	ds_read_b128 v[170:173], v169 offset:1024
	ds_read_b128 v[174:177], v169 offset:2048
	ds_read_b128 v[182:185], v169 offset:3072
	s_add_u32 s16, s22, 0x160000
	s_addc_u32 s17, s23, 0
	s_mov_b32 m0, s35
	v_lshl_add_u64 v[230:231], s[16:17], 0, v[2:3]
	ds_read_b128 v[186:189], v168 offset:32768
	ds_read_b128 v[190:193], v168 offset:33792
	ds_read_b128 v[194:197], v168 offset:34816
	ds_read_b128 v[198:201], v168 offset:35840
	ds_read_b128 v[202:205], v168 offset:36864
	ds_read_b128 v[206:209], v168 offset:37888
	ds_read_b128 v[216:219], v168 offset:38912
	ds_read_b128 v[220:223], v168 offset:39936
	global_load_lds_dwordx4 v[230:231], off
	v_lshl_add_u64 v[230:231], s[16:17], 0, v[144:145]
	s_mov_b32 m0, s36
	s_nop 0
	global_load_lds_dwordx4 v[230:231], off
	s_waitcnt vmcnt(8)
	s_waitcnt lgkmcnt(0)
	s_barrier
	s_waitcnt lgkmcnt(0)
	v_mfma_f32_16x16x32_bf16 v[128:131], v[132:135], v[186:189], v[128:131]
	v_mfma_f32_16x16x32_bf16 v[124:127], v[140:143], v[186:189], v[124:127]
	v_mfma_f32_16x16x32_bf16 v[120:123], v[132:135], v[194:197], v[120:123]
	v_mfma_f32_16x16x32_bf16 v[108:111], v[140:143], v[194:197], v[108:111]
	v_mfma_f32_16x16x32_bf16 v[104:107], v[132:135], v[202:205], v[104:107]
	v_mfma_f32_16x16x32_bf16 v[92:95], v[140:143], v[202:205], v[92:95]
	v_mfma_f32_16x16x32_bf16 v[88:91], v[132:135], v[216:219], v[88:91]
	v_mfma_f32_16x16x32_bf16 v[76:79], v[140:143], v[216:219], v[76:79]
	v_mfma_f32_16x16x32_bf16 v[128:131], v[136:139], v[190:193], v[128:131]
	v_mfma_f32_16x16x32_bf16 v[124:127], v[150:153], v[190:193], v[124:127]
	v_mfma_f32_16x16x32_bf16 v[120:123], v[136:139], v[198:201], v[120:123]
	v_mfma_f32_16x16x32_bf16 v[108:111], v[150:153], v[198:201], v[108:111]
	v_mfma_f32_16x16x32_bf16 v[104:107], v[136:139], v[206:209], v[104:107]
	v_mfma_f32_16x16x32_bf16 v[92:95], v[150:153], v[206:209], v[92:95]
	v_mfma_f32_16x16x32_bf16 v[88:91], v[136:139], v[220:223], v[88:91]
	v_mfma_f32_16x16x32_bf16 v[76:79], v[150:153], v[220:223], v[76:79]
	v_mfma_f32_16x16x32_bf16 v[116:119], v[154:157], v[186:189], v[116:119]
	v_mfma_f32_16x16x32_bf16 v[112:115], v[174:177], v[186:189], v[112:115]
	v_mfma_f32_16x16x32_bf16 v[100:103], v[154:157], v[194:197], v[100:103]
	v_mfma_f32_16x16x32_bf16 v[96:99], v[174:177], v[194:197], v[96:99]
	v_mfma_f32_16x16x32_bf16 v[84:87], v[154:157], v[202:205], v[84:87]
	v_mfma_f32_16x16x32_bf16 v[80:83], v[174:177], v[202:205], v[80:83]
	v_mfma_f32_16x16x32_bf16 v[72:75], v[154:157], v[216:219], v[72:75]
	v_mfma_f32_16x16x32_bf16 v[68:71], v[174:177], v[216:219], v[68:71]
	v_mfma_f32_16x16x32_bf16 v[116:119], v[170:173], v[190:193], v[116:119]
	v_mfma_f32_16x16x32_bf16 v[112:115], v[182:185], v[190:193], v[112:115]
	v_mfma_f32_16x16x32_bf16 v[100:103], v[170:173], v[198:201], v[100:103]
	v_mfma_f32_16x16x32_bf16 v[96:99], v[182:185], v[198:201], v[96:99]
	v_mfma_f32_16x16x32_bf16 v[84:87], v[170:173], v[206:209], v[84:87]
	v_mfma_f32_16x16x32_bf16 v[80:83], v[182:185], v[206:209], v[80:83]
	v_mfma_f32_16x16x32_bf16 v[72:75], v[170:173], v[220:223], v[72:75]
	v_mfma_f32_16x16x32_bf16 v[68:71], v[182:185], v[220:223], v[68:71]
	s_barrier
	s_add_i32 s16, s45, s30
	v_lshl_add_u64 v[178:179], v[178:179], 0, s[86:87]
	s_mov_b32 m0, s16
	ds_read_b128 v[186:189], v168 offset:49152
	ds_read_b128 v[190:193], v168 offset:50176
	ds_read_b128 v[194:197], v168 offset:51200
	ds_read_b128 v[198:201], v168 offset:52224
	ds_read_b128 v[202:205], v168 offset:53248
	ds_read_b128 v[206:209], v168 offset:54272
	ds_read_b128 v[216:219], v168 offset:55296
	ds_read_b128 v[220:223], v168 offset:56320
	global_load_lds_dwordx4 v[178:179], off
	s_add_i32 m0, s16, 0x2000
	s_add_u32 s16, s20, 0x160080
	v_lshl_add_u64 v[178:179], v[210:211], 0, s[86:87]
	s_addc_u32 s17, s21, 0
	s_add_i32 s20, s51, s30
	global_load_lds_dwordx4 v[178:179], off
	v_lshl_add_u64 v[178:179], s[16:17], 0, v[2:3]
	s_mov_b32 m0, s20
	s_nop 0
	global_load_lds_dwordx4 v[178:179], off
	v_lshl_add_u64 v[178:179], s[16:17], 0, v[144:145]
	s_add_i32 m0, s20, 0x2000
	s_nop 0
	global_load_lds_dwordx4 v[178:179], off
	v_lshl_add_u64 v[178:179], v[224:225], 0, s[86:87]
	s_mov_b32 m0, s37
	s_nop 0
	global_load_lds_dwordx4 v[178:179], off
	v_lshl_add_u64 v[178:179], v[228:229], 0, s[86:87]
	s_mov_b32 m0, s47
	s_nop 0
	global_load_lds_dwordx4 v[178:179], off
	s_waitcnt vmcnt(8)
	s_waitcnt lgkmcnt(0)
	s_barrier
	s_waitcnt lgkmcnt(0)
	v_mfma_f32_16x16x32_bf16 v[64:67], v[132:135], v[186:189], v[64:67]
	v_mfma_f32_16x16x32_bf16 v[60:63], v[140:143], v[186:189], v[60:63]
	v_mfma_f32_16x16x32_bf16 v[56:59], v[132:135], v[194:197], v[56:59]
	v_mfma_f32_16x16x32_bf16 v[44:47], v[140:143], v[194:197], v[44:47]
	v_mfma_f32_16x16x32_bf16 v[40:43], v[132:135], v[202:205], v[40:43]
	v_mfma_f32_16x16x32_bf16 v[28:31], v[140:143], v[202:205], v[28:31]
	v_mfma_f32_16x16x32_bf16 v[24:27], v[132:135], v[216:219], v[24:27]
	v_mfma_f32_16x16x32_bf16 v[12:15], v[140:143], v[216:219], v[12:15]
	v_mfma_f32_16x16x32_bf16 v[64:67], v[136:139], v[190:193], v[64:67]
	v_mfma_f32_16x16x32_bf16 v[60:63], v[150:153], v[190:193], v[60:63]
	v_mfma_f32_16x16x32_bf16 v[56:59], v[136:139], v[198:201], v[56:59]
	v_mfma_f32_16x16x32_bf16 v[44:47], v[150:153], v[198:201], v[44:47]
	v_mfma_f32_16x16x32_bf16 v[40:43], v[136:139], v[206:209], v[40:43]
	v_mfma_f32_16x16x32_bf16 v[28:31], v[150:153], v[206:209], v[28:31]
	v_mfma_f32_16x16x32_bf16 v[24:27], v[136:139], v[220:223], v[24:27]
	v_mfma_f32_16x16x32_bf16 v[12:15], v[150:153], v[220:223], v[12:15]
	v_mfma_f32_16x16x32_bf16 v[52:55], v[154:157], v[186:189], v[52:55]
	v_mfma_f32_16x16x32_bf16 v[48:51], v[174:177], v[186:189], v[48:51]
	v_mfma_f32_16x16x32_bf16 v[36:39], v[154:157], v[194:197], v[36:39]
	v_mfma_f32_16x16x32_bf16 v[32:35], v[174:177], v[194:197], v[32:35]
	v_mfma_f32_16x16x32_bf16 v[20:23], v[154:157], v[202:205], v[20:23]
	v_mfma_f32_16x16x32_bf16 v[16:19], v[174:177], v[202:205], v[16:19]
	v_mfma_f32_16x16x32_bf16 v[8:11], v[154:157], v[216:219], v[8:11]
	v_mfma_f32_16x16x32_bf16 v[4:7], v[174:177], v[216:219], v[4:7]
	v_mfma_f32_16x16x32_bf16 v[52:55], v[170:173], v[190:193], v[52:55]
	v_mfma_f32_16x16x32_bf16 v[48:51], v[182:185], v[190:193], v[48:51]
	v_mfma_f32_16x16x32_bf16 v[36:39], v[170:173], v[198:201], v[36:39]
	v_mfma_f32_16x16x32_bf16 v[32:35], v[182:185], v[198:201], v[32:35]
	v_mfma_f32_16x16x32_bf16 v[20:23], v[170:173], v[206:209], v[20:23]
	v_mfma_f32_16x16x32_bf16 v[16:19], v[182:185], v[206:209], v[16:19]
	v_mfma_f32_16x16x32_bf16 v[8:11], v[170:173], v[220:223], v[8:11]
	v_mfma_f32_16x16x32_bf16 v[4:7], v[182:185], v[220:223], v[4:7]
	s_barrier
	s_add_i32 s33, s33, 2
	s_add_u32 s0, s0, 0x100
	s_addc_u32 s13, s13, 0
	s_cmpk_gt_u32 s33, 0x55
	s_mov_b64 s[16:17], s[18:19]
	s_cbranch_scc0 .LBB6_2159
	s_and_b64 vcc, exec, s[6:7]
	s_cbranch_vccz .LBB6_2162
	s_barrier
